# pooling fast path also for the chunk that starts a sequence (constant correctly rounded 1/n, no window subtraction before token W)
# speedup vs baseline: 1.0191x; 1.0053x over previous
; template <int W>
; __device__ __forceinline__ void pool_item(const bf16* U, bf16* Z, int b, int t0, int g, int lane) {
;     const size_t base = (size_t)b * SEQ * D + 256 * g + 4 * lane;
; __global__ void __launch_bounds__(NWAVES * 64, 2) mk_fwd(Args args) {
;     ...
;                   for (int i = 0; S.next(i, pu); ++i) {
;                       const int b = pu.pm >> 3, t0 = (pu.pm & 7) * 256 + 32 * F.wave, g = pu.pn;
;                       if (g == 0) pool_item<2>(U, Z, b, t0, 0, F.lane); else if (g == 1) pool_item<4>(U, Z, b, t0, 1, F.lane);
;                       else if (g == 2) pool_item<8>(U, Z, b, t0, 2, F.lane); else pool_item<16>(U, Z, b, t0, 3, F.lane); }
.LBB0_869:
	s_nop 0
	v_writelane_b32 v255, s8, 3
	s_mov_b64 s[46:47], -1
	s_and_b64 vcc, exec, s[40:41]
	s_cbranch_vccz .LBB0_862
	v_readlane_b32 s8, v255, 4
	s_ashr_i32 s48, s8, 3
	s_lshl_b32 s8, s8, 8
	s_and_b32 s8, s8, 0x700
	s_ashr_i32 s49, s48, 31
	s_add_i32 s46, s8, s5
	s_lshl_b64 s[50:51], s[48:49], 21
	s_cmp_gt_i32 s46, 0
	v_readlane_b32 s9, v255, 3
	s_cselect_b64 s[40:41], -1, 0
	s_mov_b64 s[56:57], -1
	s_mov_b64 s[52:53], 0
	s_lshl_b64 s[10:11], s[50:51], 1
	s_add_u32 s10, s10, s44
	s_addc_u32 s11, s11, s45
	s_add_i32 s22, s46, -16
	s_lshl_b32 s28, s22, 11
	s_ashr_i32 s29, s28, 31
	s_add_u32 s10, s10, s28
	s_addc_u32 s11, s11, s29
	s_add_u32 s28, s10, 0x2008000
	s_addc_u32 s29, s11, 0
	s_lshl_b32 s22, s9, 9
	v_lshl_add_u32 v190, v4, 1, s22
	s_cmp_lt_i32 s46, 16
	s_cbranch_scc1 .Lpool_first
	s_cmp_eq_u32 s9, 0
	s_cbranch_scc1 .Lpool_w2
	s_cmp_eq_u32 s9, 1
	s_cbranch_scc1 .Lpool_w4
	s_cmp_eq_u32 s9, 2
	s_cbranch_scc1 .Lpool_w8

; #define GAS __attribute__((address_space(1)))
; __device__ __forceinline__ unsigned pk2(float lo, float hi) { const f32x2 v = {lo, hi}; return __builtin_bit_cast(unsigned, __builtin_convertvector(v, b16x2)); }
; template <int W>
; __device__ __forceinline__ void pool_item(const bf16* U, bf16* Z, int b, int t0, int g, int lane) {
;     const size_t base = (size_t)b * SEQ * D + 256 * g + 4 * lane;
;     float s[4] = {0.f, 0.f, 0.f, 0.f};
; #pragma unroll
;     for (int j = 1; j <= W; ++j) { const int t = t0 - j; if (t >= 0) { const u32x2 v = *(const GAS u32x2*)(U + base + (size_t)t * D);
;             s[0] += bf2f(v.x & 0xffffu); s[1] += bf2f(v.x >> 16); s[2] += bf2f(v.y & 0xffffu); s[3] += bf2f(v.y >> 16); } }
; #pragma unroll 8
;     for (int i = 0; i < 32; ++i) { const int t = t0 + i;
;         const u32x2 v = *(const GAS u32x2*)(U + base + (size_t)t * D);
;         const float c0 = bf2f(v.x & 0xffffu), c1 = bf2f(v.x >> 16), c2 = bf2f(v.y & 0xffffu), c3 = bf2f(v.y >> 16);
;         s[0] += c0; s[1] += c1; s[2] += c2; s[3] += c3;
;         if (t - W >= 0) { const u32x2 o = *(const GAS u32x2*)(U + base + (size_t)(t - W) * D);
;             s[0] -= bf2f(o.x & 0xffffu); s[1] -= bf2f(o.x >> 16); s[2] -= bf2f(o.y & 0xffffu); s[3] -= bf2f(o.y >> 16); }
;         const float inv = 1.0f / (float)((t + 1) < W ? (t + 1) : W);
;         u32x2 w; w.x = pk2(s[0] * inv - c0, s[1] * inv - c1); w.y = pk2(s[2] * inv - c2, s[3] * inv - c3);
;         *(GAS u32x2*)(Z + base + (size_t)t * D) = w; }
.Lpool_first:
	s_cmp_eq_u32 s9, 0
	s_cbranch_scc1 .Lpool0_w2
	s_cmp_eq_u32 s9, 1
	s_cbranch_scc1 .Lpool0_w4
	s_cmp_eq_u32 s9, 2
	s_cbranch_scc1 .Lpool0_w8
.Lpool0_w16:
	v_add_u32_e32 v192, 0x8000, v190
	global_load_dwordx2 v[100:101], v192, s[10:11]
	global_load_dwordx2 v[102:103], v192, s[10:11] offset:2048
	v_add_u32_e32 v191, 0x9000, v190
	global_load_dwordx2 v[104:105], v191, s[10:11]
	global_load_dwordx2 v[106:107], v191, s[10:11] offset:2048
	v_add_u32_e32 v192, 0xa000, v190
	global_load_dwordx2 v[108:109], v192, s[10:11]
	global_load_dwordx2 v[110:111], v192, s[10:11] offset:2048
	v_add_u32_e32 v191, 0xb000, v190
	global_load_dwordx2 v[112:113], v191, s[10:11]
	global_load_dwordx2 v[114:115], v191, s[10:11] offset:2048
	v_add_u32_e32 v192, 0xc000, v190
	global_load_dwordx2 v[116:117], v192, s[10:11]
	global_load_dwordx2 v[118:119], v192, s[10:11] offset:2048
	v_add_u32_e32 v191, 0xd000, v190
	global_load_dwordx2 v[120:121], v191, s[10:11]
	global_load_dwordx2 v[122:123], v191, s[10:11] offset:2048
	v_add_u32_e32 v192, 0xe000, v190
	global_load_dwordx2 v[124:125], v192, s[10:11]
	global_load_dwordx2 v[126:127], v192, s[10:11] offset:2048
	v_add_u32_e32 v191, 0xf000, v190
	global_load_dwordx2 v[128:129], v191, s[10:11]
	global_load_dwordx2 v[130:131], v191, s[10:11] offset:2048
	v_add_u32_e32 v192, 0x10000, v190
	global_load_dwordx2 v[132:133], v192, s[10:11]
	global_load_dwordx2 v[134:135], v192, s[10:11] offset:2048
	v_add_u32_e32 v191, 0x11000, v190
	global_load_dwordx2 v[136:137], v191, s[10:11]
	global_load_dwordx2 v[138:139], v191, s[10:11] offset:2048
	v_add_u32_e32 v192, 0x12000, v190
	global_load_dwordx2 v[140:141], v192, s[10:11]
	global_load_dwordx2 v[142:143], v192, s[10:11] offset:2048
	v_add_u32_e32 v191, 0x13000, v190
	global_load_dwordx2 v[144:145], v191, s[10:11]
	global_load_dwordx2 v[146:147], v191, s[10:11] offset:2048
	v_add_u32_e32 v192, 0x14000, v190
	global_load_dwordx2 v[148:149], v192, s[10:11]
	global_load_dwordx2 v[150:151], v192, s[10:11] offset:2048
	v_add_u32_e32 v191, 0x15000, v190
	global_load_dwordx2 v[152:153], v191, s[10:11]
	global_load_dwordx2 v[154:155], v191, s[10:11] offset:2048
	v_add_u32_e32 v192, 0x16000, v190
	global_load_dwordx2 v[156:157], v192, s[10:11]
	global_load_dwordx2 v[158:159], v192, s[10:11] offset:2048
	v_add_u32_e32 v191, 0x17000, v190
	global_load_dwordx2 v[160:161], v191, s[10:11]
	global_load_dwordx2 v[162:163], v191, s[10:11] offset:2048
	v_mov_b32_e32 v184, 0
	v_mov_b32_e32 v185, 0
	v_mov_b32_e32 v186, 0
	v_mov_b32_e32 v187, 0
	v_mov_b32_e32 v188, 0x3f800000
	s_waitcnt vmcnt(31)
	v_lshlrev_b32_e32 v164, 16, v100
	v_and_b32_e32 v165, 0xffff0000, v100
	v_lshlrev_b32_e32 v166, 16, v101
	v_and_b32_e32 v167, 0xffff0000, v101
	v_pk_add_f32 v[184:185], v[184:185], v[164:165]
	v_pk_add_f32 v[186:187], v[186:187], v[166:167]
	v_pk_fma_f32 v[172:173], v[188:189], v[184:185], v[164:165] op_sel_hi:[0,1,1] neg_lo:[0,0,1] neg_hi:[0,0,1]
	v_pk_fma_f32 v[174:175], v[188:189], v[186:187], v[166:167] op_sel_hi:[0,1,1] neg_lo:[0,0,1] neg_hi:[0,0,1]
	v_cvt_pk_bf16_f32 v176, v172, v173
	v_cvt_pk_bf16_f32 v177, v174, v175
	global_store_dwordx2 v190, v[176:177], s[28:29]
	v_mov_b32_e32 v188, 0x3f000000
	s_waitcnt vmcnt(31)
	v_lshlrev_b32_e32 v164, 16, v102
	v_and_b32_e32 v165, 0xffff0000, v102
	v_lshlrev_b32_e32 v166, 16, v103
	v_and_b32_e32 v167, 0xffff0000, v103
	v_pk_add_f32 v[184:185], v[184:185], v[164:165]
	v_pk_add_f32 v[186:187], v[186:187], v[166:167]
	v_pk_fma_f32 v[172:173], v[188:189], v[184:185], v[164:165] op_sel_hi:[0,1,1] neg_lo:[0,0,1] neg_hi:[0,0,1]
	v_pk_fma_f32 v[174:175], v[188:189], v[186:187], v[166:167] op_sel_hi:[0,1,1] neg_lo:[0,0,1] neg_hi:[0,0,1]
	v_cvt_pk_bf16_f32 v178, v172, v173
	v_cvt_pk_bf16_f32 v179, v174, v175
	global_store_dwordx2 v190, v[178:179], s[28:29] offset:2048
	v_mov_b32_e32 v188, 0x3eaaaaab
	s_waitcnt vmcnt(31)
	v_lshlrev_b32_e32 v164, 16, v104
	v_and_b32_e32 v165, 0xffff0000, v104
	v_lshlrev_b32_e32 v166, 16, v105
	v_and_b32_e32 v167, 0xffff0000, v105
	v_pk_add_f32 v[184:185], v[184:185], v[164:165]
	v_pk_add_f32 v[186:187], v[186:187], v[166:167]
	v_pk_fma_f32 v[172:173], v[188:189], v[184:185], v[164:165] op_sel_hi:[0,1,1] neg_lo:[0,0,1] neg_hi:[0,0,1]
	v_pk_fma_f32 v[174:175], v[188:189], v[186:187], v[166:167] op_sel_hi:[0,1,1] neg_lo:[0,0,1] neg_hi:[0,0,1]
	v_cvt_pk_bf16_f32 v180, v172, v173
	v_cvt_pk_bf16_f32 v181, v174, v175
	v_add_u32_e32 v194, 0x1000, v190
	global_store_dwordx2 v194, v[180:181], s[28:29]
	v_mov_b32_e32 v188, 0x3e800000
	s_waitcnt vmcnt(31)
	v_lshlrev_b32_e32 v164, 16, v106
	v_and_b32_e32 v165, 0xffff0000, v106
	v_lshlrev_b32_e32 v166, 16, v107
	v_and_b32_e32 v167, 0xffff0000, v107
	v_pk_add_f32 v[184:185], v[184:185], v[164:165]
	v_pk_add_f32 v[186:187], v[186:187], v[166:167]
	v_pk_fma_f32 v[172:173], v[188:189], v[184:185], v[164:165] op_sel_hi:[0,1,1] neg_lo:[0,0,1] neg_hi:[0,0,1]
	v_pk_fma_f32 v[174:175], v[188:189], v[186:187], v[166:167] op_sel_hi:[0,1,1] neg_lo:[0,0,1] neg_hi:[0,0,1]
	v_cvt_pk_bf16_f32 v182, v172, v173
	v_cvt_pk_bf16_f32 v183, v174, v175
	global_store_dwordx2 v194, v[182:183], s[28:29] offset:2048
	v_mov_b32_e32 v188, 0x3e4ccccd
	s_waitcnt vmcnt(31)
	v_lshlrev_b32_e32 v164, 16, v108
	v_and_b32_e32 v165, 0xffff0000, v108
	v_lshlrev_b32_e32 v166, 16, v109
	v_and_b32_e32 v167, 0xffff0000, v109
	v_pk_add_f32 v[184:185], v[184:185], v[164:165]
	v_pk_add_f32 v[186:187], v[186:187], v[166:167]
	v_pk_fma_f32 v[172:173], v[188:189], v[184:185], v[164:165] op_sel_hi:[0,1,1] neg_lo:[0,0,1] neg_hi:[0,0,1]
	v_pk_fma_f32 v[174:175], v[188:189], v[186:187], v[166:167] op_sel_hi:[0,1,1] neg_lo:[0,0,1] neg_hi:[0,0,1]
	v_cvt_pk_bf16_f32 v176, v172, v173
	v_cvt_pk_bf16_f32 v177, v174, v175
	v_add_u32_e32 v193, 0x2000, v190
	global_store_dwordx2 v193, v[176:177], s[28:29]
	v_mov_b32_e32 v188, 0x3e2aaaab
	s_waitcnt vmcnt(31)
; #define GAS __attribute__((address_space(1)))
; __device__ __forceinline__ unsigned pk2(float lo, float hi) { const f32x2 v = {lo, hi}; return __builtin_bit_cast(unsigned, __builtin_convertvector(v, b16x2)); }
; template <int W>
; __device__ __forceinline__ void pool_item(const bf16* U, bf16* Z, int b, int t0, int g, int lane) {
;     ...
; #pragma unroll 8
;     for (int i = 0; i < 32; ++i) { const int t = t0 + i;
;         const u32x2 v = *(const GAS u32x2*)(U + base + (size_t)t * D);
;         const float c0 = bf2f(v.x & 0xffffu), c1 = bf2f(v.x >> 16), c2 = bf2f(v.y & 0xffffu), c3 = bf2f(v.y >> 16);
;         s[0] += c0; s[1] += c1; s[2] += c2; s[3] += c3;
;         if (t - W >= 0) { const u32x2 o = *(const GAS u32x2*)(U + base + (size_t)(t - W) * D);
;             s[0] -= bf2f(o.x & 0xffffu); s[1] -= bf2f(o.x >> 16); s[2] -= bf2f(o.y & 0xffffu); s[3] -= bf2f(o.y >> 16); }
;         const float inv = 1.0f / (float)((t + 1) < W ? (t + 1) : W);
;         u32x2 w; w.x = pk2(s[0] * inv - c0, s[1] * inv - c1); w.y = pk2(s[2] * inv - c2, s[3] * inv - c3);
;         *(GAS u32x2*)(Z + base + (size_t)t * D) = w; }
	v_lshlrev_b32_e32 v164, 16, v110
	v_and_b32_e32 v165, 0xffff0000, v110
	v_lshlrev_b32_e32 v166, 16, v111
	v_and_b32_e32 v167, 0xffff0000, v111
	v_pk_add_f32 v[184:185], v[184:185], v[164:165]
	v_pk_add_f32 v[186:187], v[186:187], v[166:167]
	v_pk_fma_f32 v[172:173], v[188:189], v[184:185], v[164:165] op_sel_hi:[0,1,1] neg_lo:[0,0,1] neg_hi:[0,0,1]
	v_pk_fma_f32 v[174:175], v[188:189], v[186:187], v[166:167] op_sel_hi:[0,1,1] neg_lo:[0,0,1] neg_hi:[0,0,1]
	v_cvt_pk_bf16_f32 v178, v172, v173
	v_cvt_pk_bf16_f32 v179, v174, v175
	global_store_dwordx2 v193, v[178:179], s[28:29] offset:2048
	v_mov_b32_e32 v188, 0x3e124925
	s_waitcnt vmcnt(31)
	v_lshlrev_b32_e32 v164, 16, v112
	v_and_b32_e32 v165, 0xffff0000, v112
	v_lshlrev_b32_e32 v166, 16, v113
	v_and_b32_e32 v167, 0xffff0000, v113
	v_pk_add_f32 v[184:185], v[184:185], v[164:165]
	v_pk_add_f32 v[186:187], v[186:187], v[166:167]
	v_pk_fma_f32 v[172:173], v[188:189], v[184:185], v[164:165] op_sel_hi:[0,1,1] neg_lo:[0,0,1] neg_hi:[0,0,1]
	v_pk_fma_f32 v[174:175], v[188:189], v[186:187], v[166:167] op_sel_hi:[0,1,1] neg_lo:[0,0,1] neg_hi:[0,0,1]
	v_cvt_pk_bf16_f32 v180, v172, v173
	v_cvt_pk_bf16_f32 v181, v174, v175
	v_add_u32_e32 v194, 0x3000, v190
	global_store_dwordx2 v194, v[180:181], s[28:29]
	v_mov_b32_e32 v188, 0x3e000000
	s_waitcnt vmcnt(31)
	v_lshlrev_b32_e32 v164, 16, v114
	v_and_b32_e32 v165, 0xffff0000, v114
	v_lshlrev_b32_e32 v166, 16, v115
	v_and_b32_e32 v167, 0xffff0000, v115
	v_pk_add_f32 v[184:185], v[184:185], v[164:165]
	v_pk_add_f32 v[186:187], v[186:187], v[166:167]
	v_pk_fma_f32 v[172:173], v[188:189], v[184:185], v[164:165] op_sel_hi:[0,1,1] neg_lo:[0,0,1] neg_hi:[0,0,1]
	v_pk_fma_f32 v[174:175], v[188:189], v[186:187], v[166:167] op_sel_hi:[0,1,1] neg_lo:[0,0,1] neg_hi:[0,0,1]
	v_cvt_pk_bf16_f32 v182, v172, v173
	v_cvt_pk_bf16_f32 v183, v174, v175
	global_store_dwordx2 v194, v[182:183], s[28:29] offset:2048
	v_mov_b32_e32 v188, 0x3de38e39
	s_waitcnt vmcnt(31)
	v_lshlrev_b32_e32 v164, 16, v116
	v_and_b32_e32 v165, 0xffff0000, v116
	v_lshlrev_b32_e32 v166, 16, v117
	v_and_b32_e32 v167, 0xffff0000, v117
	v_pk_add_f32 v[184:185], v[184:185], v[164:165]
	v_pk_add_f32 v[186:187], v[186:187], v[166:167]
	v_pk_fma_f32 v[172:173], v[188:189], v[184:185], v[164:165] op_sel_hi:[0,1,1] neg_lo:[0,0,1] neg_hi:[0,0,1]
	v_pk_fma_f32 v[174:175], v[188:189], v[186:187], v[166:167] op_sel_hi:[0,1,1] neg_lo:[0,0,1] neg_hi:[0,0,1]
	v_cvt_pk_bf16_f32 v176, v172, v173
	v_cvt_pk_bf16_f32 v177, v174, v175
	v_add_u32_e32 v193, 0x4000, v190
	global_store_dwordx2 v193, v[176:177], s[28:29]
	v_mov_b32_e32 v188, 0x3dcccccd
	s_waitcnt vmcnt(31)
	v_lshlrev_b32_e32 v164, 16, v118
	v_and_b32_e32 v165, 0xffff0000, v118
	v_lshlrev_b32_e32 v166, 16, v119
	v_and_b32_e32 v167, 0xffff0000, v119
	v_pk_add_f32 v[184:185], v[184:185], v[164:165]
	v_pk_add_f32 v[186:187], v[186:187], v[166:167]
	v_pk_fma_f32 v[172:173], v[188:189], v[184:185], v[164:165] op_sel_hi:[0,1,1] neg_lo:[0,0,1] neg_hi:[0,0,1]
	v_pk_fma_f32 v[174:175], v[188:189], v[186:187], v[166:167] op_sel_hi:[0,1,1] neg_lo:[0,0,1] neg_hi:[0,0,1]
	v_cvt_pk_bf16_f32 v178, v172, v173
	v_cvt_pk_bf16_f32 v179, v174, v175
	global_store_dwordx2 v193, v[178:179], s[28:29] offset:2048
	v_mov_b32_e32 v188, 0x3dba2e8c
	s_waitcnt vmcnt(31)
	v_lshlrev_b32_e32 v164, 16, v120
	v_and_b32_e32 v165, 0xffff0000, v120
	v_lshlrev_b32_e32 v166, 16, v121
	v_and_b32_e32 v167, 0xffff0000, v121
	v_pk_add_f32 v[184:185], v[184:185], v[164:165]
	v_pk_add_f32 v[186:187], v[186:187], v[166:167]
	v_pk_fma_f32 v[172:173], v[188:189], v[184:185], v[164:165] op_sel_hi:[0,1,1] neg_lo:[0,0,1] neg_hi:[0,0,1]
	v_pk_fma_f32 v[174:175], v[188:189], v[186:187], v[166:167] op_sel_hi:[0,1,1] neg_lo:[0,0,1] neg_hi:[0,0,1]
	v_cvt_pk_bf16_f32 v180, v172, v173
	v_cvt_pk_bf16_f32 v181, v174, v175
	v_add_u32_e32 v194, 0x5000, v190
	global_store_dwordx2 v194, v[180:181], s[28:29]
	v_mov_b32_e32 v188, 0x3daaaaab
	s_waitcnt vmcnt(31)
	v_lshlrev_b32_e32 v164, 16, v122
	v_and_b32_e32 v165, 0xffff0000, v122
	v_lshlrev_b32_e32 v166, 16, v123
	v_and_b32_e32 v167, 0xffff0000, v123
	v_pk_add_f32 v[184:185], v[184:185], v[164:165]
	v_pk_add_f32 v[186:187], v[186:187], v[166:167]
	v_pk_fma_f32 v[172:173], v[188:189], v[184:185], v[164:165] op_sel_hi:[0,1,1] neg_lo:[0,0,1] neg_hi:[0,0,1]
	v_pk_fma_f32 v[174:175], v[188:189], v[186:187], v[166:167] op_sel_hi:[0,1,1] neg_lo:[0,0,1] neg_hi:[0,0,1]
	v_cvt_pk_bf16_f32 v182, v172, v173
	v_cvt_pk_bf16_f32 v183, v174, v175
	global_store_dwordx2 v194, v[182:183], s[28:29] offset:2048
	v_mov_b32_e32 v188, 0x3d9d89d9
	s_waitcnt vmcnt(31)
	v_lshlrev_b32_e32 v164, 16, v124
	v_and_b32_e32 v165, 0xffff0000, v124
	v_lshlrev_b32_e32 v166, 16, v125
	v_and_b32_e32 v167, 0xffff0000, v125
	v_pk_add_f32 v[184:185], v[184:185], v[164:165]
	v_pk_add_f32 v[186:187], v[186:187], v[166:167]
	v_pk_fma_f32 v[172:173], v[188:189], v[184:185], v[164:165] op_sel_hi:[0,1,1] neg_lo:[0,0,1] neg_hi:[0,0,1]
	v_pk_fma_f32 v[174:175], v[188:189], v[186:187], v[166:167] op_sel_hi:[0,1,1] neg_lo:[0,0,1] neg_hi:[0,0,1]
	v_cvt_pk_bf16_f32 v176, v172, v173
	v_cvt_pk_bf16_f32 v177, v174, v175
	v_add_u32_e32 v193, 0x6000, v190
	global_store_dwordx2 v193, v[176:177], s[28:29]
	v_mov_b32_e32 v188, 0x3d924925
	s_waitcnt vmcnt(31)
	v_lshlrev_b32_e32 v164, 16, v126
	v_and_b32_e32 v165, 0xffff0000, v126
	v_lshlrev_b32_e32 v166, 16, v127
	v_and_b32_e32 v167, 0xffff0000, v127
	v_pk_add_f32 v[184:185], v[184:185], v[164:165]
	v_pk_add_f32 v[186:187], v[186:187], v[166:167]
	v_pk_fma_f32 v[172:173], v[188:189], v[184:185], v[164:165] op_sel_hi:[0,1,1] neg_lo:[0,0,1] neg_hi:[0,0,1]
	v_pk_fma_f32 v[174:175], v[188:189], v[186:187], v[166:167] op_sel_hi:[0,1,1] neg_lo:[0,0,1] neg_hi:[0,0,1]
	v_cvt_pk_bf16_f32 v178, v172, v173
	v_cvt_pk_bf16_f32 v179, v174, v175
	global_store_dwordx2 v193, v[178:179], s[28:29] offset:2048
	v_mov_b32_e32 v188, 0x3d888889
	s_waitcnt vmcnt(31)
; #define GAS __attribute__((address_space(1)))
; __device__ __forceinline__ unsigned pk2(float lo, float hi) { const f32x2 v = {lo, hi}; return __builtin_bit_cast(unsigned, __builtin_convertvector(v, b16x2)); }
; template <int W>
; __device__ __forceinline__ void pool_item(const bf16* U, bf16* Z, int b, int t0, int g, int lane) {
;     ...
; #pragma unroll 8
;     for (int i = 0; i < 32; ++i) { const int t = t0 + i;
;         const u32x2 v = *(const GAS u32x2*)(U + base + (size_t)t * D);
;         const float c0 = bf2f(v.x & 0xffffu), c1 = bf2f(v.x >> 16), c2 = bf2f(v.y & 0xffffu), c3 = bf2f(v.y >> 16);
;         s[0] += c0; s[1] += c1; s[2] += c2; s[3] += c3;
;         if (t - W >= 0) { const u32x2 o = *(const GAS u32x2*)(U + base + (size_t)(t - W) * D);
;             s[0] -= bf2f(o.x & 0xffffu); s[1] -= bf2f(o.x >> 16); s[2] -= bf2f(o.y & 0xffffu); s[3] -= bf2f(o.y >> 16); }
;         const float inv = 1.0f / (float)((t + 1) < W ? (t + 1) : W);
;         u32x2 w; w.x = pk2(s[0] * inv - c0, s[1] * inv - c1); w.y = pk2(s[2] * inv - c2, s[3] * inv - c3);
;         *(GAS u32x2*)(Z + base + (size_t)t * D) = w; }
	v_lshlrev_b32_e32 v164, 16, v128
	v_and_b32_e32 v165, 0xffff0000, v128
	v_lshlrev_b32_e32 v166, 16, v129
	v_and_b32_e32 v167, 0xffff0000, v129
	v_pk_add_f32 v[184:185], v[184:185], v[164:165]
	v_pk_add_f32 v[186:187], v[186:187], v[166:167]
	v_pk_fma_f32 v[172:173], v[188:189], v[184:185], v[164:165] op_sel_hi:[0,1,1] neg_lo:[0,0,1] neg_hi:[0,0,1]
	v_pk_fma_f32 v[174:175], v[188:189], v[186:187], v[166:167] op_sel_hi:[0,1,1] neg_lo:[0,0,1] neg_hi:[0,0,1]
	v_cvt_pk_bf16_f32 v180, v172, v173
	v_cvt_pk_bf16_f32 v181, v174, v175
	v_add_u32_e32 v194, 0x7000, v190
	global_store_dwordx2 v194, v[180:181], s[28:29]
	v_mov_b32_e32 v188, 0x3d800000
	s_waitcnt vmcnt(31)
	v_lshlrev_b32_e32 v164, 16, v130
	v_and_b32_e32 v165, 0xffff0000, v130
	v_lshlrev_b32_e32 v166, 16, v131
	v_and_b32_e32 v167, 0xffff0000, v131
	v_pk_add_f32 v[184:185], v[184:185], v[164:165]
	v_pk_add_f32 v[186:187], v[186:187], v[166:167]
	v_pk_fma_f32 v[172:173], v[188:189], v[184:185], v[164:165] op_sel_hi:[0,1,1] neg_lo:[0,0,1] neg_hi:[0,0,1]
	v_pk_fma_f32 v[174:175], v[188:189], v[186:187], v[166:167] op_sel_hi:[0,1,1] neg_lo:[0,0,1] neg_hi:[0,0,1]
	v_cvt_pk_bf16_f32 v182, v172, v173
	v_cvt_pk_bf16_f32 v183, v174, v175
	global_store_dwordx2 v194, v[182:183], s[28:29] offset:2048
	s_waitcnt vmcnt(31)
	v_lshlrev_b32_e32 v164, 16, v132
	v_and_b32_e32 v165, 0xffff0000, v132
	v_lshlrev_b32_e32 v166, 16, v133
	v_and_b32_e32 v167, 0xffff0000, v133
	v_pk_add_f32 v[184:185], v[184:185], v[164:165]
	v_pk_add_f32 v[186:187], v[186:187], v[166:167]
	v_lshlrev_b32_e32 v168, 16, v100
	v_and_b32_e32 v169, 0xffff0000, v100
	v_lshlrev_b32_e32 v170, 16, v101
	v_and_b32_e32 v171, 0xffff0000, v101
	v_pk_add_f32 v[184:185], v[184:185], v[168:169] neg_lo:[0,1] neg_hi:[0,1]
	v_pk_add_f32 v[186:187], v[186:187], v[170:171] neg_lo:[0,1] neg_hi:[0,1]
	v_pk_fma_f32 v[172:173], v[188:189], v[184:185], v[164:165] op_sel_hi:[0,1,1] neg_lo:[0,0,1] neg_hi:[0,0,1]
	v_pk_fma_f32 v[174:175], v[188:189], v[186:187], v[166:167] op_sel_hi:[0,1,1] neg_lo:[0,0,1] neg_hi:[0,0,1]
	v_cvt_pk_bf16_f32 v176, v172, v173
	v_cvt_pk_bf16_f32 v177, v174, v175
	v_add_u32_e32 v193, 0x8000, v190
	global_store_dwordx2 v193, v[176:177], s[28:29]
	s_waitcnt vmcnt(31)
	v_lshlrev_b32_e32 v164, 16, v134
	v_and_b32_e32 v165, 0xffff0000, v134
	v_lshlrev_b32_e32 v166, 16, v135
	v_and_b32_e32 v167, 0xffff0000, v135
	v_pk_add_f32 v[184:185], v[184:185], v[164:165]
	v_pk_add_f32 v[186:187], v[186:187], v[166:167]
	v_lshlrev_b32_e32 v168, 16, v102
	v_and_b32_e32 v169, 0xffff0000, v102
	v_lshlrev_b32_e32 v170, 16, v103
	v_and_b32_e32 v171, 0xffff0000, v103
	v_pk_add_f32 v[184:185], v[184:185], v[168:169] neg_lo:[0,1] neg_hi:[0,1]
	v_pk_add_f32 v[186:187], v[186:187], v[170:171] neg_lo:[0,1] neg_hi:[0,1]
	v_pk_fma_f32 v[172:173], v[188:189], v[184:185], v[164:165] op_sel_hi:[0,1,1] neg_lo:[0,0,1] neg_hi:[0,0,1]
	v_pk_fma_f32 v[174:175], v[188:189], v[186:187], v[166:167] op_sel_hi:[0,1,1] neg_lo:[0,0,1] neg_hi:[0,0,1]
	v_cvt_pk_bf16_f32 v178, v172, v173
	v_cvt_pk_bf16_f32 v179, v174, v175
	global_store_dwordx2 v193, v[178:179], s[28:29] offset:2048
	s_waitcnt vmcnt(31)
	v_lshlrev_b32_e32 v164, 16, v136
	v_and_b32_e32 v165, 0xffff0000, v136
	v_lshlrev_b32_e32 v166, 16, v137
	v_and_b32_e32 v167, 0xffff0000, v137
	v_pk_add_f32 v[184:185], v[184:185], v[164:165]
	v_pk_add_f32 v[186:187], v[186:187], v[166:167]
	v_lshlrev_b32_e32 v168, 16, v104
	v_and_b32_e32 v169, 0xffff0000, v104
	v_lshlrev_b32_e32 v170, 16, v105
	v_and_b32_e32 v171, 0xffff0000, v105
	v_pk_add_f32 v[184:185], v[184:185], v[168:169] neg_lo:[0,1] neg_hi:[0,1]
	v_pk_add_f32 v[186:187], v[186:187], v[170:171] neg_lo:[0,1] neg_hi:[0,1]
	v_pk_fma_f32 v[172:173], v[188:189], v[184:185], v[164:165] op_sel_hi:[0,1,1] neg_lo:[0,0,1] neg_hi:[0,0,1]
	v_pk_fma_f32 v[174:175], v[188:189], v[186:187], v[166:167] op_sel_hi:[0,1,1] neg_lo:[0,0,1] neg_hi:[0,0,1]
	v_cvt_pk_bf16_f32 v180, v172, v173
	v_cvt_pk_bf16_f32 v181, v174, v175
	v_add_u32_e32 v194, 0x9000, v190
	global_store_dwordx2 v194, v[180:181], s[28:29]
	s_waitcnt vmcnt(31)
	v_lshlrev_b32_e32 v164, 16, v138
	v_and_b32_e32 v165, 0xffff0000, v138
	v_lshlrev_b32_e32 v166, 16, v139
	v_and_b32_e32 v167, 0xffff0000, v139
	v_pk_add_f32 v[184:185], v[184:185], v[164:165]
	v_pk_add_f32 v[186:187], v[186:187], v[166:167]
	v_lshlrev_b32_e32 v168, 16, v106
	v_and_b32_e32 v169, 0xffff0000, v106
	v_lshlrev_b32_e32 v170, 16, v107
	v_and_b32_e32 v171, 0xffff0000, v107
	v_pk_add_f32 v[184:185], v[184:185], v[168:169] neg_lo:[0,1] neg_hi:[0,1]
	v_pk_add_f32 v[186:187], v[186:187], v[170:171] neg_lo:[0,1] neg_hi:[0,1]
	v_pk_fma_f32 v[172:173], v[188:189], v[184:185], v[164:165] op_sel_hi:[0,1,1] neg_lo:[0,0,1] neg_hi:[0,0,1]
	v_pk_fma_f32 v[174:175], v[188:189], v[186:187], v[166:167] op_sel_hi:[0,1,1] neg_lo:[0,0,1] neg_hi:[0,0,1]
	v_cvt_pk_bf16_f32 v182, v172, v173
	v_cvt_pk_bf16_f32 v183, v174, v175
	global_store_dwordx2 v194, v[182:183], s[28:29] offset:2048
	s_waitcnt vmcnt(31)
	v_lshlrev_b32_e32 v164, 16, v140
	v_and_b32_e32 v165, 0xffff0000, v140
	v_lshlrev_b32_e32 v166, 16, v141
	v_and_b32_e32 v167, 0xffff0000, v141
	v_pk_add_f32 v[184:185], v[184:185], v[164:165]
	v_pk_add_f32 v[186:187], v[186:187], v[166:167]
	v_lshlrev_b32_e32 v168, 16, v108
	v_and_b32_e32 v169, 0xffff0000, v108
	v_lshlrev_b32_e32 v170, 16, v109
	v_and_b32_e32 v171, 0xffff0000, v109
	v_pk_add_f32 v[184:185], v[184:185], v[168:169] neg_lo:[0,1] neg_hi:[0,1]
	v_pk_add_f32 v[186:187], v[186:187], v[170:171] neg_lo:[0,1] neg_hi:[0,1]
	v_pk_fma_f32 v[172:173], v[188:189], v[184:185], v[164:165] op_sel_hi:[0,1,1] neg_lo:[0,0,1] neg_hi:[0,0,1]
	v_pk_fma_f32 v[174:175], v[188:189], v[186:187], v[166:167] op_sel_hi:[0,1,1] neg_lo:[0,0,1] neg_hi:[0,0,1]
	v_cvt_pk_bf16_f32 v176, v172, v173
	v_cvt_pk_bf16_f32 v177, v174, v175
	v_add_u32_e32 v193, 0xa000, v190
	global_store_dwordx2 v193, v[176:177], s[28:29]
	s_waitcnt vmcnt(31)
; #define GAS __attribute__((address_space(1)))
; __device__ __forceinline__ unsigned pk2(float lo, float hi) { const f32x2 v = {lo, hi}; return __builtin_bit_cast(unsigned, __builtin_convertvector(v, b16x2)); }
; template <int W>
; __device__ __forceinline__ void pool_item(const bf16* U, bf16* Z, int b, int t0, int g, int lane) {
;     ...
; #pragma unroll 8
;     for (int i = 0; i < 32; ++i) { const int t = t0 + i;
;         const u32x2 v = *(const GAS u32x2*)(U + base + (size_t)t * D);
;         const float c0 = bf2f(v.x & 0xffffu), c1 = bf2f(v.x >> 16), c2 = bf2f(v.y & 0xffffu), c3 = bf2f(v.y >> 16);
;         s[0] += c0; s[1] += c1; s[2] += c2; s[3] += c3;
;         if (t - W >= 0) { const u32x2 o = *(const GAS u32x2*)(U + base + (size_t)(t - W) * D);
;             s[0] -= bf2f(o.x & 0xffffu); s[1] -= bf2f(o.x >> 16); s[2] -= bf2f(o.y & 0xffffu); s[3] -= bf2f(o.y >> 16); }
;         const float inv = 1.0f / (float)((t + 1) < W ? (t + 1) : W);
;         u32x2 w; w.x = pk2(s[0] * inv - c0, s[1] * inv - c1); w.y = pk2(s[2] * inv - c2, s[3] * inv - c3);
;         *(GAS u32x2*)(Z + base + (size_t)t * D) = w; }
	v_lshlrev_b32_e32 v164, 16, v142
	v_and_b32_e32 v165, 0xffff0000, v142
	v_lshlrev_b32_e32 v166, 16, v143
	v_and_b32_e32 v167, 0xffff0000, v143
	v_pk_add_f32 v[184:185], v[184:185], v[164:165]
	v_pk_add_f32 v[186:187], v[186:187], v[166:167]
	v_lshlrev_b32_e32 v168, 16, v110
	v_and_b32_e32 v169, 0xffff0000, v110
	v_lshlrev_b32_e32 v170, 16, v111
	v_and_b32_e32 v171, 0xffff0000, v111
	v_pk_add_f32 v[184:185], v[184:185], v[168:169] neg_lo:[0,1] neg_hi:[0,1]
	v_pk_add_f32 v[186:187], v[186:187], v[170:171] neg_lo:[0,1] neg_hi:[0,1]
	v_pk_fma_f32 v[172:173], v[188:189], v[184:185], v[164:165] op_sel_hi:[0,1,1] neg_lo:[0,0,1] neg_hi:[0,0,1]
	v_pk_fma_f32 v[174:175], v[188:189], v[186:187], v[166:167] op_sel_hi:[0,1,1] neg_lo:[0,0,1] neg_hi:[0,0,1]
	v_cvt_pk_bf16_f32 v178, v172, v173
	v_cvt_pk_bf16_f32 v179, v174, v175
	global_store_dwordx2 v193, v[178:179], s[28:29] offset:2048
	s_waitcnt vmcnt(31)
	v_lshlrev_b32_e32 v164, 16, v144
	v_and_b32_e32 v165, 0xffff0000, v144
	v_lshlrev_b32_e32 v166, 16, v145
	v_and_b32_e32 v167, 0xffff0000, v145
	v_pk_add_f32 v[184:185], v[184:185], v[164:165]
	v_pk_add_f32 v[186:187], v[186:187], v[166:167]
	v_lshlrev_b32_e32 v168, 16, v112
	v_and_b32_e32 v169, 0xffff0000, v112
	v_lshlrev_b32_e32 v170, 16, v113
	v_and_b32_e32 v171, 0xffff0000, v113
	v_pk_add_f32 v[184:185], v[184:185], v[168:169] neg_lo:[0,1] neg_hi:[0,1]
	v_pk_add_f32 v[186:187], v[186:187], v[170:171] neg_lo:[0,1] neg_hi:[0,1]
	v_pk_fma_f32 v[172:173], v[188:189], v[184:185], v[164:165] op_sel_hi:[0,1,1] neg_lo:[0,0,1] neg_hi:[0,0,1]
	v_pk_fma_f32 v[174:175], v[188:189], v[186:187], v[166:167] op_sel_hi:[0,1,1] neg_lo:[0,0,1] neg_hi:[0,0,1]
	v_cvt_pk_bf16_f32 v180, v172, v173
	v_cvt_pk_bf16_f32 v181, v174, v175
	v_add_u32_e32 v194, 0xb000, v190
	global_store_dwordx2 v194, v[180:181], s[28:29]
	s_waitcnt vmcnt(31)
	v_lshlrev_b32_e32 v164, 16, v146
	v_and_b32_e32 v165, 0xffff0000, v146
	v_lshlrev_b32_e32 v166, 16, v147
	v_and_b32_e32 v167, 0xffff0000, v147
	v_pk_add_f32 v[184:185], v[184:185], v[164:165]
	v_pk_add_f32 v[186:187], v[186:187], v[166:167]
	v_lshlrev_b32_e32 v168, 16, v114
	v_and_b32_e32 v169, 0xffff0000, v114
	v_lshlrev_b32_e32 v170, 16, v115
	v_and_b32_e32 v171, 0xffff0000, v115
	v_pk_add_f32 v[184:185], v[184:185], v[168:169] neg_lo:[0,1] neg_hi:[0,1]
	v_pk_add_f32 v[186:187], v[186:187], v[170:171] neg_lo:[0,1] neg_hi:[0,1]
	v_pk_fma_f32 v[172:173], v[188:189], v[184:185], v[164:165] op_sel_hi:[0,1,1] neg_lo:[0,0,1] neg_hi:[0,0,1]
	v_pk_fma_f32 v[174:175], v[188:189], v[186:187], v[166:167] op_sel_hi:[0,1,1] neg_lo:[0,0,1] neg_hi:[0,0,1]
	v_cvt_pk_bf16_f32 v182, v172, v173
	v_cvt_pk_bf16_f32 v183, v174, v175
	global_store_dwordx2 v194, v[182:183], s[28:29] offset:2048
	s_waitcnt vmcnt(31)
	v_lshlrev_b32_e32 v164, 16, v148
	v_and_b32_e32 v165, 0xffff0000, v148
	v_lshlrev_b32_e32 v166, 16, v149
	v_and_b32_e32 v167, 0xffff0000, v149
	v_pk_add_f32 v[184:185], v[184:185], v[164:165]
	v_pk_add_f32 v[186:187], v[186:187], v[166:167]
	v_lshlrev_b32_e32 v168, 16, v116
	v_and_b32_e32 v169, 0xffff0000, v116
	v_lshlrev_b32_e32 v170, 16, v117
	v_and_b32_e32 v171, 0xffff0000, v117
	v_pk_add_f32 v[184:185], v[184:185], v[168:169] neg_lo:[0,1] neg_hi:[0,1]
	v_pk_add_f32 v[186:187], v[186:187], v[170:171] neg_lo:[0,1] neg_hi:[0,1]
	v_pk_fma_f32 v[172:173], v[188:189], v[184:185], v[164:165] op_sel_hi:[0,1,1] neg_lo:[0,0,1] neg_hi:[0,0,1]
	v_pk_fma_f32 v[174:175], v[188:189], v[186:187], v[166:167] op_sel_hi:[0,1,1] neg_lo:[0,0,1] neg_hi:[0,0,1]
	v_cvt_pk_bf16_f32 v176, v172, v173
	v_cvt_pk_bf16_f32 v177, v174, v175
	v_add_u32_e32 v193, 0xc000, v190
	global_store_dwordx2 v193, v[176:177], s[28:29]
	s_waitcnt vmcnt(31)
	v_lshlrev_b32_e32 v164, 16, v150
	v_and_b32_e32 v165, 0xffff0000, v150
	v_lshlrev_b32_e32 v166, 16, v151
	v_and_b32_e32 v167, 0xffff0000, v151
	v_pk_add_f32 v[184:185], v[184:185], v[164:165]
	v_pk_add_f32 v[186:187], v[186:187], v[166:167]
	v_lshlrev_b32_e32 v168, 16, v118
	v_and_b32_e32 v169, 0xffff0000, v118
	v_lshlrev_b32_e32 v170, 16, v119
	v_and_b32_e32 v171, 0xffff0000, v119
	v_pk_add_f32 v[184:185], v[184:185], v[168:169] neg_lo:[0,1] neg_hi:[0,1]
	v_pk_add_f32 v[186:187], v[186:187], v[170:171] neg_lo:[0,1] neg_hi:[0,1]
	v_pk_fma_f32 v[172:173], v[188:189], v[184:185], v[164:165] op_sel_hi:[0,1,1] neg_lo:[0,0,1] neg_hi:[0,0,1]
	v_pk_fma_f32 v[174:175], v[188:189], v[186:187], v[166:167] op_sel_hi:[0,1,1] neg_lo:[0,0,1] neg_hi:[0,0,1]
	v_cvt_pk_bf16_f32 v178, v172, v173
	v_cvt_pk_bf16_f32 v179, v174, v175
	global_store_dwordx2 v193, v[178:179], s[28:29] offset:2048
	s_waitcnt vmcnt(31)
	v_lshlrev_b32_e32 v164, 16, v152
	v_and_b32_e32 v165, 0xffff0000, v152
	v_lshlrev_b32_e32 v166, 16, v153
	v_and_b32_e32 v167, 0xffff0000, v153
	v_pk_add_f32 v[184:185], v[184:185], v[164:165]
	v_pk_add_f32 v[186:187], v[186:187], v[166:167]
	v_lshlrev_b32_e32 v168, 16, v120
	v_and_b32_e32 v169, 0xffff0000, v120
	v_lshlrev_b32_e32 v170, 16, v121
	v_and_b32_e32 v171, 0xffff0000, v121
	v_pk_add_f32 v[184:185], v[184:185], v[168:169] neg_lo:[0,1] neg_hi:[0,1]
	v_pk_add_f32 v[186:187], v[186:187], v[170:171] neg_lo:[0,1] neg_hi:[0,1]
	v_pk_fma_f32 v[172:173], v[188:189], v[184:185], v[164:165] op_sel_hi:[0,1,1] neg_lo:[0,0,1] neg_hi:[0,0,1]
	v_pk_fma_f32 v[174:175], v[188:189], v[186:187], v[166:167] op_sel_hi:[0,1,1] neg_lo:[0,0,1] neg_hi:[0,0,1]
	v_cvt_pk_bf16_f32 v180, v172, v173
	v_cvt_pk_bf16_f32 v181, v174, v175
	v_add_u32_e32 v194, 0xd000, v190
	global_store_dwordx2 v194, v[180:181], s[28:29]
	s_waitcnt vmcnt(31)
; #define GAS __attribute__((address_space(1)))
; __device__ __forceinline__ unsigned pk2(float lo, float hi) { const f32x2 v = {lo, hi}; return __builtin_bit_cast(unsigned, __builtin_convertvector(v, b16x2)); }
; template <int W>
; __device__ __forceinline__ void pool_item(const bf16* U, bf16* Z, int b, int t0, int g, int lane) {
;     ...
; #pragma unroll 8
;     for (int i = 0; i < 32; ++i) { const int t = t0 + i;
;         const u32x2 v = *(const GAS u32x2*)(U + base + (size_t)t * D);
;         const float c0 = bf2f(v.x & 0xffffu), c1 = bf2f(v.x >> 16), c2 = bf2f(v.y & 0xffffu), c3 = bf2f(v.y >> 16);
;         s[0] += c0; s[1] += c1; s[2] += c2; s[3] += c3;
;         if (t - W >= 0) { const u32x2 o = *(const GAS u32x2*)(U + base + (size_t)(t - W) * D);
;             s[0] -= bf2f(o.x & 0xffffu); s[1] -= bf2f(o.x >> 16); s[2] -= bf2f(o.y & 0xffffu); s[3] -= bf2f(o.y >> 16); }
;         const float inv = 1.0f / (float)((t + 1) < W ? (t + 1) : W);
;         u32x2 w; w.x = pk2(s[0] * inv - c0, s[1] * inv - c1); w.y = pk2(s[2] * inv - c2, s[3] * inv - c3);
;         *(GAS u32x2*)(Z + base + (size_t)t * D) = w; }
	v_lshlrev_b32_e32 v164, 16, v154
	v_and_b32_e32 v165, 0xffff0000, v154
	v_lshlrev_b32_e32 v166, 16, v155
	v_and_b32_e32 v167, 0xffff0000, v155
	v_pk_add_f32 v[184:185], v[184:185], v[164:165]
	v_pk_add_f32 v[186:187], v[186:187], v[166:167]
	v_lshlrev_b32_e32 v168, 16, v122
	v_and_b32_e32 v169, 0xffff0000, v122
	v_lshlrev_b32_e32 v170, 16, v123
	v_and_b32_e32 v171, 0xffff0000, v123
	v_pk_add_f32 v[184:185], v[184:185], v[168:169] neg_lo:[0,1] neg_hi:[0,1]
	v_pk_add_f32 v[186:187], v[186:187], v[170:171] neg_lo:[0,1] neg_hi:[0,1]
	v_pk_fma_f32 v[172:173], v[188:189], v[184:185], v[164:165] op_sel_hi:[0,1,1] neg_lo:[0,0,1] neg_hi:[0,0,1]
	v_pk_fma_f32 v[174:175], v[188:189], v[186:187], v[166:167] op_sel_hi:[0,1,1] neg_lo:[0,0,1] neg_hi:[0,0,1]
	v_cvt_pk_bf16_f32 v182, v172, v173
	v_cvt_pk_bf16_f32 v183, v174, v175
	global_store_dwordx2 v194, v[182:183], s[28:29] offset:2048
	s_waitcnt vmcnt(31)
	v_lshlrev_b32_e32 v164, 16, v156
	v_and_b32_e32 v165, 0xffff0000, v156
	v_lshlrev_b32_e32 v166, 16, v157
	v_and_b32_e32 v167, 0xffff0000, v157
	v_pk_add_f32 v[184:185], v[184:185], v[164:165]
	v_pk_add_f32 v[186:187], v[186:187], v[166:167]
	v_lshlrev_b32_e32 v168, 16, v124
	v_and_b32_e32 v169, 0xffff0000, v124
	v_lshlrev_b32_e32 v170, 16, v125
	v_and_b32_e32 v171, 0xffff0000, v125
	v_pk_add_f32 v[184:185], v[184:185], v[168:169] neg_lo:[0,1] neg_hi:[0,1]
	v_pk_add_f32 v[186:187], v[186:187], v[170:171] neg_lo:[0,1] neg_hi:[0,1]
	v_pk_fma_f32 v[172:173], v[188:189], v[184:185], v[164:165] op_sel_hi:[0,1,1] neg_lo:[0,0,1] neg_hi:[0,0,1]
	v_pk_fma_f32 v[174:175], v[188:189], v[186:187], v[166:167] op_sel_hi:[0,1,1] neg_lo:[0,0,1] neg_hi:[0,0,1]
	v_cvt_pk_bf16_f32 v176, v172, v173
	v_cvt_pk_bf16_f32 v177, v174, v175
	v_add_u32_e32 v193, 0xe000, v190
	global_store_dwordx2 v193, v[176:177], s[28:29]
	s_waitcnt vmcnt(31)
	v_lshlrev_b32_e32 v164, 16, v158
	v_and_b32_e32 v165, 0xffff0000, v158
	v_lshlrev_b32_e32 v166, 16, v159
	v_and_b32_e32 v167, 0xffff0000, v159
	v_pk_add_f32 v[184:185], v[184:185], v[164:165]
	v_pk_add_f32 v[186:187], v[186:187], v[166:167]
	v_lshlrev_b32_e32 v168, 16, v126
	v_and_b32_e32 v169, 0xffff0000, v126
	v_lshlrev_b32_e32 v170, 16, v127
	v_and_b32_e32 v171, 0xffff0000, v127
	v_pk_add_f32 v[184:185], v[184:185], v[168:169] neg_lo:[0,1] neg_hi:[0,1]
	v_pk_add_f32 v[186:187], v[186:187], v[170:171] neg_lo:[0,1] neg_hi:[0,1]
	v_pk_fma_f32 v[172:173], v[188:189], v[184:185], v[164:165] op_sel_hi:[0,1,1] neg_lo:[0,0,1] neg_hi:[0,0,1]
	v_pk_fma_f32 v[174:175], v[188:189], v[186:187], v[166:167] op_sel_hi:[0,1,1] neg_lo:[0,0,1] neg_hi:[0,0,1]
	v_cvt_pk_bf16_f32 v178, v172, v173
	v_cvt_pk_bf16_f32 v179, v174, v175
	global_store_dwordx2 v193, v[178:179], s[28:29] offset:2048
	s_waitcnt vmcnt(31)
	v_lshlrev_b32_e32 v164, 16, v160
	v_and_b32_e32 v165, 0xffff0000, v160
	v_lshlrev_b32_e32 v166, 16, v161
	v_and_b32_e32 v167, 0xffff0000, v161
	v_pk_add_f32 v[184:185], v[184:185], v[164:165]
	v_pk_add_f32 v[186:187], v[186:187], v[166:167]
	v_lshlrev_b32_e32 v168, 16, v128
	v_and_b32_e32 v169, 0xffff0000, v128
	v_lshlrev_b32_e32 v170, 16, v129
	v_and_b32_e32 v171, 0xffff0000, v129
	v_pk_add_f32 v[184:185], v[184:185], v[168:169] neg_lo:[0,1] neg_hi:[0,1]
	v_pk_add_f32 v[186:187], v[186:187], v[170:171] neg_lo:[0,1] neg_hi:[0,1]
	v_pk_fma_f32 v[172:173], v[188:189], v[184:185], v[164:165] op_sel_hi:[0,1,1] neg_lo:[0,0,1] neg_hi:[0,0,1]
	v_pk_fma_f32 v[174:175], v[188:189], v[186:187], v[166:167] op_sel_hi:[0,1,1] neg_lo:[0,0,1] neg_hi:[0,0,1]
	v_cvt_pk_bf16_f32 v180, v172, v173
	v_cvt_pk_bf16_f32 v181, v174, v175
	v_add_u32_e32 v194, 0xf000, v190
	global_store_dwordx2 v194, v[180:181], s[28:29]
	s_waitcnt vmcnt(31)
	v_lshlrev_b32_e32 v164, 16, v162
	v_and_b32_e32 v165, 0xffff0000, v162
	v_lshlrev_b32_e32 v166, 16, v163
	v_and_b32_e32 v167, 0xffff0000, v163
	v_pk_add_f32 v[184:185], v[184:185], v[164:165]
	v_pk_add_f32 v[186:187], v[186:187], v[166:167]
	v_lshlrev_b32_e32 v168, 16, v130
	v_and_b32_e32 v169, 0xffff0000, v130
	v_lshlrev_b32_e32 v170, 16, v131
	v_and_b32_e32 v171, 0xffff0000, v131
	v_pk_add_f32 v[184:185], v[184:185], v[168:169] neg_lo:[0,1] neg_hi:[0,1]
	v_pk_add_f32 v[186:187], v[186:187], v[170:171] neg_lo:[0,1] neg_hi:[0,1]
	v_pk_fma_f32 v[172:173], v[188:189], v[184:185], v[164:165] op_sel_hi:[0,1,1] neg_lo:[0,0,1] neg_hi:[0,0,1]
	v_pk_fma_f32 v[174:175], v[188:189], v[186:187], v[166:167] op_sel_hi:[0,1,1] neg_lo:[0,0,1] neg_hi:[0,0,1]
	v_cvt_pk_bf16_f32 v182, v172, v173
	v_cvt_pk_bf16_f32 v183, v174, v175
	global_store_dwordx2 v194, v[182:183], s[28:29] offset:2048
	s_branch .LBB0_861
; #define GAS __attribute__((address_space(1)))
; __device__ __forceinline__ unsigned pk2(float lo, float hi) { const f32x2 v = {lo, hi}; return __builtin_bit_cast(unsigned, __builtin_convertvector(v, b16x2)); }
; template <int W>
; __device__ __forceinline__ void pool_item(const bf16* U, bf16* Z, int b, int t0, int g, int lane) {
;     const size_t base = (size_t)b * SEQ * D + 256 * g + 4 * lane;
;     float s[4] = {0.f, 0.f, 0.f, 0.f};
; #pragma unroll
;     for (int j = 1; j <= W; ++j) { const int t = t0 - j; if (t >= 0) { const u32x2 v = *(const GAS u32x2*)(U + base + (size_t)t * D);
;             s[0] += bf2f(v.x & 0xffffu); s[1] += bf2f(v.x >> 16); s[2] += bf2f(v.y & 0xffffu); s[3] += bf2f(v.y >> 16); } }
; #pragma unroll 8
;     for (int i = 0; i < 32; ++i) { const int t = t0 + i;
;         const u32x2 v = *(const GAS u32x2*)(U + base + (size_t)t * D);
;         const float c0 = bf2f(v.x & 0xffffu), c1 = bf2f(v.x >> 16), c2 = bf2f(v.y & 0xffffu), c3 = bf2f(v.y >> 16);
;         s[0] += c0; s[1] += c1; s[2] += c2; s[3] += c3;
;         if (t - W >= 0) { const u32x2 o = *(const GAS u32x2*)(U + base + (size_t)(t - W) * D);
;             s[0] -= bf2f(o.x & 0xffffu); s[1] -= bf2f(o.x >> 16); s[2] -= bf2f(o.y & 0xffffu); s[3] -= bf2f(o.y >> 16); }
;         const float inv = 1.0f / (float)((t + 1) < W ? (t + 1) : W);
;         u32x2 w; w.x = pk2(s[0] * inv - c0, s[1] * inv - c1); w.y = pk2(s[2] * inv - c2, s[3] * inv - c3);
;         *(GAS u32x2*)(Z + base + (size_t)t * D) = w; }
.Lpool0_w8:
	v_add_u32_e32 v192, 0x8000, v190
	global_load_dwordx2 v[100:101], v192, s[10:11]
	global_load_dwordx2 v[102:103], v192, s[10:11] offset:2048
	v_add_u32_e32 v191, 0x9000, v190
	global_load_dwordx2 v[104:105], v191, s[10:11]
	global_load_dwordx2 v[106:107], v191, s[10:11] offset:2048
	v_add_u32_e32 v192, 0xa000, v190
	global_load_dwordx2 v[108:109], v192, s[10:11]
	global_load_dwordx2 v[110:111], v192, s[10:11] offset:2048
	v_add_u32_e32 v191, 0xb000, v190
	global_load_dwordx2 v[112:113], v191, s[10:11]
	global_load_dwordx2 v[114:115], v191, s[10:11] offset:2048
	v_add_u32_e32 v192, 0xc000, v190
	global_load_dwordx2 v[116:117], v192, s[10:11]
	global_load_dwordx2 v[118:119], v192, s[10:11] offset:2048
	v_add_u32_e32 v191, 0xd000, v190
	global_load_dwordx2 v[120:121], v191, s[10:11]
	global_load_dwordx2 v[122:123], v191, s[10:11] offset:2048
	v_add_u32_e32 v192, 0xe000, v190
	global_load_dwordx2 v[124:125], v192, s[10:11]
	global_load_dwordx2 v[126:127], v192, s[10:11] offset:2048
	v_add_u32_e32 v191, 0xf000, v190
	global_load_dwordx2 v[128:129], v191, s[10:11]
	global_load_dwordx2 v[130:131], v191, s[10:11] offset:2048
	v_add_u32_e32 v192, 0x10000, v190
	global_load_dwordx2 v[132:133], v192, s[10:11]
	global_load_dwordx2 v[134:135], v192, s[10:11] offset:2048
	v_add_u32_e32 v191, 0x11000, v190
	global_load_dwordx2 v[136:137], v191, s[10:11]
	global_load_dwordx2 v[138:139], v191, s[10:11] offset:2048
	v_add_u32_e32 v192, 0x12000, v190
	global_load_dwordx2 v[140:141], v192, s[10:11]
	global_load_dwordx2 v[142:143], v192, s[10:11] offset:2048
	v_add_u32_e32 v191, 0x13000, v190
	global_load_dwordx2 v[144:145], v191, s[10:11]
	global_load_dwordx2 v[146:147], v191, s[10:11] offset:2048
	v_add_u32_e32 v192, 0x14000, v190
	global_load_dwordx2 v[148:149], v192, s[10:11]
	global_load_dwordx2 v[150:151], v192, s[10:11] offset:2048
	v_add_u32_e32 v191, 0x15000, v190
	global_load_dwordx2 v[152:153], v191, s[10:11]
	global_load_dwordx2 v[154:155], v191, s[10:11] offset:2048
	v_add_u32_e32 v192, 0x16000, v190
	global_load_dwordx2 v[156:157], v192, s[10:11]
	global_load_dwordx2 v[158:159], v192, s[10:11] offset:2048
	v_add_u32_e32 v191, 0x17000, v190
	global_load_dwordx2 v[160:161], v191, s[10:11]
	global_load_dwordx2 v[162:163], v191, s[10:11] offset:2048
	v_mov_b32_e32 v184, 0
	v_mov_b32_e32 v185, 0
	v_mov_b32_e32 v186, 0
	v_mov_b32_e32 v187, 0
	v_mov_b32_e32 v188, 0x3f800000
	s_waitcnt vmcnt(31)
	v_lshlrev_b32_e32 v164, 16, v100
	v_and_b32_e32 v165, 0xffff0000, v100
	v_lshlrev_b32_e32 v166, 16, v101
	v_and_b32_e32 v167, 0xffff0000, v101
	v_pk_add_f32 v[184:185], v[184:185], v[164:165]
	v_pk_add_f32 v[186:187], v[186:187], v[166:167]
	v_pk_fma_f32 v[172:173], v[188:189], v[184:185], v[164:165] op_sel_hi:[0,1,1] neg_lo:[0,0,1] neg_hi:[0,0,1]
	v_pk_fma_f32 v[174:175], v[188:189], v[186:187], v[166:167] op_sel_hi:[0,1,1] neg_lo:[0,0,1] neg_hi:[0,0,1]
	v_cvt_pk_bf16_f32 v176, v172, v173
	v_cvt_pk_bf16_f32 v177, v174, v175
	global_store_dwordx2 v190, v[176:177], s[28:29]
	v_mov_b32_e32 v188, 0x3f000000
	s_waitcnt vmcnt(31)
	v_lshlrev_b32_e32 v164, 16, v102
	v_and_b32_e32 v165, 0xffff0000, v102
	v_lshlrev_b32_e32 v166, 16, v103
	v_and_b32_e32 v167, 0xffff0000, v103
	v_pk_add_f32 v[184:185], v[184:185], v[164:165]
	v_pk_add_f32 v[186:187], v[186:187], v[166:167]
	v_pk_fma_f32 v[172:173], v[188:189], v[184:185], v[164:165] op_sel_hi:[0,1,1] neg_lo:[0,0,1] neg_hi:[0,0,1]
	v_pk_fma_f32 v[174:175], v[188:189], v[186:187], v[166:167] op_sel_hi:[0,1,1] neg_lo:[0,0,1] neg_hi:[0,0,1]
	v_cvt_pk_bf16_f32 v178, v172, v173
	v_cvt_pk_bf16_f32 v179, v174, v175
	global_store_dwordx2 v190, v[178:179], s[28:29] offset:2048
	v_mov_b32_e32 v188, 0x3eaaaaab
	s_waitcnt vmcnt(31)
	v_lshlrev_b32_e32 v164, 16, v104
	v_and_b32_e32 v165, 0xffff0000, v104
	v_lshlrev_b32_e32 v166, 16, v105
	v_and_b32_e32 v167, 0xffff0000, v105
	v_pk_add_f32 v[184:185], v[184:185], v[164:165]
	v_pk_add_f32 v[186:187], v[186:187], v[166:167]
	v_pk_fma_f32 v[172:173], v[188:189], v[184:185], v[164:165] op_sel_hi:[0,1,1] neg_lo:[0,0,1] neg_hi:[0,0,1]
	v_pk_fma_f32 v[174:175], v[188:189], v[186:187], v[166:167] op_sel_hi:[0,1,1] neg_lo:[0,0,1] neg_hi:[0,0,1]
	v_cvt_pk_bf16_f32 v180, v172, v173
	v_cvt_pk_bf16_f32 v181, v174, v175
	v_add_u32_e32 v194, 0x1000, v190
	global_store_dwordx2 v194, v[180:181], s[28:29]
	v_mov_b32_e32 v188, 0x3e800000
	s_waitcnt vmcnt(31)
	v_lshlrev_b32_e32 v164, 16, v106
	v_and_b32_e32 v165, 0xffff0000, v106
	v_lshlrev_b32_e32 v166, 16, v107
	v_and_b32_e32 v167, 0xffff0000, v107
	v_pk_add_f32 v[184:185], v[184:185], v[164:165]
	v_pk_add_f32 v[186:187], v[186:187], v[166:167]
	v_pk_fma_f32 v[172:173], v[188:189], v[184:185], v[164:165] op_sel_hi:[0,1,1] neg_lo:[0,0,1] neg_hi:[0,0,1]
	v_pk_fma_f32 v[174:175], v[188:189], v[186:187], v[166:167] op_sel_hi:[0,1,1] neg_lo:[0,0,1] neg_hi:[0,0,1]
	v_cvt_pk_bf16_f32 v182, v172, v173
	v_cvt_pk_bf16_f32 v183, v174, v175
	global_store_dwordx2 v194, v[182:183], s[28:29] offset:2048
	v_mov_b32_e32 v188, 0x3e4ccccd
	s_waitcnt vmcnt(31)
	v_lshlrev_b32_e32 v164, 16, v108
	v_and_b32_e32 v165, 0xffff0000, v108
	v_lshlrev_b32_e32 v166, 16, v109
	v_and_b32_e32 v167, 0xffff0000, v109
	v_pk_add_f32 v[184:185], v[184:185], v[164:165]
	v_pk_add_f32 v[186:187], v[186:187], v[166:167]
	v_pk_fma_f32 v[172:173], v[188:189], v[184:185], v[164:165] op_sel_hi:[0,1,1] neg_lo:[0,0,1] neg_hi:[0,0,1]
	v_pk_fma_f32 v[174:175], v[188:189], v[186:187], v[166:167] op_sel_hi:[0,1,1] neg_lo:[0,0,1] neg_hi:[0,0,1]
	v_cvt_pk_bf16_f32 v176, v172, v173
	v_cvt_pk_bf16_f32 v177, v174, v175
	v_add_u32_e32 v193, 0x2000, v190
	global_store_dwordx2 v193, v[176:177], s[28:29]
	v_mov_b32_e32 v188, 0x3e2aaaab
	s_waitcnt vmcnt(31)
; #define GAS __attribute__((address_space(1)))
; __device__ __forceinline__ unsigned pk2(float lo, float hi) { const f32x2 v = {lo, hi}; return __builtin_bit_cast(unsigned, __builtin_convertvector(v, b16x2)); }
; template <int W>
; __device__ __forceinline__ void pool_item(const bf16* U, bf16* Z, int b, int t0, int g, int lane) {
;     ...
; #pragma unroll 8
;     for (int i = 0; i < 32; ++i) { const int t = t0 + i;
;         const u32x2 v = *(const GAS u32x2*)(U + base + (size_t)t * D);
;         const float c0 = bf2f(v.x & 0xffffu), c1 = bf2f(v.x >> 16), c2 = bf2f(v.y & 0xffffu), c3 = bf2f(v.y >> 16);
;         s[0] += c0; s[1] += c1; s[2] += c2; s[3] += c3;
;         if (t - W >= 0) { const u32x2 o = *(const GAS u32x2*)(U + base + (size_t)(t - W) * D);
;             s[0] -= bf2f(o.x & 0xffffu); s[1] -= bf2f(o.x >> 16); s[2] -= bf2f(o.y & 0xffffu); s[3] -= bf2f(o.y >> 16); }
;         const float inv = 1.0f / (float)((t + 1) < W ? (t + 1) : W);
;         u32x2 w; w.x = pk2(s[0] * inv - c0, s[1] * inv - c1); w.y = pk2(s[2] * inv - c2, s[3] * inv - c3);
;         *(GAS u32x2*)(Z + base + (size_t)t * D) = w; }
	v_lshlrev_b32_e32 v164, 16, v110
	v_and_b32_e32 v165, 0xffff0000, v110
	v_lshlrev_b32_e32 v166, 16, v111
	v_and_b32_e32 v167, 0xffff0000, v111
	v_pk_add_f32 v[184:185], v[184:185], v[164:165]
	v_pk_add_f32 v[186:187], v[186:187], v[166:167]
	v_pk_fma_f32 v[172:173], v[188:189], v[184:185], v[164:165] op_sel_hi:[0,1,1] neg_lo:[0,0,1] neg_hi:[0,0,1]
	v_pk_fma_f32 v[174:175], v[188:189], v[186:187], v[166:167] op_sel_hi:[0,1,1] neg_lo:[0,0,1] neg_hi:[0,0,1]
	v_cvt_pk_bf16_f32 v178, v172, v173
	v_cvt_pk_bf16_f32 v179, v174, v175
	global_store_dwordx2 v193, v[178:179], s[28:29] offset:2048
	v_mov_b32_e32 v188, 0x3e124925
	s_waitcnt vmcnt(31)
	v_lshlrev_b32_e32 v164, 16, v112
	v_and_b32_e32 v165, 0xffff0000, v112
	v_lshlrev_b32_e32 v166, 16, v113
	v_and_b32_e32 v167, 0xffff0000, v113
	v_pk_add_f32 v[184:185], v[184:185], v[164:165]
	v_pk_add_f32 v[186:187], v[186:187], v[166:167]
	v_pk_fma_f32 v[172:173], v[188:189], v[184:185], v[164:165] op_sel_hi:[0,1,1] neg_lo:[0,0,1] neg_hi:[0,0,1]
	v_pk_fma_f32 v[174:175], v[188:189], v[186:187], v[166:167] op_sel_hi:[0,1,1] neg_lo:[0,0,1] neg_hi:[0,0,1]
	v_cvt_pk_bf16_f32 v180, v172, v173
	v_cvt_pk_bf16_f32 v181, v174, v175
	v_add_u32_e32 v194, 0x3000, v190
	global_store_dwordx2 v194, v[180:181], s[28:29]
	v_mov_b32_e32 v188, 0x3e000000
	s_waitcnt vmcnt(31)
	v_lshlrev_b32_e32 v164, 16, v114
	v_and_b32_e32 v165, 0xffff0000, v114
	v_lshlrev_b32_e32 v166, 16, v115
	v_and_b32_e32 v167, 0xffff0000, v115
	v_pk_add_f32 v[184:185], v[184:185], v[164:165]
	v_pk_add_f32 v[186:187], v[186:187], v[166:167]
	v_pk_fma_f32 v[172:173], v[188:189], v[184:185], v[164:165] op_sel_hi:[0,1,1] neg_lo:[0,0,1] neg_hi:[0,0,1]
	v_pk_fma_f32 v[174:175], v[188:189], v[186:187], v[166:167] op_sel_hi:[0,1,1] neg_lo:[0,0,1] neg_hi:[0,0,1]
	v_cvt_pk_bf16_f32 v182, v172, v173
	v_cvt_pk_bf16_f32 v183, v174, v175
	global_store_dwordx2 v194, v[182:183], s[28:29] offset:2048
	s_waitcnt vmcnt(31)
	v_lshlrev_b32_e32 v164, 16, v116
	v_and_b32_e32 v165, 0xffff0000, v116
	v_lshlrev_b32_e32 v166, 16, v117
	v_and_b32_e32 v167, 0xffff0000, v117
	v_pk_add_f32 v[184:185], v[184:185], v[164:165]
	v_pk_add_f32 v[186:187], v[186:187], v[166:167]
	v_lshlrev_b32_e32 v168, 16, v100
	v_and_b32_e32 v169, 0xffff0000, v100
	v_lshlrev_b32_e32 v170, 16, v101
	v_and_b32_e32 v171, 0xffff0000, v101
	v_pk_add_f32 v[184:185], v[184:185], v[168:169] neg_lo:[0,1] neg_hi:[0,1]
	v_pk_add_f32 v[186:187], v[186:187], v[170:171] neg_lo:[0,1] neg_hi:[0,1]
	v_pk_fma_f32 v[172:173], v[188:189], v[184:185], v[164:165] op_sel_hi:[0,1,1] neg_lo:[0,0,1] neg_hi:[0,0,1]
	v_pk_fma_f32 v[174:175], v[188:189], v[186:187], v[166:167] op_sel_hi:[0,1,1] neg_lo:[0,0,1] neg_hi:[0,0,1]
	v_cvt_pk_bf16_f32 v176, v172, v173
	v_cvt_pk_bf16_f32 v177, v174, v175
	v_add_u32_e32 v193, 0x4000, v190
	global_store_dwordx2 v193, v[176:177], s[28:29]
	s_waitcnt vmcnt(31)
	v_lshlrev_b32_e32 v164, 16, v118
	v_and_b32_e32 v165, 0xffff0000, v118
	v_lshlrev_b32_e32 v166, 16, v119
	v_and_b32_e32 v167, 0xffff0000, v119
	v_pk_add_f32 v[184:185], v[184:185], v[164:165]
	v_pk_add_f32 v[186:187], v[186:187], v[166:167]
	v_lshlrev_b32_e32 v168, 16, v102
	v_and_b32_e32 v169, 0xffff0000, v102
	v_lshlrev_b32_e32 v170, 16, v103
	v_and_b32_e32 v171, 0xffff0000, v103
	v_pk_add_f32 v[184:185], v[184:185], v[168:169] neg_lo:[0,1] neg_hi:[0,1]
	v_pk_add_f32 v[186:187], v[186:187], v[170:171] neg_lo:[0,1] neg_hi:[0,1]
	v_pk_fma_f32 v[172:173], v[188:189], v[184:185], v[164:165] op_sel_hi:[0,1,1] neg_lo:[0,0,1] neg_hi:[0,0,1]
	v_pk_fma_f32 v[174:175], v[188:189], v[186:187], v[166:167] op_sel_hi:[0,1,1] neg_lo:[0,0,1] neg_hi:[0,0,1]
	v_cvt_pk_bf16_f32 v178, v172, v173
	v_cvt_pk_bf16_f32 v179, v174, v175
	global_store_dwordx2 v193, v[178:179], s[28:29] offset:2048
	s_waitcnt vmcnt(31)
	v_lshlrev_b32_e32 v164, 16, v120
	v_and_b32_e32 v165, 0xffff0000, v120
	v_lshlrev_b32_e32 v166, 16, v121
	v_and_b32_e32 v167, 0xffff0000, v121
	v_pk_add_f32 v[184:185], v[184:185], v[164:165]
	v_pk_add_f32 v[186:187], v[186:187], v[166:167]
	v_lshlrev_b32_e32 v168, 16, v104
	v_and_b32_e32 v169, 0xffff0000, v104
	v_lshlrev_b32_e32 v170, 16, v105
	v_and_b32_e32 v171, 0xffff0000, v105
	v_pk_add_f32 v[184:185], v[184:185], v[168:169] neg_lo:[0,1] neg_hi:[0,1]
	v_pk_add_f32 v[186:187], v[186:187], v[170:171] neg_lo:[0,1] neg_hi:[0,1]
	v_pk_fma_f32 v[172:173], v[188:189], v[184:185], v[164:165] op_sel_hi:[0,1,1] neg_lo:[0,0,1] neg_hi:[0,0,1]
	v_pk_fma_f32 v[174:175], v[188:189], v[186:187], v[166:167] op_sel_hi:[0,1,1] neg_lo:[0,0,1] neg_hi:[0,0,1]
	v_cvt_pk_bf16_f32 v180, v172, v173
	v_cvt_pk_bf16_f32 v181, v174, v175
	v_add_u32_e32 v194, 0x5000, v190
	global_store_dwordx2 v194, v[180:181], s[28:29]
	s_waitcnt vmcnt(31)
	v_lshlrev_b32_e32 v164, 16, v122
	v_and_b32_e32 v165, 0xffff0000, v122
	v_lshlrev_b32_e32 v166, 16, v123
	v_and_b32_e32 v167, 0xffff0000, v123
	v_pk_add_f32 v[184:185], v[184:185], v[164:165]
	v_pk_add_f32 v[186:187], v[186:187], v[166:167]
	v_lshlrev_b32_e32 v168, 16, v106
	v_and_b32_e32 v169, 0xffff0000, v106
	v_lshlrev_b32_e32 v170, 16, v107
	v_and_b32_e32 v171, 0xffff0000, v107
	v_pk_add_f32 v[184:185], v[184:185], v[168:169] neg_lo:[0,1] neg_hi:[0,1]
	v_pk_add_f32 v[186:187], v[186:187], v[170:171] neg_lo:[0,1] neg_hi:[0,1]
	v_pk_fma_f32 v[172:173], v[188:189], v[184:185], v[164:165] op_sel_hi:[0,1,1] neg_lo:[0,0,1] neg_hi:[0,0,1]
	v_pk_fma_f32 v[174:175], v[188:189], v[186:187], v[166:167] op_sel_hi:[0,1,1] neg_lo:[0,0,1] neg_hi:[0,0,1]
	v_cvt_pk_bf16_f32 v182, v172, v173
	v_cvt_pk_bf16_f32 v183, v174, v175
	global_store_dwordx2 v194, v[182:183], s[28:29] offset:2048
	s_waitcnt vmcnt(31)
; #define GAS __attribute__((address_space(1)))
; __device__ __forceinline__ unsigned pk2(float lo, float hi) { const f32x2 v = {lo, hi}; return __builtin_bit_cast(unsigned, __builtin_convertvector(v, b16x2)); }
; template <int W>
; __device__ __forceinline__ void pool_item(const bf16* U, bf16* Z, int b, int t0, int g, int lane) {
;     ...
; #pragma unroll 8
;     for (int i = 0; i < 32; ++i) { const int t = t0 + i;
;         const u32x2 v = *(const GAS u32x2*)(U + base + (size_t)t * D);
;         const float c0 = bf2f(v.x & 0xffffu), c1 = bf2f(v.x >> 16), c2 = bf2f(v.y & 0xffffu), c3 = bf2f(v.y >> 16);
;         s[0] += c0; s[1] += c1; s[2] += c2; s[3] += c3;
;         if (t - W >= 0) { const u32x2 o = *(const GAS u32x2*)(U + base + (size_t)(t - W) * D);
;             s[0] -= bf2f(o.x & 0xffffu); s[1] -= bf2f(o.x >> 16); s[2] -= bf2f(o.y & 0xffffu); s[3] -= bf2f(o.y >> 16); }
;         const float inv = 1.0f / (float)((t + 1) < W ? (t + 1) : W);
;         u32x2 w; w.x = pk2(s[0] * inv - c0, s[1] * inv - c1); w.y = pk2(s[2] * inv - c2, s[3] * inv - c3);
;         *(GAS u32x2*)(Z + base + (size_t)t * D) = w; }
	v_lshlrev_b32_e32 v164, 16, v124
	v_and_b32_e32 v165, 0xffff0000, v124
	v_lshlrev_b32_e32 v166, 16, v125
	v_and_b32_e32 v167, 0xffff0000, v125
	v_pk_add_f32 v[184:185], v[184:185], v[164:165]
	v_pk_add_f32 v[186:187], v[186:187], v[166:167]
	v_lshlrev_b32_e32 v168, 16, v108
	v_and_b32_e32 v169, 0xffff0000, v108
	v_lshlrev_b32_e32 v170, 16, v109
	v_and_b32_e32 v171, 0xffff0000, v109
	v_pk_add_f32 v[184:185], v[184:185], v[168:169] neg_lo:[0,1] neg_hi:[0,1]
	v_pk_add_f32 v[186:187], v[186:187], v[170:171] neg_lo:[0,1] neg_hi:[0,1]
	v_pk_fma_f32 v[172:173], v[188:189], v[184:185], v[164:165] op_sel_hi:[0,1,1] neg_lo:[0,0,1] neg_hi:[0,0,1]
	v_pk_fma_f32 v[174:175], v[188:189], v[186:187], v[166:167] op_sel_hi:[0,1,1] neg_lo:[0,0,1] neg_hi:[0,0,1]
	v_cvt_pk_bf16_f32 v176, v172, v173
	v_cvt_pk_bf16_f32 v177, v174, v175
	v_add_u32_e32 v193, 0x6000, v190
	global_store_dwordx2 v193, v[176:177], s[28:29]
	s_waitcnt vmcnt(31)
	v_lshlrev_b32_e32 v164, 16, v126
	v_and_b32_e32 v165, 0xffff0000, v126
	v_lshlrev_b32_e32 v166, 16, v127
	v_and_b32_e32 v167, 0xffff0000, v127
	v_pk_add_f32 v[184:185], v[184:185], v[164:165]
	v_pk_add_f32 v[186:187], v[186:187], v[166:167]
	v_lshlrev_b32_e32 v168, 16, v110
	v_and_b32_e32 v169, 0xffff0000, v110
	v_lshlrev_b32_e32 v170, 16, v111
	v_and_b32_e32 v171, 0xffff0000, v111
	v_pk_add_f32 v[184:185], v[184:185], v[168:169] neg_lo:[0,1] neg_hi:[0,1]
	v_pk_add_f32 v[186:187], v[186:187], v[170:171] neg_lo:[0,1] neg_hi:[0,1]
	v_pk_fma_f32 v[172:173], v[188:189], v[184:185], v[164:165] op_sel_hi:[0,1,1] neg_lo:[0,0,1] neg_hi:[0,0,1]
	v_pk_fma_f32 v[174:175], v[188:189], v[186:187], v[166:167] op_sel_hi:[0,1,1] neg_lo:[0,0,1] neg_hi:[0,0,1]
	v_cvt_pk_bf16_f32 v178, v172, v173
	v_cvt_pk_bf16_f32 v179, v174, v175
	global_store_dwordx2 v193, v[178:179], s[28:29] offset:2048
	s_waitcnt vmcnt(31)
	v_lshlrev_b32_e32 v164, 16, v128
	v_and_b32_e32 v165, 0xffff0000, v128
	v_lshlrev_b32_e32 v166, 16, v129
	v_and_b32_e32 v167, 0xffff0000, v129
	v_pk_add_f32 v[184:185], v[184:185], v[164:165]
	v_pk_add_f32 v[186:187], v[186:187], v[166:167]
	v_lshlrev_b32_e32 v168, 16, v112
	v_and_b32_e32 v169, 0xffff0000, v112
	v_lshlrev_b32_e32 v170, 16, v113
	v_and_b32_e32 v171, 0xffff0000, v113
	v_pk_add_f32 v[184:185], v[184:185], v[168:169] neg_lo:[0,1] neg_hi:[0,1]
	v_pk_add_f32 v[186:187], v[186:187], v[170:171] neg_lo:[0,1] neg_hi:[0,1]
	v_pk_fma_f32 v[172:173], v[188:189], v[184:185], v[164:165] op_sel_hi:[0,1,1] neg_lo:[0,0,1] neg_hi:[0,0,1]
	v_pk_fma_f32 v[174:175], v[188:189], v[186:187], v[166:167] op_sel_hi:[0,1,1] neg_lo:[0,0,1] neg_hi:[0,0,1]
	v_cvt_pk_bf16_f32 v180, v172, v173
	v_cvt_pk_bf16_f32 v181, v174, v175
	v_add_u32_e32 v194, 0x7000, v190
	global_store_dwordx2 v194, v[180:181], s[28:29]
	s_waitcnt vmcnt(31)
	v_lshlrev_b32_e32 v164, 16, v130
	v_and_b32_e32 v165, 0xffff0000, v130
	v_lshlrev_b32_e32 v166, 16, v131
	v_and_b32_e32 v167, 0xffff0000, v131
	v_pk_add_f32 v[184:185], v[184:185], v[164:165]
	v_pk_add_f32 v[186:187], v[186:187], v[166:167]
	v_lshlrev_b32_e32 v168, 16, v114
	v_and_b32_e32 v169, 0xffff0000, v114
	v_lshlrev_b32_e32 v170, 16, v115
	v_and_b32_e32 v171, 0xffff0000, v115
	v_pk_add_f32 v[184:185], v[184:185], v[168:169] neg_lo:[0,1] neg_hi:[0,1]
	v_pk_add_f32 v[186:187], v[186:187], v[170:171] neg_lo:[0,1] neg_hi:[0,1]
	v_pk_fma_f32 v[172:173], v[188:189], v[184:185], v[164:165] op_sel_hi:[0,1,1] neg_lo:[0,0,1] neg_hi:[0,0,1]
	v_pk_fma_f32 v[174:175], v[188:189], v[186:187], v[166:167] op_sel_hi:[0,1,1] neg_lo:[0,0,1] neg_hi:[0,0,1]
	v_cvt_pk_bf16_f32 v182, v172, v173
	v_cvt_pk_bf16_f32 v183, v174, v175
	global_store_dwordx2 v194, v[182:183], s[28:29] offset:2048
	s_waitcnt vmcnt(31)
	v_lshlrev_b32_e32 v164, 16, v132
	v_and_b32_e32 v165, 0xffff0000, v132
	v_lshlrev_b32_e32 v166, 16, v133
	v_and_b32_e32 v167, 0xffff0000, v133
	v_pk_add_f32 v[184:185], v[184:185], v[164:165]
	v_pk_add_f32 v[186:187], v[186:187], v[166:167]
	v_lshlrev_b32_e32 v168, 16, v116
	v_and_b32_e32 v169, 0xffff0000, v116
	v_lshlrev_b32_e32 v170, 16, v117
	v_and_b32_e32 v171, 0xffff0000, v117
	v_pk_add_f32 v[184:185], v[184:185], v[168:169] neg_lo:[0,1] neg_hi:[0,1]
	v_pk_add_f32 v[186:187], v[186:187], v[170:171] neg_lo:[0,1] neg_hi:[0,1]
	v_pk_fma_f32 v[172:173], v[188:189], v[184:185], v[164:165] op_sel_hi:[0,1,1] neg_lo:[0,0,1] neg_hi:[0,0,1]
	v_pk_fma_f32 v[174:175], v[188:189], v[186:187], v[166:167] op_sel_hi:[0,1,1] neg_lo:[0,0,1] neg_hi:[0,0,1]
	v_cvt_pk_bf16_f32 v176, v172, v173
	v_cvt_pk_bf16_f32 v177, v174, v175
	v_add_u32_e32 v193, 0x8000, v190
	global_store_dwordx2 v193, v[176:177], s[28:29]
	s_waitcnt vmcnt(31)
	v_lshlrev_b32_e32 v164, 16, v134
	v_and_b32_e32 v165, 0xffff0000, v134
	v_lshlrev_b32_e32 v166, 16, v135
	v_and_b32_e32 v167, 0xffff0000, v135
	v_pk_add_f32 v[184:185], v[184:185], v[164:165]
	v_pk_add_f32 v[186:187], v[186:187], v[166:167]
	v_lshlrev_b32_e32 v168, 16, v118
	v_and_b32_e32 v169, 0xffff0000, v118
	v_lshlrev_b32_e32 v170, 16, v119
	v_and_b32_e32 v171, 0xffff0000, v119
	v_pk_add_f32 v[184:185], v[184:185], v[168:169] neg_lo:[0,1] neg_hi:[0,1]
	v_pk_add_f32 v[186:187], v[186:187], v[170:171] neg_lo:[0,1] neg_hi:[0,1]
	v_pk_fma_f32 v[172:173], v[188:189], v[184:185], v[164:165] op_sel_hi:[0,1,1] neg_lo:[0,0,1] neg_hi:[0,0,1]
	v_pk_fma_f32 v[174:175], v[188:189], v[186:187], v[166:167] op_sel_hi:[0,1,1] neg_lo:[0,0,1] neg_hi:[0,0,1]
	v_cvt_pk_bf16_f32 v178, v172, v173
	v_cvt_pk_bf16_f32 v179, v174, v175
	global_store_dwordx2 v193, v[178:179], s[28:29] offset:2048
	s_waitcnt vmcnt(31)
; #define GAS __attribute__((address_space(1)))
; __device__ __forceinline__ unsigned pk2(float lo, float hi) { const f32x2 v = {lo, hi}; return __builtin_bit_cast(unsigned, __builtin_convertvector(v, b16x2)); }
; template <int W>
; __device__ __forceinline__ void pool_item(const bf16* U, bf16* Z, int b, int t0, int g, int lane) {
;     ...
; #pragma unroll 8
;     for (int i = 0; i < 32; ++i) { const int t = t0 + i;
;         const u32x2 v = *(const GAS u32x2*)(U + base + (size_t)t * D);
;         const float c0 = bf2f(v.x & 0xffffu), c1 = bf2f(v.x >> 16), c2 = bf2f(v.y & 0xffffu), c3 = bf2f(v.y >> 16);
;         s[0] += c0; s[1] += c1; s[2] += c2; s[3] += c3;
;         if (t - W >= 0) { const u32x2 o = *(const GAS u32x2*)(U + base + (size_t)(t - W) * D);
;             s[0] -= bf2f(o.x & 0xffffu); s[1] -= bf2f(o.x >> 16); s[2] -= bf2f(o.y & 0xffffu); s[3] -= bf2f(o.y >> 16); }
;         const float inv = 1.0f / (float)((t + 1) < W ? (t + 1) : W);
;         u32x2 w; w.x = pk2(s[0] * inv - c0, s[1] * inv - c1); w.y = pk2(s[2] * inv - c2, s[3] * inv - c3);
;         *(GAS u32x2*)(Z + base + (size_t)t * D) = w; }
	v_lshlrev_b32_e32 v164, 16, v136
	v_and_b32_e32 v165, 0xffff0000, v136
	v_lshlrev_b32_e32 v166, 16, v137
	v_and_b32_e32 v167, 0xffff0000, v137
	v_pk_add_f32 v[184:185], v[184:185], v[164:165]
	v_pk_add_f32 v[186:187], v[186:187], v[166:167]
	v_lshlrev_b32_e32 v168, 16, v120
	v_and_b32_e32 v169, 0xffff0000, v120
	v_lshlrev_b32_e32 v170, 16, v121
	v_and_b32_e32 v171, 0xffff0000, v121
	v_pk_add_f32 v[184:185], v[184:185], v[168:169] neg_lo:[0,1] neg_hi:[0,1]
	v_pk_add_f32 v[186:187], v[186:187], v[170:171] neg_lo:[0,1] neg_hi:[0,1]
	v_pk_fma_f32 v[172:173], v[188:189], v[184:185], v[164:165] op_sel_hi:[0,1,1] neg_lo:[0,0,1] neg_hi:[0,0,1]
	v_pk_fma_f32 v[174:175], v[188:189], v[186:187], v[166:167] op_sel_hi:[0,1,1] neg_lo:[0,0,1] neg_hi:[0,0,1]
	v_cvt_pk_bf16_f32 v180, v172, v173
	v_cvt_pk_bf16_f32 v181, v174, v175
	v_add_u32_e32 v194, 0x9000, v190
	global_store_dwordx2 v194, v[180:181], s[28:29]
	s_waitcnt vmcnt(31)
	v_lshlrev_b32_e32 v164, 16, v138
	v_and_b32_e32 v165, 0xffff0000, v138
	v_lshlrev_b32_e32 v166, 16, v139
	v_and_b32_e32 v167, 0xffff0000, v139
	v_pk_add_f32 v[184:185], v[184:185], v[164:165]
	v_pk_add_f32 v[186:187], v[186:187], v[166:167]
	v_lshlrev_b32_e32 v168, 16, v122
	v_and_b32_e32 v169, 0xffff0000, v122
	v_lshlrev_b32_e32 v170, 16, v123
	v_and_b32_e32 v171, 0xffff0000, v123
	v_pk_add_f32 v[184:185], v[184:185], v[168:169] neg_lo:[0,1] neg_hi:[0,1]
	v_pk_add_f32 v[186:187], v[186:187], v[170:171] neg_lo:[0,1] neg_hi:[0,1]
	v_pk_fma_f32 v[172:173], v[188:189], v[184:185], v[164:165] op_sel_hi:[0,1,1] neg_lo:[0,0,1] neg_hi:[0,0,1]
	v_pk_fma_f32 v[174:175], v[188:189], v[186:187], v[166:167] op_sel_hi:[0,1,1] neg_lo:[0,0,1] neg_hi:[0,0,1]
	v_cvt_pk_bf16_f32 v182, v172, v173
	v_cvt_pk_bf16_f32 v183, v174, v175
	global_store_dwordx2 v194, v[182:183], s[28:29] offset:2048
	s_waitcnt vmcnt(31)
	v_lshlrev_b32_e32 v164, 16, v140
	v_and_b32_e32 v165, 0xffff0000, v140
	v_lshlrev_b32_e32 v166, 16, v141
	v_and_b32_e32 v167, 0xffff0000, v141
	v_pk_add_f32 v[184:185], v[184:185], v[164:165]
	v_pk_add_f32 v[186:187], v[186:187], v[166:167]
	v_lshlrev_b32_e32 v168, 16, v124
	v_and_b32_e32 v169, 0xffff0000, v124
	v_lshlrev_b32_e32 v170, 16, v125
	v_and_b32_e32 v171, 0xffff0000, v125
	v_pk_add_f32 v[184:185], v[184:185], v[168:169] neg_lo:[0,1] neg_hi:[0,1]
	v_pk_add_f32 v[186:187], v[186:187], v[170:171] neg_lo:[0,1] neg_hi:[0,1]
	v_pk_fma_f32 v[172:173], v[188:189], v[184:185], v[164:165] op_sel_hi:[0,1,1] neg_lo:[0,0,1] neg_hi:[0,0,1]
	v_pk_fma_f32 v[174:175], v[188:189], v[186:187], v[166:167] op_sel_hi:[0,1,1] neg_lo:[0,0,1] neg_hi:[0,0,1]
	v_cvt_pk_bf16_f32 v176, v172, v173
	v_cvt_pk_bf16_f32 v177, v174, v175
	v_add_u32_e32 v193, 0xa000, v190
	global_store_dwordx2 v193, v[176:177], s[28:29]
	s_waitcnt vmcnt(31)
	v_lshlrev_b32_e32 v164, 16, v142
	v_and_b32_e32 v165, 0xffff0000, v142
	v_lshlrev_b32_e32 v166, 16, v143
	v_and_b32_e32 v167, 0xffff0000, v143
	v_pk_add_f32 v[184:185], v[184:185], v[164:165]
	v_pk_add_f32 v[186:187], v[186:187], v[166:167]
	v_lshlrev_b32_e32 v168, 16, v126
	v_and_b32_e32 v169, 0xffff0000, v126
	v_lshlrev_b32_e32 v170, 16, v127
	v_and_b32_e32 v171, 0xffff0000, v127
	v_pk_add_f32 v[184:185], v[184:185], v[168:169] neg_lo:[0,1] neg_hi:[0,1]
	v_pk_add_f32 v[186:187], v[186:187], v[170:171] neg_lo:[0,1] neg_hi:[0,1]
	v_pk_fma_f32 v[172:173], v[188:189], v[184:185], v[164:165] op_sel_hi:[0,1,1] neg_lo:[0,0,1] neg_hi:[0,0,1]
	v_pk_fma_f32 v[174:175], v[188:189], v[186:187], v[166:167] op_sel_hi:[0,1,1] neg_lo:[0,0,1] neg_hi:[0,0,1]
	v_cvt_pk_bf16_f32 v178, v172, v173
	v_cvt_pk_bf16_f32 v179, v174, v175
	global_store_dwordx2 v193, v[178:179], s[28:29] offset:2048
	s_waitcnt vmcnt(31)
	v_lshlrev_b32_e32 v164, 16, v144
	v_and_b32_e32 v165, 0xffff0000, v144
	v_lshlrev_b32_e32 v166, 16, v145
	v_and_b32_e32 v167, 0xffff0000, v145
	v_pk_add_f32 v[184:185], v[184:185], v[164:165]
	v_pk_add_f32 v[186:187], v[186:187], v[166:167]
	v_lshlrev_b32_e32 v168, 16, v128
	v_and_b32_e32 v169, 0xffff0000, v128
	v_lshlrev_b32_e32 v170, 16, v129
	v_and_b32_e32 v171, 0xffff0000, v129
	v_pk_add_f32 v[184:185], v[184:185], v[168:169] neg_lo:[0,1] neg_hi:[0,1]
	v_pk_add_f32 v[186:187], v[186:187], v[170:171] neg_lo:[0,1] neg_hi:[0,1]
	v_pk_fma_f32 v[172:173], v[188:189], v[184:185], v[164:165] op_sel_hi:[0,1,1] neg_lo:[0,0,1] neg_hi:[0,0,1]
	v_pk_fma_f32 v[174:175], v[188:189], v[186:187], v[166:167] op_sel_hi:[0,1,1] neg_lo:[0,0,1] neg_hi:[0,0,1]
	v_cvt_pk_bf16_f32 v180, v172, v173
	v_cvt_pk_bf16_f32 v181, v174, v175
	v_add_u32_e32 v194, 0xb000, v190
	global_store_dwordx2 v194, v[180:181], s[28:29]
	s_waitcnt vmcnt(31)
	v_lshlrev_b32_e32 v164, 16, v146
	v_and_b32_e32 v165, 0xffff0000, v146
	v_lshlrev_b32_e32 v166, 16, v147
	v_and_b32_e32 v167, 0xffff0000, v147
	v_pk_add_f32 v[184:185], v[184:185], v[164:165]
	v_pk_add_f32 v[186:187], v[186:187], v[166:167]
	v_lshlrev_b32_e32 v168, 16, v130
	v_and_b32_e32 v169, 0xffff0000, v130
	v_lshlrev_b32_e32 v170, 16, v131
	v_and_b32_e32 v171, 0xffff0000, v131
	v_pk_add_f32 v[184:185], v[184:185], v[168:169] neg_lo:[0,1] neg_hi:[0,1]
	v_pk_add_f32 v[186:187], v[186:187], v[170:171] neg_lo:[0,1] neg_hi:[0,1]
	v_pk_fma_f32 v[172:173], v[188:189], v[184:185], v[164:165] op_sel_hi:[0,1,1] neg_lo:[0,0,1] neg_hi:[0,0,1]
	v_pk_fma_f32 v[174:175], v[188:189], v[186:187], v[166:167] op_sel_hi:[0,1,1] neg_lo:[0,0,1] neg_hi:[0,0,1]
	v_cvt_pk_bf16_f32 v182, v172, v173
	v_cvt_pk_bf16_f32 v183, v174, v175
	global_store_dwordx2 v194, v[182:183], s[28:29] offset:2048
	s_waitcnt vmcnt(31)
; #define GAS __attribute__((address_space(1)))
; __device__ __forceinline__ unsigned pk2(float lo, float hi) { const f32x2 v = {lo, hi}; return __builtin_bit_cast(unsigned, __builtin_convertvector(v, b16x2)); }
; template <int W>
; __device__ __forceinline__ void pool_item(const bf16* U, bf16* Z, int b, int t0, int g, int lane) {
;     ...
; #pragma unroll 8
;     for (int i = 0; i < 32; ++i) { const int t = t0 + i;
;         const u32x2 v = *(const GAS u32x2*)(U + base + (size_t)t * D);
;         const float c0 = bf2f(v.x & 0xffffu), c1 = bf2f(v.x >> 16), c2 = bf2f(v.y & 0xffffu), c3 = bf2f(v.y >> 16);
;         s[0] += c0; s[1] += c1; s[2] += c2; s[3] += c3;
;         if (t - W >= 0) { const u32x2 o = *(const GAS u32x2*)(U + base + (size_t)(t - W) * D);
;             s[0] -= bf2f(o.x & 0xffffu); s[1] -= bf2f(o.x >> 16); s[2] -= bf2f(o.y & 0xffffu); s[3] -= bf2f(o.y >> 16); }
;         const float inv = 1.0f / (float)((t + 1) < W ? (t + 1) : W);
;         u32x2 w; w.x = pk2(s[0] * inv - c0, s[1] * inv - c1); w.y = pk2(s[2] * inv - c2, s[3] * inv - c3);
;         *(GAS u32x2*)(Z + base + (size_t)t * D) = w; }
	v_lshlrev_b32_e32 v164, 16, v148
	v_and_b32_e32 v165, 0xffff0000, v148
	v_lshlrev_b32_e32 v166, 16, v149
	v_and_b32_e32 v167, 0xffff0000, v149
	v_pk_add_f32 v[184:185], v[184:185], v[164:165]
	v_pk_add_f32 v[186:187], v[186:187], v[166:167]
	v_lshlrev_b32_e32 v168, 16, v132
	v_and_b32_e32 v169, 0xffff0000, v132
	v_lshlrev_b32_e32 v170, 16, v133
	v_and_b32_e32 v171, 0xffff0000, v133
	v_pk_add_f32 v[184:185], v[184:185], v[168:169] neg_lo:[0,1] neg_hi:[0,1]
	v_pk_add_f32 v[186:187], v[186:187], v[170:171] neg_lo:[0,1] neg_hi:[0,1]
	v_pk_fma_f32 v[172:173], v[188:189], v[184:185], v[164:165] op_sel_hi:[0,1,1] neg_lo:[0,0,1] neg_hi:[0,0,1]
	v_pk_fma_f32 v[174:175], v[188:189], v[186:187], v[166:167] op_sel_hi:[0,1,1] neg_lo:[0,0,1] neg_hi:[0,0,1]
	v_cvt_pk_bf16_f32 v176, v172, v173
	v_cvt_pk_bf16_f32 v177, v174, v175
	v_add_u32_e32 v193, 0xc000, v190
	global_store_dwordx2 v193, v[176:177], s[28:29]
	s_waitcnt vmcnt(31)
	v_lshlrev_b32_e32 v164, 16, v150
	v_and_b32_e32 v165, 0xffff0000, v150
	v_lshlrev_b32_e32 v166, 16, v151
	v_and_b32_e32 v167, 0xffff0000, v151
	v_pk_add_f32 v[184:185], v[184:185], v[164:165]
	v_pk_add_f32 v[186:187], v[186:187], v[166:167]
	v_lshlrev_b32_e32 v168, 16, v134
	v_and_b32_e32 v169, 0xffff0000, v134
	v_lshlrev_b32_e32 v170, 16, v135
	v_and_b32_e32 v171, 0xffff0000, v135
	v_pk_add_f32 v[184:185], v[184:185], v[168:169] neg_lo:[0,1] neg_hi:[0,1]
	v_pk_add_f32 v[186:187], v[186:187], v[170:171] neg_lo:[0,1] neg_hi:[0,1]
	v_pk_fma_f32 v[172:173], v[188:189], v[184:185], v[164:165] op_sel_hi:[0,1,1] neg_lo:[0,0,1] neg_hi:[0,0,1]
	v_pk_fma_f32 v[174:175], v[188:189], v[186:187], v[166:167] op_sel_hi:[0,1,1] neg_lo:[0,0,1] neg_hi:[0,0,1]
	v_cvt_pk_bf16_f32 v178, v172, v173
	v_cvt_pk_bf16_f32 v179, v174, v175
	global_store_dwordx2 v193, v[178:179], s[28:29] offset:2048
	s_waitcnt vmcnt(31)
	v_lshlrev_b32_e32 v164, 16, v152
	v_and_b32_e32 v165, 0xffff0000, v152
	v_lshlrev_b32_e32 v166, 16, v153
	v_and_b32_e32 v167, 0xffff0000, v153
	v_pk_add_f32 v[184:185], v[184:185], v[164:165]
	v_pk_add_f32 v[186:187], v[186:187], v[166:167]
	v_lshlrev_b32_e32 v168, 16, v136
	v_and_b32_e32 v169, 0xffff0000, v136
	v_lshlrev_b32_e32 v170, 16, v137
	v_and_b32_e32 v171, 0xffff0000, v137
	v_pk_add_f32 v[184:185], v[184:185], v[168:169] neg_lo:[0,1] neg_hi:[0,1]
	v_pk_add_f32 v[186:187], v[186:187], v[170:171] neg_lo:[0,1] neg_hi:[0,1]
	v_pk_fma_f32 v[172:173], v[188:189], v[184:185], v[164:165] op_sel_hi:[0,1,1] neg_lo:[0,0,1] neg_hi:[0,0,1]
	v_pk_fma_f32 v[174:175], v[188:189], v[186:187], v[166:167] op_sel_hi:[0,1,1] neg_lo:[0,0,1] neg_hi:[0,0,1]
	v_cvt_pk_bf16_f32 v180, v172, v173
	v_cvt_pk_bf16_f32 v181, v174, v175
	v_add_u32_e32 v194, 0xd000, v190
	global_store_dwordx2 v194, v[180:181], s[28:29]
	s_waitcnt vmcnt(31)
	v_lshlrev_b32_e32 v164, 16, v154
	v_and_b32_e32 v165, 0xffff0000, v154
	v_lshlrev_b32_e32 v166, 16, v155
	v_and_b32_e32 v167, 0xffff0000, v155
	v_pk_add_f32 v[184:185], v[184:185], v[164:165]
	v_pk_add_f32 v[186:187], v[186:187], v[166:167]
	v_lshlrev_b32_e32 v168, 16, v138
	v_and_b32_e32 v169, 0xffff0000, v138
	v_lshlrev_b32_e32 v170, 16, v139
	v_and_b32_e32 v171, 0xffff0000, v139
	v_pk_add_f32 v[184:185], v[184:185], v[168:169] neg_lo:[0,1] neg_hi:[0,1]
	v_pk_add_f32 v[186:187], v[186:187], v[170:171] neg_lo:[0,1] neg_hi:[0,1]
	v_pk_fma_f32 v[172:173], v[188:189], v[184:185], v[164:165] op_sel_hi:[0,1,1] neg_lo:[0,0,1] neg_hi:[0,0,1]
	v_pk_fma_f32 v[174:175], v[188:189], v[186:187], v[166:167] op_sel_hi:[0,1,1] neg_lo:[0,0,1] neg_hi:[0,0,1]
	v_cvt_pk_bf16_f32 v182, v172, v173
	v_cvt_pk_bf16_f32 v183, v174, v175
	global_store_dwordx2 v194, v[182:183], s[28:29] offset:2048
	s_waitcnt vmcnt(31)
	v_lshlrev_b32_e32 v164, 16, v156
	v_and_b32_e32 v165, 0xffff0000, v156
	v_lshlrev_b32_e32 v166, 16, v157
	v_and_b32_e32 v167, 0xffff0000, v157
	v_pk_add_f32 v[184:185], v[184:185], v[164:165]
	v_pk_add_f32 v[186:187], v[186:187], v[166:167]
	v_lshlrev_b32_e32 v168, 16, v140
	v_and_b32_e32 v169, 0xffff0000, v140
	v_lshlrev_b32_e32 v170, 16, v141
	v_and_b32_e32 v171, 0xffff0000, v141
	v_pk_add_f32 v[184:185], v[184:185], v[168:169] neg_lo:[0,1] neg_hi:[0,1]
	v_pk_add_f32 v[186:187], v[186:187], v[170:171] neg_lo:[0,1] neg_hi:[0,1]
	v_pk_fma_f32 v[172:173], v[188:189], v[184:185], v[164:165] op_sel_hi:[0,1,1] neg_lo:[0,0,1] neg_hi:[0,0,1]
	v_pk_fma_f32 v[174:175], v[188:189], v[186:187], v[166:167] op_sel_hi:[0,1,1] neg_lo:[0,0,1] neg_hi:[0,0,1]
	v_cvt_pk_bf16_f32 v176, v172, v173
	v_cvt_pk_bf16_f32 v177, v174, v175
	v_add_u32_e32 v193, 0xe000, v190
	global_store_dwordx2 v193, v[176:177], s[28:29]
	s_waitcnt vmcnt(31)
	v_lshlrev_b32_e32 v164, 16, v158
	v_and_b32_e32 v165, 0xffff0000, v158
	v_lshlrev_b32_e32 v166, 16, v159
	v_and_b32_e32 v167, 0xffff0000, v159
	v_pk_add_f32 v[184:185], v[184:185], v[164:165]
	v_pk_add_f32 v[186:187], v[186:187], v[166:167]
	v_lshlrev_b32_e32 v168, 16, v142
	v_and_b32_e32 v169, 0xffff0000, v142
	v_lshlrev_b32_e32 v170, 16, v143
	v_and_b32_e32 v171, 0xffff0000, v143
	v_pk_add_f32 v[184:185], v[184:185], v[168:169] neg_lo:[0,1] neg_hi:[0,1]
	v_pk_add_f32 v[186:187], v[186:187], v[170:171] neg_lo:[0,1] neg_hi:[0,1]
	v_pk_fma_f32 v[172:173], v[188:189], v[184:185], v[164:165] op_sel_hi:[0,1,1] neg_lo:[0,0,1] neg_hi:[0,0,1]
	v_pk_fma_f32 v[174:175], v[188:189], v[186:187], v[166:167] op_sel_hi:[0,1,1] neg_lo:[0,0,1] neg_hi:[0,0,1]
	v_cvt_pk_bf16_f32 v178, v172, v173
	v_cvt_pk_bf16_f32 v179, v174, v175
	global_store_dwordx2 v193, v[178:179], s[28:29] offset:2048
	s_waitcnt vmcnt(31)
; #define GAS __attribute__((address_space(1)))
; __device__ __forceinline__ unsigned pk2(float lo, float hi) { const f32x2 v = {lo, hi}; return __builtin_bit_cast(unsigned, __builtin_convertvector(v, b16x2)); }
; template <int W>
; __device__ __forceinline__ void pool_item(const bf16* U, bf16* Z, int b, int t0, int g, int lane) {
;     const size_t base = (size_t)b * SEQ * D + 256 * g + 4 * lane;
;     float s[4] = {0.f, 0.f, 0.f, 0.f};
; #pragma unroll
;     for (int j = 1; j <= W; ++j) { const int t = t0 - j; if (t >= 0) { const u32x2 v = *(const GAS u32x2*)(U + base + (size_t)t * D);
;             s[0] += bf2f(v.x & 0xffffu); s[1] += bf2f(v.x >> 16); s[2] += bf2f(v.y & 0xffffu); s[3] += bf2f(v.y >> 16); } }
; #pragma unroll 8
;     for (int i = 0; i < 32; ++i) { const int t = t0 + i;
;         const u32x2 v = *(const GAS u32x2*)(U + base + (size_t)t * D);
;         const float c0 = bf2f(v.x & 0xffffu), c1 = bf2f(v.x >> 16), c2 = bf2f(v.y & 0xffffu), c3 = bf2f(v.y >> 16);
;         s[0] += c0; s[1] += c1; s[2] += c2; s[3] += c3;
;         if (t - W >= 0) { const u32x2 o = *(const GAS u32x2*)(U + base + (size_t)(t - W) * D);
;             s[0] -= bf2f(o.x & 0xffffu); s[1] -= bf2f(o.x >> 16); s[2] -= bf2f(o.y & 0xffffu); s[3] -= bf2f(o.y >> 16); }
;         const float inv = 1.0f / (float)((t + 1) < W ? (t + 1) : W);
;         u32x2 w; w.x = pk2(s[0] * inv - c0, s[1] * inv - c1); w.y = pk2(s[2] * inv - c2, s[3] * inv - c3);
;         *(GAS u32x2*)(Z + base + (size_t)t * D) = w; }
	v_lshlrev_b32_e32 v164, 16, v160
	v_and_b32_e32 v165, 0xffff0000, v160
	v_lshlrev_b32_e32 v166, 16, v161
	v_and_b32_e32 v167, 0xffff0000, v161
	v_pk_add_f32 v[184:185], v[184:185], v[164:165]
	v_pk_add_f32 v[186:187], v[186:187], v[166:167]
	v_lshlrev_b32_e32 v168, 16, v144
	v_and_b32_e32 v169, 0xffff0000, v144
	v_lshlrev_b32_e32 v170, 16, v145
	v_and_b32_e32 v171, 0xffff0000, v145
	v_pk_add_f32 v[184:185], v[184:185], v[168:169] neg_lo:[0,1] neg_hi:[0,1]
	v_pk_add_f32 v[186:187], v[186:187], v[170:171] neg_lo:[0,1] neg_hi:[0,1]
	v_pk_fma_f32 v[172:173], v[188:189], v[184:185], v[164:165] op_sel_hi:[0,1,1] neg_lo:[0,0,1] neg_hi:[0,0,1]
	v_pk_fma_f32 v[174:175], v[188:189], v[186:187], v[166:167] op_sel_hi:[0,1,1] neg_lo:[0,0,1] neg_hi:[0,0,1]
	v_cvt_pk_bf16_f32 v180, v172, v173
	v_cvt_pk_bf16_f32 v181, v174, v175
	v_add_u32_e32 v194, 0xf000, v190
	global_store_dwordx2 v194, v[180:181], s[28:29]
	s_waitcnt vmcnt(31)
	v_lshlrev_b32_e32 v164, 16, v162
	v_and_b32_e32 v165, 0xffff0000, v162
	v_lshlrev_b32_e32 v166, 16, v163
	v_and_b32_e32 v167, 0xffff0000, v163
	v_pk_add_f32 v[184:185], v[184:185], v[164:165]
	v_pk_add_f32 v[186:187], v[186:187], v[166:167]
	v_lshlrev_b32_e32 v168, 16, v146
	v_and_b32_e32 v169, 0xffff0000, v146
	v_lshlrev_b32_e32 v170, 16, v147
	v_and_b32_e32 v171, 0xffff0000, v147
	v_pk_add_f32 v[184:185], v[184:185], v[168:169] neg_lo:[0,1] neg_hi:[0,1]
	v_pk_add_f32 v[186:187], v[186:187], v[170:171] neg_lo:[0,1] neg_hi:[0,1]
	v_pk_fma_f32 v[172:173], v[188:189], v[184:185], v[164:165] op_sel_hi:[0,1,1] neg_lo:[0,0,1] neg_hi:[0,0,1]
	v_pk_fma_f32 v[174:175], v[188:189], v[186:187], v[166:167] op_sel_hi:[0,1,1] neg_lo:[0,0,1] neg_hi:[0,0,1]
	v_cvt_pk_bf16_f32 v182, v172, v173
	v_cvt_pk_bf16_f32 v183, v174, v175
	global_store_dwordx2 v194, v[182:183], s[28:29] offset:2048
	s_branch .LBB0_861
.Lpool0_w4:
	v_add_u32_e32 v192, 0x8000, v190
	global_load_dwordx2 v[100:101], v192, s[10:11]
	global_load_dwordx2 v[102:103], v192, s[10:11] offset:2048
	v_add_u32_e32 v191, 0x9000, v190
	global_load_dwordx2 v[104:105], v191, s[10:11]
	global_load_dwordx2 v[106:107], v191, s[10:11] offset:2048
	v_add_u32_e32 v192, 0xa000, v190
	global_load_dwordx2 v[108:109], v192, s[10:11]
	global_load_dwordx2 v[110:111], v192, s[10:11] offset:2048
	v_add_u32_e32 v191, 0xb000, v190
	global_load_dwordx2 v[112:113], v191, s[10:11]
	global_load_dwordx2 v[114:115], v191, s[10:11] offset:2048
	v_add_u32_e32 v192, 0xc000, v190
	global_load_dwordx2 v[116:117], v192, s[10:11]
	global_load_dwordx2 v[118:119], v192, s[10:11] offset:2048
	v_add_u32_e32 v191, 0xd000, v190
	global_load_dwordx2 v[120:121], v191, s[10:11]
	global_load_dwordx2 v[122:123], v191, s[10:11] offset:2048
	v_add_u32_e32 v192, 0xe000, v190
	global_load_dwordx2 v[124:125], v192, s[10:11]
	global_load_dwordx2 v[126:127], v192, s[10:11] offset:2048
	v_add_u32_e32 v191, 0xf000, v190
	global_load_dwordx2 v[128:129], v191, s[10:11]
	global_load_dwordx2 v[130:131], v191, s[10:11] offset:2048
	v_add_u32_e32 v192, 0x10000, v190
	global_load_dwordx2 v[132:133], v192, s[10:11]
	global_load_dwordx2 v[134:135], v192, s[10:11] offset:2048
	v_add_u32_e32 v191, 0x11000, v190
	global_load_dwordx2 v[136:137], v191, s[10:11]
	global_load_dwordx2 v[138:139], v191, s[10:11] offset:2048
	v_add_u32_e32 v192, 0x12000, v190
	global_load_dwordx2 v[140:141], v192, s[10:11]
	global_load_dwordx2 v[142:143], v192, s[10:11] offset:2048
	v_add_u32_e32 v191, 0x13000, v190
	global_load_dwordx2 v[144:145], v191, s[10:11]
	global_load_dwordx2 v[146:147], v191, s[10:11] offset:2048
	v_add_u32_e32 v192, 0x14000, v190
	global_load_dwordx2 v[148:149], v192, s[10:11]
	global_load_dwordx2 v[150:151], v192, s[10:11] offset:2048
	v_add_u32_e32 v191, 0x15000, v190
	global_load_dwordx2 v[152:153], v191, s[10:11]
	global_load_dwordx2 v[154:155], v191, s[10:11] offset:2048
	v_add_u32_e32 v192, 0x16000, v190
	global_load_dwordx2 v[156:157], v192, s[10:11]
	global_load_dwordx2 v[158:159], v192, s[10:11] offset:2048
	v_add_u32_e32 v191, 0x17000, v190
	global_load_dwordx2 v[160:161], v191, s[10:11]
	global_load_dwordx2 v[162:163], v191, s[10:11] offset:2048
	v_mov_b32_e32 v184, 0
	v_mov_b32_e32 v185, 0
	v_mov_b32_e32 v186, 0
	v_mov_b32_e32 v187, 0
	v_mov_b32_e32 v188, 0x3f800000
	s_waitcnt vmcnt(31)
	v_lshlrev_b32_e32 v164, 16, v100
	v_and_b32_e32 v165, 0xffff0000, v100
	v_lshlrev_b32_e32 v166, 16, v101
	v_and_b32_e32 v167, 0xffff0000, v101
	v_pk_add_f32 v[184:185], v[184:185], v[164:165]
	v_pk_add_f32 v[186:187], v[186:187], v[166:167]
	v_pk_fma_f32 v[172:173], v[188:189], v[184:185], v[164:165] op_sel_hi:[0,1,1] neg_lo:[0,0,1] neg_hi:[0,0,1]
	v_pk_fma_f32 v[174:175], v[188:189], v[186:187], v[166:167] op_sel_hi:[0,1,1] neg_lo:[0,0,1] neg_hi:[0,0,1]
	v_cvt_pk_bf16_f32 v176, v172, v173
	v_cvt_pk_bf16_f32 v177, v174, v175
	global_store_dwordx2 v190, v[176:177], s[28:29]
	v_mov_b32_e32 v188, 0x3f000000
	s_waitcnt vmcnt(31)
	v_lshlrev_b32_e32 v164, 16, v102
	v_and_b32_e32 v165, 0xffff0000, v102
	v_lshlrev_b32_e32 v166, 16, v103
	v_and_b32_e32 v167, 0xffff0000, v103
	v_pk_add_f32 v[184:185], v[184:185], v[164:165]
	v_pk_add_f32 v[186:187], v[186:187], v[166:167]
	v_pk_fma_f32 v[172:173], v[188:189], v[184:185], v[164:165] op_sel_hi:[0,1,1] neg_lo:[0,0,1] neg_hi:[0,0,1]
	v_pk_fma_f32 v[174:175], v[188:189], v[186:187], v[166:167] op_sel_hi:[0,1,1] neg_lo:[0,0,1] neg_hi:[0,0,1]
	v_cvt_pk_bf16_f32 v178, v172, v173
	v_cvt_pk_bf16_f32 v179, v174, v175
	global_store_dwordx2 v190, v[178:179], s[28:29] offset:2048
	v_mov_b32_e32 v188, 0x3eaaaaab
	s_waitcnt vmcnt(31)
; #define GAS __attribute__((address_space(1)))
; __device__ __forceinline__ unsigned pk2(float lo, float hi) { const f32x2 v = {lo, hi}; return __builtin_bit_cast(unsigned, __builtin_convertvector(v, b16x2)); }
; template <int W>
; __device__ __forceinline__ void pool_item(const bf16* U, bf16* Z, int b, int t0, int g, int lane) {
;     ...
; #pragma unroll 8
;     for (int i = 0; i < 32; ++i) { const int t = t0 + i;
;         const u32x2 v = *(const GAS u32x2*)(U + base + (size_t)t * D);
;         const float c0 = bf2f(v.x & 0xffffu), c1 = bf2f(v.x >> 16), c2 = bf2f(v.y & 0xffffu), c3 = bf2f(v.y >> 16);
;         s[0] += c0; s[1] += c1; s[2] += c2; s[3] += c3;
;         if (t - W >= 0) { const u32x2 o = *(const GAS u32x2*)(U + base + (size_t)(t - W) * D);
;             s[0] -= bf2f(o.x & 0xffffu); s[1] -= bf2f(o.x >> 16); s[2] -= bf2f(o.y & 0xffffu); s[3] -= bf2f(o.y >> 16); }
;         const float inv = 1.0f / (float)((t + 1) < W ? (t + 1) : W);
;         u32x2 w; w.x = pk2(s[0] * inv - c0, s[1] * inv - c1); w.y = pk2(s[2] * inv - c2, s[3] * inv - c3);
;         *(GAS u32x2*)(Z + base + (size_t)t * D) = w; }
	v_lshlrev_b32_e32 v164, 16, v104
	v_and_b32_e32 v165, 0xffff0000, v104
	v_lshlrev_b32_e32 v166, 16, v105
	v_and_b32_e32 v167, 0xffff0000, v105
	v_pk_add_f32 v[184:185], v[184:185], v[164:165]
	v_pk_add_f32 v[186:187], v[186:187], v[166:167]
	v_pk_fma_f32 v[172:173], v[188:189], v[184:185], v[164:165] op_sel_hi:[0,1,1] neg_lo:[0,0,1] neg_hi:[0,0,1]
	v_pk_fma_f32 v[174:175], v[188:189], v[186:187], v[166:167] op_sel_hi:[0,1,1] neg_lo:[0,0,1] neg_hi:[0,0,1]
	v_cvt_pk_bf16_f32 v180, v172, v173
	v_cvt_pk_bf16_f32 v181, v174, v175
	v_add_u32_e32 v194, 0x1000, v190
	global_store_dwordx2 v194, v[180:181], s[28:29]
	v_mov_b32_e32 v188, 0x3e800000
	s_waitcnt vmcnt(31)
	v_lshlrev_b32_e32 v164, 16, v106
	v_and_b32_e32 v165, 0xffff0000, v106
	v_lshlrev_b32_e32 v166, 16, v107
	v_and_b32_e32 v167, 0xffff0000, v107
	v_pk_add_f32 v[184:185], v[184:185], v[164:165]
	v_pk_add_f32 v[186:187], v[186:187], v[166:167]
	v_pk_fma_f32 v[172:173], v[188:189], v[184:185], v[164:165] op_sel_hi:[0,1,1] neg_lo:[0,0,1] neg_hi:[0,0,1]
	v_pk_fma_f32 v[174:175], v[188:189], v[186:187], v[166:167] op_sel_hi:[0,1,1] neg_lo:[0,0,1] neg_hi:[0,0,1]
	v_cvt_pk_bf16_f32 v182, v172, v173
	v_cvt_pk_bf16_f32 v183, v174, v175
	global_store_dwordx2 v194, v[182:183], s[28:29] offset:2048
	s_waitcnt vmcnt(31)
	v_lshlrev_b32_e32 v164, 16, v108
	v_and_b32_e32 v165, 0xffff0000, v108
	v_lshlrev_b32_e32 v166, 16, v109
	v_and_b32_e32 v167, 0xffff0000, v109
	v_pk_add_f32 v[184:185], v[184:185], v[164:165]
	v_pk_add_f32 v[186:187], v[186:187], v[166:167]
	v_lshlrev_b32_e32 v168, 16, v100
	v_and_b32_e32 v169, 0xffff0000, v100
	v_lshlrev_b32_e32 v170, 16, v101
	v_and_b32_e32 v171, 0xffff0000, v101
	v_pk_add_f32 v[184:185], v[184:185], v[168:169] neg_lo:[0,1] neg_hi:[0,1]
	v_pk_add_f32 v[186:187], v[186:187], v[170:171] neg_lo:[0,1] neg_hi:[0,1]
	v_pk_fma_f32 v[172:173], v[188:189], v[184:185], v[164:165] op_sel_hi:[0,1,1] neg_lo:[0,0,1] neg_hi:[0,0,1]
	v_pk_fma_f32 v[174:175], v[188:189], v[186:187], v[166:167] op_sel_hi:[0,1,1] neg_lo:[0,0,1] neg_hi:[0,0,1]
	v_cvt_pk_bf16_f32 v176, v172, v173
	v_cvt_pk_bf16_f32 v177, v174, v175
	v_add_u32_e32 v193, 0x2000, v190
	global_store_dwordx2 v193, v[176:177], s[28:29]
	s_waitcnt vmcnt(31)
	v_lshlrev_b32_e32 v164, 16, v110
	v_and_b32_e32 v165, 0xffff0000, v110
	v_lshlrev_b32_e32 v166, 16, v111
	v_and_b32_e32 v167, 0xffff0000, v111
	v_pk_add_f32 v[184:185], v[184:185], v[164:165]
	v_pk_add_f32 v[186:187], v[186:187], v[166:167]
	v_lshlrev_b32_e32 v168, 16, v102
	v_and_b32_e32 v169, 0xffff0000, v102
	v_lshlrev_b32_e32 v170, 16, v103
	v_and_b32_e32 v171, 0xffff0000, v103
	v_pk_add_f32 v[184:185], v[184:185], v[168:169] neg_lo:[0,1] neg_hi:[0,1]
	v_pk_add_f32 v[186:187], v[186:187], v[170:171] neg_lo:[0,1] neg_hi:[0,1]
	v_pk_fma_f32 v[172:173], v[188:189], v[184:185], v[164:165] op_sel_hi:[0,1,1] neg_lo:[0,0,1] neg_hi:[0,0,1]
	v_pk_fma_f32 v[174:175], v[188:189], v[186:187], v[166:167] op_sel_hi:[0,1,1] neg_lo:[0,0,1] neg_hi:[0,0,1]
	v_cvt_pk_bf16_f32 v178, v172, v173
	v_cvt_pk_bf16_f32 v179, v174, v175
	global_store_dwordx2 v193, v[178:179], s[28:29] offset:2048
	s_waitcnt vmcnt(31)
	v_lshlrev_b32_e32 v164, 16, v112
	v_and_b32_e32 v165, 0xffff0000, v112
	v_lshlrev_b32_e32 v166, 16, v113
	v_and_b32_e32 v167, 0xffff0000, v113
	v_pk_add_f32 v[184:185], v[184:185], v[164:165]
	v_pk_add_f32 v[186:187], v[186:187], v[166:167]
	v_lshlrev_b32_e32 v168, 16, v104
	v_and_b32_e32 v169, 0xffff0000, v104
	v_lshlrev_b32_e32 v170, 16, v105
	v_and_b32_e32 v171, 0xffff0000, v105
	v_pk_add_f32 v[184:185], v[184:185], v[168:169] neg_lo:[0,1] neg_hi:[0,1]
	v_pk_add_f32 v[186:187], v[186:187], v[170:171] neg_lo:[0,1] neg_hi:[0,1]
	v_pk_fma_f32 v[172:173], v[188:189], v[184:185], v[164:165] op_sel_hi:[0,1,1] neg_lo:[0,0,1] neg_hi:[0,0,1]
	v_pk_fma_f32 v[174:175], v[188:189], v[186:187], v[166:167] op_sel_hi:[0,1,1] neg_lo:[0,0,1] neg_hi:[0,0,1]
	v_cvt_pk_bf16_f32 v180, v172, v173
	v_cvt_pk_bf16_f32 v181, v174, v175
	v_add_u32_e32 v194, 0x3000, v190
	global_store_dwordx2 v194, v[180:181], s[28:29]
	s_waitcnt vmcnt(31)
	v_lshlrev_b32_e32 v164, 16, v114
	v_and_b32_e32 v165, 0xffff0000, v114
	v_lshlrev_b32_e32 v166, 16, v115
	v_and_b32_e32 v167, 0xffff0000, v115
	v_pk_add_f32 v[184:185], v[184:185], v[164:165]
	v_pk_add_f32 v[186:187], v[186:187], v[166:167]
	v_lshlrev_b32_e32 v168, 16, v106
	v_and_b32_e32 v169, 0xffff0000, v106
	v_lshlrev_b32_e32 v170, 16, v107
	v_and_b32_e32 v171, 0xffff0000, v107
	v_pk_add_f32 v[184:185], v[184:185], v[168:169] neg_lo:[0,1] neg_hi:[0,1]
	v_pk_add_f32 v[186:187], v[186:187], v[170:171] neg_lo:[0,1] neg_hi:[0,1]
	v_pk_fma_f32 v[172:173], v[188:189], v[184:185], v[164:165] op_sel_hi:[0,1,1] neg_lo:[0,0,1] neg_hi:[0,0,1]
	v_pk_fma_f32 v[174:175], v[188:189], v[186:187], v[166:167] op_sel_hi:[0,1,1] neg_lo:[0,0,1] neg_hi:[0,0,1]
	v_cvt_pk_bf16_f32 v182, v172, v173
	v_cvt_pk_bf16_f32 v183, v174, v175
	global_store_dwordx2 v194, v[182:183], s[28:29] offset:2048
	s_waitcnt vmcnt(31)
	v_lshlrev_b32_e32 v164, 16, v116
	v_and_b32_e32 v165, 0xffff0000, v116
	v_lshlrev_b32_e32 v166, 16, v117
	v_and_b32_e32 v167, 0xffff0000, v117
	v_pk_add_f32 v[184:185], v[184:185], v[164:165]
	v_pk_add_f32 v[186:187], v[186:187], v[166:167]
	v_lshlrev_b32_e32 v168, 16, v108
	v_and_b32_e32 v169, 0xffff0000, v108
	v_lshlrev_b32_e32 v170, 16, v109
	v_and_b32_e32 v171, 0xffff0000, v109
	v_pk_add_f32 v[184:185], v[184:185], v[168:169] neg_lo:[0,1] neg_hi:[0,1]
	v_pk_add_f32 v[186:187], v[186:187], v[170:171] neg_lo:[0,1] neg_hi:[0,1]
	v_pk_fma_f32 v[172:173], v[188:189], v[184:185], v[164:165] op_sel_hi:[0,1,1] neg_lo:[0,0,1] neg_hi:[0,0,1]
	v_pk_fma_f32 v[174:175], v[188:189], v[186:187], v[166:167] op_sel_hi:[0,1,1] neg_lo:[0,0,1] neg_hi:[0,0,1]
	v_cvt_pk_bf16_f32 v176, v172, v173
	v_cvt_pk_bf16_f32 v177, v174, v175
	v_add_u32_e32 v193, 0x4000, v190
	global_store_dwordx2 v193, v[176:177], s[28:29]
	s_waitcnt vmcnt(31)
; #define GAS __attribute__((address_space(1)))
; __device__ __forceinline__ unsigned pk2(float lo, float hi) { const f32x2 v = {lo, hi}; return __builtin_bit_cast(unsigned, __builtin_convertvector(v, b16x2)); }
; template <int W>
; __device__ __forceinline__ void pool_item(const bf16* U, bf16* Z, int b, int t0, int g, int lane) {
;     ...
; #pragma unroll 8
;     for (int i = 0; i < 32; ++i) { const int t = t0 + i;
;         const u32x2 v = *(const GAS u32x2*)(U + base + (size_t)t * D);
;         const float c0 = bf2f(v.x & 0xffffu), c1 = bf2f(v.x >> 16), c2 = bf2f(v.y & 0xffffu), c3 = bf2f(v.y >> 16);
;         s[0] += c0; s[1] += c1; s[2] += c2; s[3] += c3;
;         if (t - W >= 0) { const u32x2 o = *(const GAS u32x2*)(U + base + (size_t)(t - W) * D);
;             s[0] -= bf2f(o.x & 0xffffu); s[1] -= bf2f(o.x >> 16); s[2] -= bf2f(o.y & 0xffffu); s[3] -= bf2f(o.y >> 16); }
;         const float inv = 1.0f / (float)((t + 1) < W ? (t + 1) : W);
;         u32x2 w; w.x = pk2(s[0] * inv - c0, s[1] * inv - c1); w.y = pk2(s[2] * inv - c2, s[3] * inv - c3);
;         *(GAS u32x2*)(Z + base + (size_t)t * D) = w; }
	v_lshlrev_b32_e32 v164, 16, v118
	v_and_b32_e32 v165, 0xffff0000, v118
	v_lshlrev_b32_e32 v166, 16, v119
	v_and_b32_e32 v167, 0xffff0000, v119
	v_pk_add_f32 v[184:185], v[184:185], v[164:165]
	v_pk_add_f32 v[186:187], v[186:187], v[166:167]
	v_lshlrev_b32_e32 v168, 16, v110
	v_and_b32_e32 v169, 0xffff0000, v110
	v_lshlrev_b32_e32 v170, 16, v111
	v_and_b32_e32 v171, 0xffff0000, v111
	v_pk_add_f32 v[184:185], v[184:185], v[168:169] neg_lo:[0,1] neg_hi:[0,1]
	v_pk_add_f32 v[186:187], v[186:187], v[170:171] neg_lo:[0,1] neg_hi:[0,1]
	v_pk_fma_f32 v[172:173], v[188:189], v[184:185], v[164:165] op_sel_hi:[0,1,1] neg_lo:[0,0,1] neg_hi:[0,0,1]
	v_pk_fma_f32 v[174:175], v[188:189], v[186:187], v[166:167] op_sel_hi:[0,1,1] neg_lo:[0,0,1] neg_hi:[0,0,1]
	v_cvt_pk_bf16_f32 v178, v172, v173
	v_cvt_pk_bf16_f32 v179, v174, v175
	global_store_dwordx2 v193, v[178:179], s[28:29] offset:2048
	s_waitcnt vmcnt(31)
	v_lshlrev_b32_e32 v164, 16, v120
	v_and_b32_e32 v165, 0xffff0000, v120
	v_lshlrev_b32_e32 v166, 16, v121
	v_and_b32_e32 v167, 0xffff0000, v121
	v_pk_add_f32 v[184:185], v[184:185], v[164:165]
	v_pk_add_f32 v[186:187], v[186:187], v[166:167]
	v_lshlrev_b32_e32 v168, 16, v112
	v_and_b32_e32 v169, 0xffff0000, v112
	v_lshlrev_b32_e32 v170, 16, v113
	v_and_b32_e32 v171, 0xffff0000, v113
	v_pk_add_f32 v[184:185], v[184:185], v[168:169] neg_lo:[0,1] neg_hi:[0,1]
	v_pk_add_f32 v[186:187], v[186:187], v[170:171] neg_lo:[0,1] neg_hi:[0,1]
	v_pk_fma_f32 v[172:173], v[188:189], v[184:185], v[164:165] op_sel_hi:[0,1,1] neg_lo:[0,0,1] neg_hi:[0,0,1]
	v_pk_fma_f32 v[174:175], v[188:189], v[186:187], v[166:167] op_sel_hi:[0,1,1] neg_lo:[0,0,1] neg_hi:[0,0,1]
	v_cvt_pk_bf16_f32 v180, v172, v173
	v_cvt_pk_bf16_f32 v181, v174, v175
	v_add_u32_e32 v194, 0x5000, v190
	global_store_dwordx2 v194, v[180:181], s[28:29]
	s_waitcnt vmcnt(31)
	v_lshlrev_b32_e32 v164, 16, v122
	v_and_b32_e32 v165, 0xffff0000, v122
	v_lshlrev_b32_e32 v166, 16, v123
	v_and_b32_e32 v167, 0xffff0000, v123
	v_pk_add_f32 v[184:185], v[184:185], v[164:165]
	v_pk_add_f32 v[186:187], v[186:187], v[166:167]
	v_lshlrev_b32_e32 v168, 16, v114
	v_and_b32_e32 v169, 0xffff0000, v114
	v_lshlrev_b32_e32 v170, 16, v115
	v_and_b32_e32 v171, 0xffff0000, v115
	v_pk_add_f32 v[184:185], v[184:185], v[168:169] neg_lo:[0,1] neg_hi:[0,1]
	v_pk_add_f32 v[186:187], v[186:187], v[170:171] neg_lo:[0,1] neg_hi:[0,1]
	v_pk_fma_f32 v[172:173], v[188:189], v[184:185], v[164:165] op_sel_hi:[0,1,1] neg_lo:[0,0,1] neg_hi:[0,0,1]
	v_pk_fma_f32 v[174:175], v[188:189], v[186:187], v[166:167] op_sel_hi:[0,1,1] neg_lo:[0,0,1] neg_hi:[0,0,1]
	v_cvt_pk_bf16_f32 v182, v172, v173
	v_cvt_pk_bf16_f32 v183, v174, v175
	global_store_dwordx2 v194, v[182:183], s[28:29] offset:2048
	s_waitcnt vmcnt(31)
	v_lshlrev_b32_e32 v164, 16, v124
	v_and_b32_e32 v165, 0xffff0000, v124
	v_lshlrev_b32_e32 v166, 16, v125
	v_and_b32_e32 v167, 0xffff0000, v125
	v_pk_add_f32 v[184:185], v[184:185], v[164:165]
	v_pk_add_f32 v[186:187], v[186:187], v[166:167]
	v_lshlrev_b32_e32 v168, 16, v116
	v_and_b32_e32 v169, 0xffff0000, v116
	v_lshlrev_b32_e32 v170, 16, v117
	v_and_b32_e32 v171, 0xffff0000, v117
	v_pk_add_f32 v[184:185], v[184:185], v[168:169] neg_lo:[0,1] neg_hi:[0,1]
	v_pk_add_f32 v[186:187], v[186:187], v[170:171] neg_lo:[0,1] neg_hi:[0,1]
	v_pk_fma_f32 v[172:173], v[188:189], v[184:185], v[164:165] op_sel_hi:[0,1,1] neg_lo:[0,0,1] neg_hi:[0,0,1]
	v_pk_fma_f32 v[174:175], v[188:189], v[186:187], v[166:167] op_sel_hi:[0,1,1] neg_lo:[0,0,1] neg_hi:[0,0,1]
	v_cvt_pk_bf16_f32 v176, v172, v173
	v_cvt_pk_bf16_f32 v177, v174, v175
	v_add_u32_e32 v193, 0x6000, v190
	global_store_dwordx2 v193, v[176:177], s[28:29]
	s_waitcnt vmcnt(31)
	v_lshlrev_b32_e32 v164, 16, v126
	v_and_b32_e32 v165, 0xffff0000, v126
	v_lshlrev_b32_e32 v166, 16, v127
	v_and_b32_e32 v167, 0xffff0000, v127
	v_pk_add_f32 v[184:185], v[184:185], v[164:165]
	v_pk_add_f32 v[186:187], v[186:187], v[166:167]
	v_lshlrev_b32_e32 v168, 16, v118
	v_and_b32_e32 v169, 0xffff0000, v118
	v_lshlrev_b32_e32 v170, 16, v119
	v_and_b32_e32 v171, 0xffff0000, v119
	v_pk_add_f32 v[184:185], v[184:185], v[168:169] neg_lo:[0,1] neg_hi:[0,1]
	v_pk_add_f32 v[186:187], v[186:187], v[170:171] neg_lo:[0,1] neg_hi:[0,1]
	v_pk_fma_f32 v[172:173], v[188:189], v[184:185], v[164:165] op_sel_hi:[0,1,1] neg_lo:[0,0,1] neg_hi:[0,0,1]
	v_pk_fma_f32 v[174:175], v[188:189], v[186:187], v[166:167] op_sel_hi:[0,1,1] neg_lo:[0,0,1] neg_hi:[0,0,1]
	v_cvt_pk_bf16_f32 v178, v172, v173
	v_cvt_pk_bf16_f32 v179, v174, v175
	global_store_dwordx2 v193, v[178:179], s[28:29] offset:2048
	s_waitcnt vmcnt(31)
	v_lshlrev_b32_e32 v164, 16, v128
	v_and_b32_e32 v165, 0xffff0000, v128
	v_lshlrev_b32_e32 v166, 16, v129
	v_and_b32_e32 v167, 0xffff0000, v129
	v_pk_add_f32 v[184:185], v[184:185], v[164:165]
	v_pk_add_f32 v[186:187], v[186:187], v[166:167]
	v_lshlrev_b32_e32 v168, 16, v120
	v_and_b32_e32 v169, 0xffff0000, v120
	v_lshlrev_b32_e32 v170, 16, v121
	v_and_b32_e32 v171, 0xffff0000, v121
	v_pk_add_f32 v[184:185], v[184:185], v[168:169] neg_lo:[0,1] neg_hi:[0,1]
	v_pk_add_f32 v[186:187], v[186:187], v[170:171] neg_lo:[0,1] neg_hi:[0,1]
	v_pk_fma_f32 v[172:173], v[188:189], v[184:185], v[164:165] op_sel_hi:[0,1,1] neg_lo:[0,0,1] neg_hi:[0,0,1]
	v_pk_fma_f32 v[174:175], v[188:189], v[186:187], v[166:167] op_sel_hi:[0,1,1] neg_lo:[0,0,1] neg_hi:[0,0,1]
	v_cvt_pk_bf16_f32 v180, v172, v173
	v_cvt_pk_bf16_f32 v181, v174, v175
	v_add_u32_e32 v194, 0x7000, v190
	global_store_dwordx2 v194, v[180:181], s[28:29]
	s_waitcnt vmcnt(31)
; #define GAS __attribute__((address_space(1)))
; __device__ __forceinline__ unsigned pk2(float lo, float hi) { const f32x2 v = {lo, hi}; return __builtin_bit_cast(unsigned, __builtin_convertvector(v, b16x2)); }
; template <int W>
; __device__ __forceinline__ void pool_item(const bf16* U, bf16* Z, int b, int t0, int g, int lane) {
;     ...
; #pragma unroll 8
;     for (int i = 0; i < 32; ++i) { const int t = t0 + i;
;         const u32x2 v = *(const GAS u32x2*)(U + base + (size_t)t * D);
;         const float c0 = bf2f(v.x & 0xffffu), c1 = bf2f(v.x >> 16), c2 = bf2f(v.y & 0xffffu), c3 = bf2f(v.y >> 16);
;         s[0] += c0; s[1] += c1; s[2] += c2; s[3] += c3;
;         if (t - W >= 0) { const u32x2 o = *(const GAS u32x2*)(U + base + (size_t)(t - W) * D);
;             s[0] -= bf2f(o.x & 0xffffu); s[1] -= bf2f(o.x >> 16); s[2] -= bf2f(o.y & 0xffffu); s[3] -= bf2f(o.y >> 16); }
;         const float inv = 1.0f / (float)((t + 1) < W ? (t + 1) : W);
;         u32x2 w; w.x = pk2(s[0] * inv - c0, s[1] * inv - c1); w.y = pk2(s[2] * inv - c2, s[3] * inv - c3);
;         *(GAS u32x2*)(Z + base + (size_t)t * D) = w; }
	v_lshlrev_b32_e32 v164, 16, v130
	v_and_b32_e32 v165, 0xffff0000, v130
	v_lshlrev_b32_e32 v166, 16, v131
	v_and_b32_e32 v167, 0xffff0000, v131
	v_pk_add_f32 v[184:185], v[184:185], v[164:165]
	v_pk_add_f32 v[186:187], v[186:187], v[166:167]
	v_lshlrev_b32_e32 v168, 16, v122
	v_and_b32_e32 v169, 0xffff0000, v122
	v_lshlrev_b32_e32 v170, 16, v123
	v_and_b32_e32 v171, 0xffff0000, v123
	v_pk_add_f32 v[184:185], v[184:185], v[168:169] neg_lo:[0,1] neg_hi:[0,1]
	v_pk_add_f32 v[186:187], v[186:187], v[170:171] neg_lo:[0,1] neg_hi:[0,1]
	v_pk_fma_f32 v[172:173], v[188:189], v[184:185], v[164:165] op_sel_hi:[0,1,1] neg_lo:[0,0,1] neg_hi:[0,0,1]
	v_pk_fma_f32 v[174:175], v[188:189], v[186:187], v[166:167] op_sel_hi:[0,1,1] neg_lo:[0,0,1] neg_hi:[0,0,1]
	v_cvt_pk_bf16_f32 v182, v172, v173
	v_cvt_pk_bf16_f32 v183, v174, v175
	global_store_dwordx2 v194, v[182:183], s[28:29] offset:2048
	s_waitcnt vmcnt(31)
	v_lshlrev_b32_e32 v164, 16, v132
	v_and_b32_e32 v165, 0xffff0000, v132
	v_lshlrev_b32_e32 v166, 16, v133
	v_and_b32_e32 v167, 0xffff0000, v133
	v_pk_add_f32 v[184:185], v[184:185], v[164:165]
	v_pk_add_f32 v[186:187], v[186:187], v[166:167]
	v_lshlrev_b32_e32 v168, 16, v124
	v_and_b32_e32 v169, 0xffff0000, v124
	v_lshlrev_b32_e32 v170, 16, v125
	v_and_b32_e32 v171, 0xffff0000, v125
	v_pk_add_f32 v[184:185], v[184:185], v[168:169] neg_lo:[0,1] neg_hi:[0,1]
	v_pk_add_f32 v[186:187], v[186:187], v[170:171] neg_lo:[0,1] neg_hi:[0,1]
	v_pk_fma_f32 v[172:173], v[188:189], v[184:185], v[164:165] op_sel_hi:[0,1,1] neg_lo:[0,0,1] neg_hi:[0,0,1]
	v_pk_fma_f32 v[174:175], v[188:189], v[186:187], v[166:167] op_sel_hi:[0,1,1] neg_lo:[0,0,1] neg_hi:[0,0,1]
	v_cvt_pk_bf16_f32 v176, v172, v173
	v_cvt_pk_bf16_f32 v177, v174, v175
	v_add_u32_e32 v193, 0x8000, v190
	global_store_dwordx2 v193, v[176:177], s[28:29]
	s_waitcnt vmcnt(31)
	v_lshlrev_b32_e32 v164, 16, v134
	v_and_b32_e32 v165, 0xffff0000, v134
	v_lshlrev_b32_e32 v166, 16, v135
	v_and_b32_e32 v167, 0xffff0000, v135
	v_pk_add_f32 v[184:185], v[184:185], v[164:165]
	v_pk_add_f32 v[186:187], v[186:187], v[166:167]
	v_lshlrev_b32_e32 v168, 16, v126
	v_and_b32_e32 v169, 0xffff0000, v126
	v_lshlrev_b32_e32 v170, 16, v127
	v_and_b32_e32 v171, 0xffff0000, v127
	v_pk_add_f32 v[184:185], v[184:185], v[168:169] neg_lo:[0,1] neg_hi:[0,1]
	v_pk_add_f32 v[186:187], v[186:187], v[170:171] neg_lo:[0,1] neg_hi:[0,1]
	v_pk_fma_f32 v[172:173], v[188:189], v[184:185], v[164:165] op_sel_hi:[0,1,1] neg_lo:[0,0,1] neg_hi:[0,0,1]
	v_pk_fma_f32 v[174:175], v[188:189], v[186:187], v[166:167] op_sel_hi:[0,1,1] neg_lo:[0,0,1] neg_hi:[0,0,1]
	v_cvt_pk_bf16_f32 v178, v172, v173
	v_cvt_pk_bf16_f32 v179, v174, v175
	global_store_dwordx2 v193, v[178:179], s[28:29] offset:2048
	s_waitcnt vmcnt(31)
	v_lshlrev_b32_e32 v164, 16, v136
	v_and_b32_e32 v165, 0xffff0000, v136
	v_lshlrev_b32_e32 v166, 16, v137
	v_and_b32_e32 v167, 0xffff0000, v137
	v_pk_add_f32 v[184:185], v[184:185], v[164:165]
	v_pk_add_f32 v[186:187], v[186:187], v[166:167]
	v_lshlrev_b32_e32 v168, 16, v128
	v_and_b32_e32 v169, 0xffff0000, v128
	v_lshlrev_b32_e32 v170, 16, v129
	v_and_b32_e32 v171, 0xffff0000, v129
	v_pk_add_f32 v[184:185], v[184:185], v[168:169] neg_lo:[0,1] neg_hi:[0,1]
	v_pk_add_f32 v[186:187], v[186:187], v[170:171] neg_lo:[0,1] neg_hi:[0,1]
	v_pk_fma_f32 v[172:173], v[188:189], v[184:185], v[164:165] op_sel_hi:[0,1,1] neg_lo:[0,0,1] neg_hi:[0,0,1]
	v_pk_fma_f32 v[174:175], v[188:189], v[186:187], v[166:167] op_sel_hi:[0,1,1] neg_lo:[0,0,1] neg_hi:[0,0,1]
	v_cvt_pk_bf16_f32 v180, v172, v173
	v_cvt_pk_bf16_f32 v181, v174, v175
	v_add_u32_e32 v194, 0x9000, v190
	global_store_dwordx2 v194, v[180:181], s[28:29]
	s_waitcnt vmcnt(31)
	v_lshlrev_b32_e32 v164, 16, v138
	v_and_b32_e32 v165, 0xffff0000, v138
	v_lshlrev_b32_e32 v166, 16, v139
	v_and_b32_e32 v167, 0xffff0000, v139
	v_pk_add_f32 v[184:185], v[184:185], v[164:165]
	v_pk_add_f32 v[186:187], v[186:187], v[166:167]
	v_lshlrev_b32_e32 v168, 16, v130
	v_and_b32_e32 v169, 0xffff0000, v130
	v_lshlrev_b32_e32 v170, 16, v131
	v_and_b32_e32 v171, 0xffff0000, v131
	v_pk_add_f32 v[184:185], v[184:185], v[168:169] neg_lo:[0,1] neg_hi:[0,1]
	v_pk_add_f32 v[186:187], v[186:187], v[170:171] neg_lo:[0,1] neg_hi:[0,1]
	v_pk_fma_f32 v[172:173], v[188:189], v[184:185], v[164:165] op_sel_hi:[0,1,1] neg_lo:[0,0,1] neg_hi:[0,0,1]
	v_pk_fma_f32 v[174:175], v[188:189], v[186:187], v[166:167] op_sel_hi:[0,1,1] neg_lo:[0,0,1] neg_hi:[0,0,1]
	v_cvt_pk_bf16_f32 v182, v172, v173
	v_cvt_pk_bf16_f32 v183, v174, v175
	global_store_dwordx2 v194, v[182:183], s[28:29] offset:2048
	s_waitcnt vmcnt(31)
	v_lshlrev_b32_e32 v164, 16, v140
	v_and_b32_e32 v165, 0xffff0000, v140
	v_lshlrev_b32_e32 v166, 16, v141
	v_and_b32_e32 v167, 0xffff0000, v141
	v_pk_add_f32 v[184:185], v[184:185], v[164:165]
	v_pk_add_f32 v[186:187], v[186:187], v[166:167]
	v_lshlrev_b32_e32 v168, 16, v132
	v_and_b32_e32 v169, 0xffff0000, v132
	v_lshlrev_b32_e32 v170, 16, v133
	v_and_b32_e32 v171, 0xffff0000, v133
	v_pk_add_f32 v[184:185], v[184:185], v[168:169] neg_lo:[0,1] neg_hi:[0,1]
	v_pk_add_f32 v[186:187], v[186:187], v[170:171] neg_lo:[0,1] neg_hi:[0,1]
	v_pk_fma_f32 v[172:173], v[188:189], v[184:185], v[164:165] op_sel_hi:[0,1,1] neg_lo:[0,0,1] neg_hi:[0,0,1]
	v_pk_fma_f32 v[174:175], v[188:189], v[186:187], v[166:167] op_sel_hi:[0,1,1] neg_lo:[0,0,1] neg_hi:[0,0,1]
	v_cvt_pk_bf16_f32 v176, v172, v173
	v_cvt_pk_bf16_f32 v177, v174, v175
	v_add_u32_e32 v193, 0xa000, v190
	global_store_dwordx2 v193, v[176:177], s[28:29]
	s_waitcnt vmcnt(31)
; #define GAS __attribute__((address_space(1)))
; __device__ __forceinline__ unsigned pk2(float lo, float hi) { const f32x2 v = {lo, hi}; return __builtin_bit_cast(unsigned, __builtin_convertvector(v, b16x2)); }
; template <int W>
; __device__ __forceinline__ void pool_item(const bf16* U, bf16* Z, int b, int t0, int g, int lane) {
;     ...
; #pragma unroll 8
;     for (int i = 0; i < 32; ++i) { const int t = t0 + i;
;         const u32x2 v = *(const GAS u32x2*)(U + base + (size_t)t * D);
;         const float c0 = bf2f(v.x & 0xffffu), c1 = bf2f(v.x >> 16), c2 = bf2f(v.y & 0xffffu), c3 = bf2f(v.y >> 16);
;         s[0] += c0; s[1] += c1; s[2] += c2; s[3] += c3;
;         if (t - W >= 0) { const u32x2 o = *(const GAS u32x2*)(U + base + (size_t)(t - W) * D);
;             s[0] -= bf2f(o.x & 0xffffu); s[1] -= bf2f(o.x >> 16); s[2] -= bf2f(o.y & 0xffffu); s[3] -= bf2f(o.y >> 16); }
;         const float inv = 1.0f / (float)((t + 1) < W ? (t + 1) : W);
;         u32x2 w; w.x = pk2(s[0] * inv - c0, s[1] * inv - c1); w.y = pk2(s[2] * inv - c2, s[3] * inv - c3);
;         *(GAS u32x2*)(Z + base + (size_t)t * D) = w; }
	v_lshlrev_b32_e32 v164, 16, v142
	v_and_b32_e32 v165, 0xffff0000, v142
	v_lshlrev_b32_e32 v166, 16, v143
	v_and_b32_e32 v167, 0xffff0000, v143
	v_pk_add_f32 v[184:185], v[184:185], v[164:165]
	v_pk_add_f32 v[186:187], v[186:187], v[166:167]
	v_lshlrev_b32_e32 v168, 16, v134
	v_and_b32_e32 v169, 0xffff0000, v134
	v_lshlrev_b32_e32 v170, 16, v135
	v_and_b32_e32 v171, 0xffff0000, v135
	v_pk_add_f32 v[184:185], v[184:185], v[168:169] neg_lo:[0,1] neg_hi:[0,1]
	v_pk_add_f32 v[186:187], v[186:187], v[170:171] neg_lo:[0,1] neg_hi:[0,1]
	v_pk_fma_f32 v[172:173], v[188:189], v[184:185], v[164:165] op_sel_hi:[0,1,1] neg_lo:[0,0,1] neg_hi:[0,0,1]
	v_pk_fma_f32 v[174:175], v[188:189], v[186:187], v[166:167] op_sel_hi:[0,1,1] neg_lo:[0,0,1] neg_hi:[0,0,1]
	v_cvt_pk_bf16_f32 v178, v172, v173
	v_cvt_pk_bf16_f32 v179, v174, v175
	global_store_dwordx2 v193, v[178:179], s[28:29] offset:2048
	s_waitcnt vmcnt(31)
	v_lshlrev_b32_e32 v164, 16, v144
	v_and_b32_e32 v165, 0xffff0000, v144
	v_lshlrev_b32_e32 v166, 16, v145
	v_and_b32_e32 v167, 0xffff0000, v145
	v_pk_add_f32 v[184:185], v[184:185], v[164:165]
	v_pk_add_f32 v[186:187], v[186:187], v[166:167]
	v_lshlrev_b32_e32 v168, 16, v136
	v_and_b32_e32 v169, 0xffff0000, v136
	v_lshlrev_b32_e32 v170, 16, v137
	v_and_b32_e32 v171, 0xffff0000, v137
	v_pk_add_f32 v[184:185], v[184:185], v[168:169] neg_lo:[0,1] neg_hi:[0,1]
	v_pk_add_f32 v[186:187], v[186:187], v[170:171] neg_lo:[0,1] neg_hi:[0,1]
	v_pk_fma_f32 v[172:173], v[188:189], v[184:185], v[164:165] op_sel_hi:[0,1,1] neg_lo:[0,0,1] neg_hi:[0,0,1]
	v_pk_fma_f32 v[174:175], v[188:189], v[186:187], v[166:167] op_sel_hi:[0,1,1] neg_lo:[0,0,1] neg_hi:[0,0,1]
	v_cvt_pk_bf16_f32 v180, v172, v173
	v_cvt_pk_bf16_f32 v181, v174, v175
	v_add_u32_e32 v194, 0xb000, v190
	global_store_dwordx2 v194, v[180:181], s[28:29]
	s_waitcnt vmcnt(31)
	v_lshlrev_b32_e32 v164, 16, v146
	v_and_b32_e32 v165, 0xffff0000, v146
	v_lshlrev_b32_e32 v166, 16, v147
	v_and_b32_e32 v167, 0xffff0000, v147
	v_pk_add_f32 v[184:185], v[184:185], v[164:165]
	v_pk_add_f32 v[186:187], v[186:187], v[166:167]
	v_lshlrev_b32_e32 v168, 16, v138
	v_and_b32_e32 v169, 0xffff0000, v138
	v_lshlrev_b32_e32 v170, 16, v139
	v_and_b32_e32 v171, 0xffff0000, v139
	v_pk_add_f32 v[184:185], v[184:185], v[168:169] neg_lo:[0,1] neg_hi:[0,1]
	v_pk_add_f32 v[186:187], v[186:187], v[170:171] neg_lo:[0,1] neg_hi:[0,1]
	v_pk_fma_f32 v[172:173], v[188:189], v[184:185], v[164:165] op_sel_hi:[0,1,1] neg_lo:[0,0,1] neg_hi:[0,0,1]
	v_pk_fma_f32 v[174:175], v[188:189], v[186:187], v[166:167] op_sel_hi:[0,1,1] neg_lo:[0,0,1] neg_hi:[0,0,1]
	v_cvt_pk_bf16_f32 v182, v172, v173
	v_cvt_pk_bf16_f32 v183, v174, v175
	global_store_dwordx2 v194, v[182:183], s[28:29] offset:2048
	s_waitcnt vmcnt(31)
	v_lshlrev_b32_e32 v164, 16, v148
	v_and_b32_e32 v165, 0xffff0000, v148
	v_lshlrev_b32_e32 v166, 16, v149
	v_and_b32_e32 v167, 0xffff0000, v149
	v_pk_add_f32 v[184:185], v[184:185], v[164:165]
	v_pk_add_f32 v[186:187], v[186:187], v[166:167]
	v_lshlrev_b32_e32 v168, 16, v140
	v_and_b32_e32 v169, 0xffff0000, v140
	v_lshlrev_b32_e32 v170, 16, v141
	v_and_b32_e32 v171, 0xffff0000, v141
	v_pk_add_f32 v[184:185], v[184:185], v[168:169] neg_lo:[0,1] neg_hi:[0,1]
	v_pk_add_f32 v[186:187], v[186:187], v[170:171] neg_lo:[0,1] neg_hi:[0,1]
	v_pk_fma_f32 v[172:173], v[188:189], v[184:185], v[164:165] op_sel_hi:[0,1,1] neg_lo:[0,0,1] neg_hi:[0,0,1]
	v_pk_fma_f32 v[174:175], v[188:189], v[186:187], v[166:167] op_sel_hi:[0,1,1] neg_lo:[0,0,1] neg_hi:[0,0,1]
	v_cvt_pk_bf16_f32 v176, v172, v173
	v_cvt_pk_bf16_f32 v177, v174, v175
	v_add_u32_e32 v193, 0xc000, v190
	global_store_dwordx2 v193, v[176:177], s[28:29]
	s_waitcnt vmcnt(31)
	v_lshlrev_b32_e32 v164, 16, v150
	v_and_b32_e32 v165, 0xffff0000, v150
	v_lshlrev_b32_e32 v166, 16, v151
	v_and_b32_e32 v167, 0xffff0000, v151
	v_pk_add_f32 v[184:185], v[184:185], v[164:165]
	v_pk_add_f32 v[186:187], v[186:187], v[166:167]
	v_lshlrev_b32_e32 v168, 16, v142
	v_and_b32_e32 v169, 0xffff0000, v142
	v_lshlrev_b32_e32 v170, 16, v143
	v_and_b32_e32 v171, 0xffff0000, v143
	v_pk_add_f32 v[184:185], v[184:185], v[168:169] neg_lo:[0,1] neg_hi:[0,1]
	v_pk_add_f32 v[186:187], v[186:187], v[170:171] neg_lo:[0,1] neg_hi:[0,1]
	v_pk_fma_f32 v[172:173], v[188:189], v[184:185], v[164:165] op_sel_hi:[0,1,1] neg_lo:[0,0,1] neg_hi:[0,0,1]
	v_pk_fma_f32 v[174:175], v[188:189], v[186:187], v[166:167] op_sel_hi:[0,1,1] neg_lo:[0,0,1] neg_hi:[0,0,1]
	v_cvt_pk_bf16_f32 v178, v172, v173
	v_cvt_pk_bf16_f32 v179, v174, v175
	global_store_dwordx2 v193, v[178:179], s[28:29] offset:2048
	s_waitcnt vmcnt(31)
	v_lshlrev_b32_e32 v164, 16, v152
	v_and_b32_e32 v165, 0xffff0000, v152
	v_lshlrev_b32_e32 v166, 16, v153
	v_and_b32_e32 v167, 0xffff0000, v153
	v_pk_add_f32 v[184:185], v[184:185], v[164:165]
	v_pk_add_f32 v[186:187], v[186:187], v[166:167]
	v_lshlrev_b32_e32 v168, 16, v144
	v_and_b32_e32 v169, 0xffff0000, v144
	v_lshlrev_b32_e32 v170, 16, v145
	v_and_b32_e32 v171, 0xffff0000, v145
	v_pk_add_f32 v[184:185], v[184:185], v[168:169] neg_lo:[0,1] neg_hi:[0,1]
	v_pk_add_f32 v[186:187], v[186:187], v[170:171] neg_lo:[0,1] neg_hi:[0,1]
	v_pk_fma_f32 v[172:173], v[188:189], v[184:185], v[164:165] op_sel_hi:[0,1,1] neg_lo:[0,0,1] neg_hi:[0,0,1]
	v_pk_fma_f32 v[174:175], v[188:189], v[186:187], v[166:167] op_sel_hi:[0,1,1] neg_lo:[0,0,1] neg_hi:[0,0,1]
	v_cvt_pk_bf16_f32 v180, v172, v173
	v_cvt_pk_bf16_f32 v181, v174, v175
	v_add_u32_e32 v194, 0xd000, v190
	global_store_dwordx2 v194, v[180:181], s[28:29]
	s_waitcnt vmcnt(31)
; #define GAS __attribute__((address_space(1)))
; __device__ __forceinline__ unsigned pk2(float lo, float hi) { const f32x2 v = {lo, hi}; return __builtin_bit_cast(unsigned, __builtin_convertvector(v, b16x2)); }
; template <int W>
; __device__ __forceinline__ void pool_item(const bf16* U, bf16* Z, int b, int t0, int g, int lane) {
;     ...
; #pragma unroll 8
;     for (int i = 0; i < 32; ++i) { const int t = t0 + i;
;         const u32x2 v = *(const GAS u32x2*)(U + base + (size_t)t * D);
;         const float c0 = bf2f(v.x & 0xffffu), c1 = bf2f(v.x >> 16), c2 = bf2f(v.y & 0xffffu), c3 = bf2f(v.y >> 16);
;         s[0] += c0; s[1] += c1; s[2] += c2; s[3] += c3;
;         if (t - W >= 0) { const u32x2 o = *(const GAS u32x2*)(U + base + (size_t)(t - W) * D);
;             s[0] -= bf2f(o.x & 0xffffu); s[1] -= bf2f(o.x >> 16); s[2] -= bf2f(o.y & 0xffffu); s[3] -= bf2f(o.y >> 16); }
;         const float inv = 1.0f / (float)((t + 1) < W ? (t + 1) : W);
;         u32x2 w; w.x = pk2(s[0] * inv - c0, s[1] * inv - c1); w.y = pk2(s[2] * inv - c2, s[3] * inv - c3);
;         *(GAS u32x2*)(Z + base + (size_t)t * D) = w; }
	v_lshlrev_b32_e32 v164, 16, v154
	v_and_b32_e32 v165, 0xffff0000, v154
	v_lshlrev_b32_e32 v166, 16, v155
	v_and_b32_e32 v167, 0xffff0000, v155
	v_pk_add_f32 v[184:185], v[184:185], v[164:165]
	v_pk_add_f32 v[186:187], v[186:187], v[166:167]
	v_lshlrev_b32_e32 v168, 16, v146
	v_and_b32_e32 v169, 0xffff0000, v146
	v_lshlrev_b32_e32 v170, 16, v147
	v_and_b32_e32 v171, 0xffff0000, v147
	v_pk_add_f32 v[184:185], v[184:185], v[168:169] neg_lo:[0,1] neg_hi:[0,1]
	v_pk_add_f32 v[186:187], v[186:187], v[170:171] neg_lo:[0,1] neg_hi:[0,1]
	v_pk_fma_f32 v[172:173], v[188:189], v[184:185], v[164:165] op_sel_hi:[0,1,1] neg_lo:[0,0,1] neg_hi:[0,0,1]
	v_pk_fma_f32 v[174:175], v[188:189], v[186:187], v[166:167] op_sel_hi:[0,1,1] neg_lo:[0,0,1] neg_hi:[0,0,1]
	v_cvt_pk_bf16_f32 v182, v172, v173
	v_cvt_pk_bf16_f32 v183, v174, v175
	global_store_dwordx2 v194, v[182:183], s[28:29] offset:2048
	s_waitcnt vmcnt(31)
	v_lshlrev_b32_e32 v164, 16, v156
	v_and_b32_e32 v165, 0xffff0000, v156
	v_lshlrev_b32_e32 v166, 16, v157
	v_and_b32_e32 v167, 0xffff0000, v157
	v_pk_add_f32 v[184:185], v[184:185], v[164:165]
	v_pk_add_f32 v[186:187], v[186:187], v[166:167]
	v_lshlrev_b32_e32 v168, 16, v148
	v_and_b32_e32 v169, 0xffff0000, v148
	v_lshlrev_b32_e32 v170, 16, v149
	v_and_b32_e32 v171, 0xffff0000, v149
	v_pk_add_f32 v[184:185], v[184:185], v[168:169] neg_lo:[0,1] neg_hi:[0,1]
	v_pk_add_f32 v[186:187], v[186:187], v[170:171] neg_lo:[0,1] neg_hi:[0,1]
	v_pk_fma_f32 v[172:173], v[188:189], v[184:185], v[164:165] op_sel_hi:[0,1,1] neg_lo:[0,0,1] neg_hi:[0,0,1]
	v_pk_fma_f32 v[174:175], v[188:189], v[186:187], v[166:167] op_sel_hi:[0,1,1] neg_lo:[0,0,1] neg_hi:[0,0,1]
	v_cvt_pk_bf16_f32 v176, v172, v173
	v_cvt_pk_bf16_f32 v177, v174, v175
	v_add_u32_e32 v193, 0xe000, v190
	global_store_dwordx2 v193, v[176:177], s[28:29]
	s_waitcnt vmcnt(31)
	v_lshlrev_b32_e32 v164, 16, v158
	v_and_b32_e32 v165, 0xffff0000, v158
	v_lshlrev_b32_e32 v166, 16, v159
	v_and_b32_e32 v167, 0xffff0000, v159
	v_pk_add_f32 v[184:185], v[184:185], v[164:165]
	v_pk_add_f32 v[186:187], v[186:187], v[166:167]
	v_lshlrev_b32_e32 v168, 16, v150
	v_and_b32_e32 v169, 0xffff0000, v150
	v_lshlrev_b32_e32 v170, 16, v151
	v_and_b32_e32 v171, 0xffff0000, v151
	v_pk_add_f32 v[184:185], v[184:185], v[168:169] neg_lo:[0,1] neg_hi:[0,1]
	v_pk_add_f32 v[186:187], v[186:187], v[170:171] neg_lo:[0,1] neg_hi:[0,1]
	v_pk_fma_f32 v[172:173], v[188:189], v[184:185], v[164:165] op_sel_hi:[0,1,1] neg_lo:[0,0,1] neg_hi:[0,0,1]
	v_pk_fma_f32 v[174:175], v[188:189], v[186:187], v[166:167] op_sel_hi:[0,1,1] neg_lo:[0,0,1] neg_hi:[0,0,1]
	v_cvt_pk_bf16_f32 v178, v172, v173
	v_cvt_pk_bf16_f32 v179, v174, v175
	global_store_dwordx2 v193, v[178:179], s[28:29] offset:2048
	s_waitcnt vmcnt(31)
	v_lshlrev_b32_e32 v164, 16, v160
	v_and_b32_e32 v165, 0xffff0000, v160
	v_lshlrev_b32_e32 v166, 16, v161
	v_and_b32_e32 v167, 0xffff0000, v161
	v_pk_add_f32 v[184:185], v[184:185], v[164:165]
	v_pk_add_f32 v[186:187], v[186:187], v[166:167]
	v_lshlrev_b32_e32 v168, 16, v152
	v_and_b32_e32 v169, 0xffff0000, v152
	v_lshlrev_b32_e32 v170, 16, v153
	v_and_b32_e32 v171, 0xffff0000, v153
	v_pk_add_f32 v[184:185], v[184:185], v[168:169] neg_lo:[0,1] neg_hi:[0,1]
	v_pk_add_f32 v[186:187], v[186:187], v[170:171] neg_lo:[0,1] neg_hi:[0,1]
	v_pk_fma_f32 v[172:173], v[188:189], v[184:185], v[164:165] op_sel_hi:[0,1,1] neg_lo:[0,0,1] neg_hi:[0,0,1]
	v_pk_fma_f32 v[174:175], v[188:189], v[186:187], v[166:167] op_sel_hi:[0,1,1] neg_lo:[0,0,1] neg_hi:[0,0,1]
	v_cvt_pk_bf16_f32 v180, v172, v173
	v_cvt_pk_bf16_f32 v181, v174, v175
	v_add_u32_e32 v194, 0xf000, v190
	global_store_dwordx2 v194, v[180:181], s[28:29]
	s_waitcnt vmcnt(31)
	v_lshlrev_b32_e32 v164, 16, v162
	v_and_b32_e32 v165, 0xffff0000, v162
	v_lshlrev_b32_e32 v166, 16, v163
	v_and_b32_e32 v167, 0xffff0000, v163
	v_pk_add_f32 v[184:185], v[184:185], v[164:165]
	v_pk_add_f32 v[186:187], v[186:187], v[166:167]
	v_lshlrev_b32_e32 v168, 16, v154
	v_and_b32_e32 v169, 0xffff0000, v154
	v_lshlrev_b32_e32 v170, 16, v155
	v_and_b32_e32 v171, 0xffff0000, v155
	v_pk_add_f32 v[184:185], v[184:185], v[168:169] neg_lo:[0,1] neg_hi:[0,1]
	v_pk_add_f32 v[186:187], v[186:187], v[170:171] neg_lo:[0,1] neg_hi:[0,1]
	v_pk_fma_f32 v[172:173], v[188:189], v[184:185], v[164:165] op_sel_hi:[0,1,1] neg_lo:[0,0,1] neg_hi:[0,0,1]
	v_pk_fma_f32 v[174:175], v[188:189], v[186:187], v[166:167] op_sel_hi:[0,1,1] neg_lo:[0,0,1] neg_hi:[0,0,1]
	v_cvt_pk_bf16_f32 v182, v172, v173
	v_cvt_pk_bf16_f32 v183, v174, v175
	global_store_dwordx2 v194, v[182:183], s[28:29] offset:2048
	s_branch .LBB0_861
; #define GAS __attribute__((address_space(1)))
; __device__ __forceinline__ unsigned pk2(float lo, float hi) { const f32x2 v = {lo, hi}; return __builtin_bit_cast(unsigned, __builtin_convertvector(v, b16x2)); }
; template <int W>
; __device__ __forceinline__ void pool_item(const bf16* U, bf16* Z, int b, int t0, int g, int lane) {
;     const size_t base = (size_t)b * SEQ * D + 256 * g + 4 * lane;
;     float s[4] = {0.f, 0.f, 0.f, 0.f};
; #pragma unroll
;     for (int j = 1; j <= W; ++j) { const int t = t0 - j; if (t >= 0) { const u32x2 v = *(const GAS u32x2*)(U + base + (size_t)t * D);
;             s[0] += bf2f(v.x & 0xffffu); s[1] += bf2f(v.x >> 16); s[2] += bf2f(v.y & 0xffffu); s[3] += bf2f(v.y >> 16); } }
; #pragma unroll 8
;     for (int i = 0; i < 32; ++i) { const int t = t0 + i;
;         const u32x2 v = *(const GAS u32x2*)(U + base + (size_t)t * D);
;         const float c0 = bf2f(v.x & 0xffffu), c1 = bf2f(v.x >> 16), c2 = bf2f(v.y & 0xffffu), c3 = bf2f(v.y >> 16);
;         s[0] += c0; s[1] += c1; s[2] += c2; s[3] += c3;
;         if (t - W >= 0) { const u32x2 o = *(const GAS u32x2*)(U + base + (size_t)(t - W) * D);
;             s[0] -= bf2f(o.x & 0xffffu); s[1] -= bf2f(o.x >> 16); s[2] -= bf2f(o.y & 0xffffu); s[3] -= bf2f(o.y >> 16); }
;         const float inv = 1.0f / (float)((t + 1) < W ? (t + 1) : W);
;         u32x2 w; w.x = pk2(s[0] * inv - c0, s[1] * inv - c1); w.y = pk2(s[2] * inv - c2, s[3] * inv - c3);
;         *(GAS u32x2*)(Z + base + (size_t)t * D) = w; }
.Lpool0_w2:
	v_add_u32_e32 v192, 0x8000, v190
	global_load_dwordx2 v[100:101], v192, s[10:11]
	global_load_dwordx2 v[102:103], v192, s[10:11] offset:2048
	v_add_u32_e32 v191, 0x9000, v190
	global_load_dwordx2 v[104:105], v191, s[10:11]
	global_load_dwordx2 v[106:107], v191, s[10:11] offset:2048
	v_add_u32_e32 v192, 0xa000, v190
	global_load_dwordx2 v[108:109], v192, s[10:11]
	global_load_dwordx2 v[110:111], v192, s[10:11] offset:2048
	v_add_u32_e32 v191, 0xb000, v190
	global_load_dwordx2 v[112:113], v191, s[10:11]
	global_load_dwordx2 v[114:115], v191, s[10:11] offset:2048
	v_add_u32_e32 v192, 0xc000, v190
	global_load_dwordx2 v[116:117], v192, s[10:11]
	global_load_dwordx2 v[118:119], v192, s[10:11] offset:2048
	v_add_u32_e32 v191, 0xd000, v190
	global_load_dwordx2 v[120:121], v191, s[10:11]
	global_load_dwordx2 v[122:123], v191, s[10:11] offset:2048
	v_add_u32_e32 v192, 0xe000, v190
	global_load_dwordx2 v[124:125], v192, s[10:11]
	global_load_dwordx2 v[126:127], v192, s[10:11] offset:2048
	v_add_u32_e32 v191, 0xf000, v190
	global_load_dwordx2 v[128:129], v191, s[10:11]
	global_load_dwordx2 v[130:131], v191, s[10:11] offset:2048
	v_add_u32_e32 v192, 0x10000, v190
	global_load_dwordx2 v[132:133], v192, s[10:11]
	global_load_dwordx2 v[134:135], v192, s[10:11] offset:2048
	v_add_u32_e32 v191, 0x11000, v190
	global_load_dwordx2 v[136:137], v191, s[10:11]
	global_load_dwordx2 v[138:139], v191, s[10:11] offset:2048
	v_add_u32_e32 v192, 0x12000, v190
	global_load_dwordx2 v[140:141], v192, s[10:11]
	global_load_dwordx2 v[142:143], v192, s[10:11] offset:2048
	v_add_u32_e32 v191, 0x13000, v190
	global_load_dwordx2 v[144:145], v191, s[10:11]
	global_load_dwordx2 v[146:147], v191, s[10:11] offset:2048
	v_add_u32_e32 v192, 0x14000, v190
	global_load_dwordx2 v[148:149], v192, s[10:11]
	global_load_dwordx2 v[150:151], v192, s[10:11] offset:2048
	v_add_u32_e32 v191, 0x15000, v190
	global_load_dwordx2 v[152:153], v191, s[10:11]
	global_load_dwordx2 v[154:155], v191, s[10:11] offset:2048
	v_add_u32_e32 v192, 0x16000, v190
	global_load_dwordx2 v[156:157], v192, s[10:11]
	global_load_dwordx2 v[158:159], v192, s[10:11] offset:2048
	v_add_u32_e32 v191, 0x17000, v190
	global_load_dwordx2 v[160:161], v191, s[10:11]
	global_load_dwordx2 v[162:163], v191, s[10:11] offset:2048
	v_mov_b32_e32 v184, 0
	v_mov_b32_e32 v185, 0
	v_mov_b32_e32 v186, 0
	v_mov_b32_e32 v187, 0
	v_mov_b32_e32 v188, 0x3f800000
	s_waitcnt vmcnt(31)
	v_lshlrev_b32_e32 v164, 16, v100
	v_and_b32_e32 v165, 0xffff0000, v100
	v_lshlrev_b32_e32 v166, 16, v101
	v_and_b32_e32 v167, 0xffff0000, v101
	v_pk_add_f32 v[184:185], v[184:185], v[164:165]
	v_pk_add_f32 v[186:187], v[186:187], v[166:167]
	v_pk_fma_f32 v[172:173], v[188:189], v[184:185], v[164:165] op_sel_hi:[0,1,1] neg_lo:[0,0,1] neg_hi:[0,0,1]
	v_pk_fma_f32 v[174:175], v[188:189], v[186:187], v[166:167] op_sel_hi:[0,1,1] neg_lo:[0,0,1] neg_hi:[0,0,1]
	v_cvt_pk_bf16_f32 v176, v172, v173
	v_cvt_pk_bf16_f32 v177, v174, v175
	global_store_dwordx2 v190, v[176:177], s[28:29]
	v_mov_b32_e32 v188, 0x3f000000
	s_waitcnt vmcnt(31)
	v_lshlrev_b32_e32 v164, 16, v102
	v_and_b32_e32 v165, 0xffff0000, v102
	v_lshlrev_b32_e32 v166, 16, v103
	v_and_b32_e32 v167, 0xffff0000, v103
	v_pk_add_f32 v[184:185], v[184:185], v[164:165]
	v_pk_add_f32 v[186:187], v[186:187], v[166:167]
	v_pk_fma_f32 v[172:173], v[188:189], v[184:185], v[164:165] op_sel_hi:[0,1,1] neg_lo:[0,0,1] neg_hi:[0,0,1]
	v_pk_fma_f32 v[174:175], v[188:189], v[186:187], v[166:167] op_sel_hi:[0,1,1] neg_lo:[0,0,1] neg_hi:[0,0,1]
	v_cvt_pk_bf16_f32 v178, v172, v173
	v_cvt_pk_bf16_f32 v179, v174, v175
	global_store_dwordx2 v190, v[178:179], s[28:29] offset:2048
	s_waitcnt vmcnt(31)
	v_lshlrev_b32_e32 v164, 16, v104
	v_and_b32_e32 v165, 0xffff0000, v104
	v_lshlrev_b32_e32 v166, 16, v105
	v_and_b32_e32 v167, 0xffff0000, v105
	v_pk_add_f32 v[184:185], v[184:185], v[164:165]
	v_pk_add_f32 v[186:187], v[186:187], v[166:167]
	v_lshlrev_b32_e32 v168, 16, v100
	v_and_b32_e32 v169, 0xffff0000, v100
	v_lshlrev_b32_e32 v170, 16, v101
	v_and_b32_e32 v171, 0xffff0000, v101
	v_pk_add_f32 v[184:185], v[184:185], v[168:169] neg_lo:[0,1] neg_hi:[0,1]
	v_pk_add_f32 v[186:187], v[186:187], v[170:171] neg_lo:[0,1] neg_hi:[0,1]
	v_pk_fma_f32 v[172:173], v[188:189], v[184:185], v[164:165] op_sel_hi:[0,1,1] neg_lo:[0,0,1] neg_hi:[0,0,1]
	v_pk_fma_f32 v[174:175], v[188:189], v[186:187], v[166:167] op_sel_hi:[0,1,1] neg_lo:[0,0,1] neg_hi:[0,0,1]
	v_cvt_pk_bf16_f32 v180, v172, v173
	v_cvt_pk_bf16_f32 v181, v174, v175
	v_add_u32_e32 v194, 0x1000, v190
	global_store_dwordx2 v194, v[180:181], s[28:29]
	s_waitcnt vmcnt(31)
	v_lshlrev_b32_e32 v164, 16, v106
	v_and_b32_e32 v165, 0xffff0000, v106
	v_lshlrev_b32_e32 v166, 16, v107
	v_and_b32_e32 v167, 0xffff0000, v107
	v_pk_add_f32 v[184:185], v[184:185], v[164:165]
	v_pk_add_f32 v[186:187], v[186:187], v[166:167]
	v_lshlrev_b32_e32 v168, 16, v102
	v_and_b32_e32 v169, 0xffff0000, v102
	v_lshlrev_b32_e32 v170, 16, v103
	v_and_b32_e32 v171, 0xffff0000, v103
	v_pk_add_f32 v[184:185], v[184:185], v[168:169] neg_lo:[0,1] neg_hi:[0,1]
	v_pk_add_f32 v[186:187], v[186:187], v[170:171] neg_lo:[0,1] neg_hi:[0,1]
	v_pk_fma_f32 v[172:173], v[188:189], v[184:185], v[164:165] op_sel_hi:[0,1,1] neg_lo:[0,0,1] neg_hi:[0,0,1]
	v_pk_fma_f32 v[174:175], v[188:189], v[186:187], v[166:167] op_sel_hi:[0,1,1] neg_lo:[0,0,1] neg_hi:[0,0,1]
	v_cvt_pk_bf16_f32 v182, v172, v173
	v_cvt_pk_bf16_f32 v183, v174, v175
	global_store_dwordx2 v194, v[182:183], s[28:29] offset:2048
	s_waitcnt vmcnt(31)
; #define GAS __attribute__((address_space(1)))
; __device__ __forceinline__ unsigned pk2(float lo, float hi) { const f32x2 v = {lo, hi}; return __builtin_bit_cast(unsigned, __builtin_convertvector(v, b16x2)); }
; template <int W>
; __device__ __forceinline__ void pool_item(const bf16* U, bf16* Z, int b, int t0, int g, int lane) {
;     ...
; #pragma unroll 8
;     for (int i = 0; i < 32; ++i) { const int t = t0 + i;
;         const u32x2 v = *(const GAS u32x2*)(U + base + (size_t)t * D);
;         const float c0 = bf2f(v.x & 0xffffu), c1 = bf2f(v.x >> 16), c2 = bf2f(v.y & 0xffffu), c3 = bf2f(v.y >> 16);
;         s[0] += c0; s[1] += c1; s[2] += c2; s[3] += c3;
;         if (t - W >= 0) { const u32x2 o = *(const GAS u32x2*)(U + base + (size_t)(t - W) * D);
;             s[0] -= bf2f(o.x & 0xffffu); s[1] -= bf2f(o.x >> 16); s[2] -= bf2f(o.y & 0xffffu); s[3] -= bf2f(o.y >> 16); }
;         const float inv = 1.0f / (float)((t + 1) < W ? (t + 1) : W);
;         u32x2 w; w.x = pk2(s[0] * inv - c0, s[1] * inv - c1); w.y = pk2(s[2] * inv - c2, s[3] * inv - c3);
;         *(GAS u32x2*)(Z + base + (size_t)t * D) = w; }
	v_lshlrev_b32_e32 v164, 16, v108
	v_and_b32_e32 v165, 0xffff0000, v108
	v_lshlrev_b32_e32 v166, 16, v109
	v_and_b32_e32 v167, 0xffff0000, v109
	v_pk_add_f32 v[184:185], v[184:185], v[164:165]
	v_pk_add_f32 v[186:187], v[186:187], v[166:167]
	v_lshlrev_b32_e32 v168, 16, v104
	v_and_b32_e32 v169, 0xffff0000, v104
	v_lshlrev_b32_e32 v170, 16, v105
	v_and_b32_e32 v171, 0xffff0000, v105
	v_pk_add_f32 v[184:185], v[184:185], v[168:169] neg_lo:[0,1] neg_hi:[0,1]
	v_pk_add_f32 v[186:187], v[186:187], v[170:171] neg_lo:[0,1] neg_hi:[0,1]
	v_pk_fma_f32 v[172:173], v[188:189], v[184:185], v[164:165] op_sel_hi:[0,1,1] neg_lo:[0,0,1] neg_hi:[0,0,1]
	v_pk_fma_f32 v[174:175], v[188:189], v[186:187], v[166:167] op_sel_hi:[0,1,1] neg_lo:[0,0,1] neg_hi:[0,0,1]
	v_cvt_pk_bf16_f32 v176, v172, v173
	v_cvt_pk_bf16_f32 v177, v174, v175
	v_add_u32_e32 v193, 0x2000, v190
	global_store_dwordx2 v193, v[176:177], s[28:29]
	s_waitcnt vmcnt(31)
	v_lshlrev_b32_e32 v164, 16, v110
	v_and_b32_e32 v165, 0xffff0000, v110
	v_lshlrev_b32_e32 v166, 16, v111
	v_and_b32_e32 v167, 0xffff0000, v111
	v_pk_add_f32 v[184:185], v[184:185], v[164:165]
	v_pk_add_f32 v[186:187], v[186:187], v[166:167]
	v_lshlrev_b32_e32 v168, 16, v106
	v_and_b32_e32 v169, 0xffff0000, v106
	v_lshlrev_b32_e32 v170, 16, v107
	v_and_b32_e32 v171, 0xffff0000, v107
	v_pk_add_f32 v[184:185], v[184:185], v[168:169] neg_lo:[0,1] neg_hi:[0,1]
	v_pk_add_f32 v[186:187], v[186:187], v[170:171] neg_lo:[0,1] neg_hi:[0,1]
	v_pk_fma_f32 v[172:173], v[188:189], v[184:185], v[164:165] op_sel_hi:[0,1,1] neg_lo:[0,0,1] neg_hi:[0,0,1]
	v_pk_fma_f32 v[174:175], v[188:189], v[186:187], v[166:167] op_sel_hi:[0,1,1] neg_lo:[0,0,1] neg_hi:[0,0,1]
	v_cvt_pk_bf16_f32 v178, v172, v173
	v_cvt_pk_bf16_f32 v179, v174, v175
	global_store_dwordx2 v193, v[178:179], s[28:29] offset:2048
	s_waitcnt vmcnt(31)
	v_lshlrev_b32_e32 v164, 16, v112
	v_and_b32_e32 v165, 0xffff0000, v112
	v_lshlrev_b32_e32 v166, 16, v113
	v_and_b32_e32 v167, 0xffff0000, v113
	v_pk_add_f32 v[184:185], v[184:185], v[164:165]
	v_pk_add_f32 v[186:187], v[186:187], v[166:167]
	v_lshlrev_b32_e32 v168, 16, v108
	v_and_b32_e32 v169, 0xffff0000, v108
	v_lshlrev_b32_e32 v170, 16, v109
	v_and_b32_e32 v171, 0xffff0000, v109
	v_pk_add_f32 v[184:185], v[184:185], v[168:169] neg_lo:[0,1] neg_hi:[0,1]
	v_pk_add_f32 v[186:187], v[186:187], v[170:171] neg_lo:[0,1] neg_hi:[0,1]
	v_pk_fma_f32 v[172:173], v[188:189], v[184:185], v[164:165] op_sel_hi:[0,1,1] neg_lo:[0,0,1] neg_hi:[0,0,1]
	v_pk_fma_f32 v[174:175], v[188:189], v[186:187], v[166:167] op_sel_hi:[0,1,1] neg_lo:[0,0,1] neg_hi:[0,0,1]
	v_cvt_pk_bf16_f32 v180, v172, v173
	v_cvt_pk_bf16_f32 v181, v174, v175
	v_add_u32_e32 v194, 0x3000, v190
	global_store_dwordx2 v194, v[180:181], s[28:29]
	s_waitcnt vmcnt(31)
	v_lshlrev_b32_e32 v164, 16, v114
	v_and_b32_e32 v165, 0xffff0000, v114
	v_lshlrev_b32_e32 v166, 16, v115
	v_and_b32_e32 v167, 0xffff0000, v115
	v_pk_add_f32 v[184:185], v[184:185], v[164:165]
	v_pk_add_f32 v[186:187], v[186:187], v[166:167]
	v_lshlrev_b32_e32 v168, 16, v110
	v_and_b32_e32 v169, 0xffff0000, v110
	v_lshlrev_b32_e32 v170, 16, v111
	v_and_b32_e32 v171, 0xffff0000, v111
	v_pk_add_f32 v[184:185], v[184:185], v[168:169] neg_lo:[0,1] neg_hi:[0,1]
	v_pk_add_f32 v[186:187], v[186:187], v[170:171] neg_lo:[0,1] neg_hi:[0,1]
	v_pk_fma_f32 v[172:173], v[188:189], v[184:185], v[164:165] op_sel_hi:[0,1,1] neg_lo:[0,0,1] neg_hi:[0,0,1]
	v_pk_fma_f32 v[174:175], v[188:189], v[186:187], v[166:167] op_sel_hi:[0,1,1] neg_lo:[0,0,1] neg_hi:[0,0,1]
	v_cvt_pk_bf16_f32 v182, v172, v173
	v_cvt_pk_bf16_f32 v183, v174, v175
	global_store_dwordx2 v194, v[182:183], s[28:29] offset:2048
	s_waitcnt vmcnt(31)
	v_lshlrev_b32_e32 v164, 16, v116
	v_and_b32_e32 v165, 0xffff0000, v116
	v_lshlrev_b32_e32 v166, 16, v117
	v_and_b32_e32 v167, 0xffff0000, v117
	v_pk_add_f32 v[184:185], v[184:185], v[164:165]
	v_pk_add_f32 v[186:187], v[186:187], v[166:167]
	v_lshlrev_b32_e32 v168, 16, v112
	v_and_b32_e32 v169, 0xffff0000, v112
	v_lshlrev_b32_e32 v170, 16, v113
	v_and_b32_e32 v171, 0xffff0000, v113
	v_pk_add_f32 v[184:185], v[184:185], v[168:169] neg_lo:[0,1] neg_hi:[0,1]
	v_pk_add_f32 v[186:187], v[186:187], v[170:171] neg_lo:[0,1] neg_hi:[0,1]
	v_pk_fma_f32 v[172:173], v[188:189], v[184:185], v[164:165] op_sel_hi:[0,1,1] neg_lo:[0,0,1] neg_hi:[0,0,1]
	v_pk_fma_f32 v[174:175], v[188:189], v[186:187], v[166:167] op_sel_hi:[0,1,1] neg_lo:[0,0,1] neg_hi:[0,0,1]
	v_cvt_pk_bf16_f32 v176, v172, v173
	v_cvt_pk_bf16_f32 v177, v174, v175
	v_add_u32_e32 v193, 0x4000, v190
	global_store_dwordx2 v193, v[176:177], s[28:29]
	s_waitcnt vmcnt(31)
	v_lshlrev_b32_e32 v164, 16, v118
	v_and_b32_e32 v165, 0xffff0000, v118
	v_lshlrev_b32_e32 v166, 16, v119
	v_and_b32_e32 v167, 0xffff0000, v119
	v_pk_add_f32 v[184:185], v[184:185], v[164:165]
	v_pk_add_f32 v[186:187], v[186:187], v[166:167]
	v_lshlrev_b32_e32 v168, 16, v114
	v_and_b32_e32 v169, 0xffff0000, v114
	v_lshlrev_b32_e32 v170, 16, v115
	v_and_b32_e32 v171, 0xffff0000, v115
	v_pk_add_f32 v[184:185], v[184:185], v[168:169] neg_lo:[0,1] neg_hi:[0,1]
	v_pk_add_f32 v[186:187], v[186:187], v[170:171] neg_lo:[0,1] neg_hi:[0,1]
	v_pk_fma_f32 v[172:173], v[188:189], v[184:185], v[164:165] op_sel_hi:[0,1,1] neg_lo:[0,0,1] neg_hi:[0,0,1]
	v_pk_fma_f32 v[174:175], v[188:189], v[186:187], v[166:167] op_sel_hi:[0,1,1] neg_lo:[0,0,1] neg_hi:[0,0,1]
	v_cvt_pk_bf16_f32 v178, v172, v173
	v_cvt_pk_bf16_f32 v179, v174, v175
	global_store_dwordx2 v193, v[178:179], s[28:29] offset:2048
	s_waitcnt vmcnt(31)
; #define GAS __attribute__((address_space(1)))
; __device__ __forceinline__ unsigned pk2(float lo, float hi) { const f32x2 v = {lo, hi}; return __builtin_bit_cast(unsigned, __builtin_convertvector(v, b16x2)); }
; template <int W>
; __device__ __forceinline__ void pool_item(const bf16* U, bf16* Z, int b, int t0, int g, int lane) {
;     ...
;     for (int i = 0; i < 32; ++i) { const int t = t0 + i;
;         const u32x2 v = *(const GAS u32x2*)(U + base + (size_t)t * D);
;         const float c0 = bf2f(v.x & 0xffffu), c1 = bf2f(v.x >> 16), c2 = bf2f(v.y & 0xffffu), c3 = bf2f(v.y >> 16);
;         s[0] += c0; s[1] += c1; s[2] += c2; s[3] += c3;
;         if (t - W >= 0) { const u32x2 o = *(const GAS u32x2*)(U + base + (size_t)(t - W) * D);
;             s[0] -= bf2f(o.x & 0xffffu); s[1] -= bf2f(o.x >> 16); s[2] -= bf2f(o.y & 0xffffu); s[3] -= bf2f(o.y >> 16); }
;         const float inv = 1.0f / (float)((t + 1) < W ? (t + 1) : W);
;         u32x2 w; w.x = pk2(s[0] * inv - c0, s[1] * inv - c1); w.y = pk2(s[2] * inv - c2, s[3] * inv - c3);
;         *(GAS u32x2*)(Z + base + (size_t)t * D) = w; }
	v_lshlrev_b32_e32 v164, 16, v120
	v_and_b32_e32 v165, 0xffff0000, v120
	v_lshlrev_b32_e32 v166, 16, v121
	v_and_b32_e32 v167, 0xffff0000, v121
	v_pk_add_f32 v[184:185], v[184:185], v[164:165]
	v_pk_add_f32 v[186:187], v[186:187], v[166:167]
	v_lshlrev_b32_e32 v168, 16, v116
	v_and_b32_e32 v169, 0xffff0000, v116
	v_lshlrev_b32_e32 v170, 16, v117
	v_and_b32_e32 v171, 0xffff0000, v117
	v_pk_add_f32 v[184:185], v[184:185], v[168:169] neg_lo:[0,1] neg_hi:[0,1]
	v_pk_add_f32 v[186:187], v[186:187], v[170:171] neg_lo:[0,1] neg_hi:[0,1]
	v_pk_fma_f32 v[172:173], v[188:189], v[184:185], v[164:165] op_sel_hi:[0,1,1] neg_lo:[0,0,1] neg_hi:[0,0,1]
	v_pk_fma_f32 v[174:175], v[188:189], v[186:187], v[166:167] op_sel_hi:[0,1,1] neg_lo:[0,0,1] neg_hi:[0,0,1]
	v_cvt_pk_bf16_f32 v180, v172, v173
	v_cvt_pk_bf16_f32 v181, v174, v175
	v_add_u32_e32 v194, 0x5000, v190
	global_store_dwordx2 v194, v[180:181], s[28:29]
	s_waitcnt vmcnt(31)
	v_lshlrev_b32_e32 v164, 16, v122
	v_and_b32_e32 v165, 0xffff0000, v122
	v_lshlrev_b32_e32 v166, 16, v123
	v_and_b32_e32 v167, 0xffff0000, v123
	v_pk_add_f32 v[184:185], v[184:185], v[164:165]
	v_pk_add_f32 v[186:187], v[186:187], v[166:167]
	v_lshlrev_b32_e32 v168, 16, v118
	v_and_b32_e32 v169, 0xffff0000, v118
	v_lshlrev_b32_e32 v170, 16, v119
	v_and_b32_e32 v171, 0xffff0000, v119
	v_pk_add_f32 v[184:185], v[184:185], v[168:169] neg_lo:[0,1] neg_hi:[0,1]
	v_pk_add_f32 v[186:187], v[186:187], v[170:171] neg_lo:[0,1] neg_hi:[0,1]
	v_pk_fma_f32 v[172:173], v[188:189], v[184:185], v[164:165] op_sel_hi:[0,1,1] neg_lo:[0,0,1] neg_hi:[0,0,1]
	v_pk_fma_f32 v[174:175], v[188:189], v[186:187], v[166:167] op_sel_hi:[0,1,1] neg_lo:[0,0,1] neg_hi:[0,0,1]
	v_cvt_pk_bf16_f32 v182, v172, v173
	v_cvt_pk_bf16_f32 v183, v174, v175
	global_store_dwordx2 v194, v[182:183], s[28:29] offset:2048
	s_waitcnt vmcnt(31)
	v_lshlrev_b32_e32 v164, 16, v124
	v_and_b32_e32 v165, 0xffff0000, v124
	v_lshlrev_b32_e32 v166, 16, v125
	v_and_b32_e32 v167, 0xffff0000, v125
	v_pk_add_f32 v[184:185], v[184:185], v[164:165]
	v_pk_add_f32 v[186:187], v[186:187], v[166:167]
	v_lshlrev_b32_e32 v168, 16, v120
	v_and_b32_e32 v169, 0xffff0000, v120
	v_lshlrev_b32_e32 v170, 16, v121
	v_and_b32_e32 v171, 0xffff0000, v121
	v_pk_add_f32 v[184:185], v[184:185], v[168:169] neg_lo:[0,1] neg_hi:[0,1]
	v_pk_add_f32 v[186:187], v[186:187], v[170:171] neg_lo:[0,1] neg_hi:[0,1]
	v_pk_fma_f32 v[172:173], v[188:189], v[184:185], v[164:165] op_sel_hi:[0,1,1] neg_lo:[0,0,1] neg_hi:[0,0,1]
	v_pk_fma_f32 v[174:175], v[188:189], v[186:187], v[166:167] op_sel_hi:[0,1,1] neg_lo:[0,0,1] neg_hi:[0,0,1]
	v_cvt_pk_bf16_f32 v176, v172, v173
	v_cvt_pk_bf16_f32 v177, v174, v175
	v_add_u32_e32 v193, 0x6000, v190
	global_store_dwordx2 v193, v[176:177], s[28:29]
	s_waitcnt vmcnt(31)
	v_lshlrev_b32_e32 v164, 16, v126
	v_and_b32_e32 v165, 0xffff0000, v126
	v_lshlrev_b32_e32 v166, 16, v127
	v_and_b32_e32 v167, 0xffff0000, v127
	v_pk_add_f32 v[184:185], v[184:185], v[164:165]
	v_pk_add_f32 v[186:187], v[186:187], v[166:167]
	v_lshlrev_b32_e32 v168, 16, v122
	v_and_b32_e32 v169, 0xffff0000, v122
	v_lshlrev_b32_e32 v170, 16, v123
	v_and_b32_e32 v171, 0xffff0000, v123
	v_pk_add_f32 v[184:185], v[184:185], v[168:169] neg_lo:[0,1] neg_hi:[0,1]
	v_pk_add_f32 v[186:187], v[186:187], v[170:171] neg_lo:[0,1] neg_hi:[0,1]
	v_pk_fma_f32 v[172:173], v[188:189], v[184:185], v[164:165] op_sel_hi:[0,1,1] neg_lo:[0,0,1] neg_hi:[0,0,1]
	v_pk_fma_f32 v[174:175], v[188:189], v[186:187], v[166:167] op_sel_hi:[0,1,1] neg_lo:[0,0,1] neg_hi:[0,0,1]
	v_cvt_pk_bf16_f32 v178, v172, v173
	v_cvt_pk_bf16_f32 v179, v174, v175
	global_store_dwordx2 v193, v[178:179], s[28:29] offset:2048
	s_waitcnt vmcnt(31)
	v_lshlrev_b32_e32 v164, 16, v128
	v_and_b32_e32 v165, 0xffff0000, v128
	v_lshlrev_b32_e32 v166, 16, v129
	v_and_b32_e32 v167, 0xffff0000, v129
	v_pk_add_f32 v[184:185], v[184:185], v[164:165]
	v_pk_add_f32 v[186:187], v[186:187], v[166:167]
	v_lshlrev_b32_e32 v168, 16, v124
	v_and_b32_e32 v169, 0xffff0000, v124
	v_lshlrev_b32_e32 v170, 16, v125
	v_and_b32_e32 v171, 0xffff0000, v125
	v_pk_add_f32 v[184:185], v[184:185], v[168:169] neg_lo:[0,1] neg_hi:[0,1]
	v_pk_add_f32 v[186:187], v[186:187], v[170:171] neg_lo:[0,1] neg_hi:[0,1]
	v_pk_fma_f32 v[172:173], v[188:189], v[184:185], v[164:165] op_sel_hi:[0,1,1] neg_lo:[0,0,1] neg_hi:[0,0,1]
	v_pk_fma_f32 v[174:175], v[188:189], v[186:187], v[166:167] op_sel_hi:[0,1,1] neg_lo:[0,0,1] neg_hi:[0,0,1]
	v_cvt_pk_bf16_f32 v180, v172, v173
	v_cvt_pk_bf16_f32 v181, v174, v175
	v_add_u32_e32 v194, 0x7000, v190
	global_store_dwordx2 v194, v[180:181], s[28:29]
	s_waitcnt vmcnt(31)
	v_lshlrev_b32_e32 v164, 16, v130
	v_and_b32_e32 v165, 0xffff0000, v130
	v_lshlrev_b32_e32 v166, 16, v131
	v_and_b32_e32 v167, 0xffff0000, v131
	v_pk_add_f32 v[184:185], v[184:185], v[164:165]
	v_pk_add_f32 v[186:187], v[186:187], v[166:167]
	v_lshlrev_b32_e32 v168, 16, v126
	v_and_b32_e32 v169, 0xffff0000, v126
	v_lshlrev_b32_e32 v170, 16, v127
	v_and_b32_e32 v171, 0xffff0000, v127
	v_pk_add_f32 v[184:185], v[184:185], v[168:169] neg_lo:[0,1] neg_hi:[0,1]
	v_pk_add_f32 v[186:187], v[186:187], v[170:171] neg_lo:[0,1] neg_hi:[0,1]
	v_pk_fma_f32 v[172:173], v[188:189], v[184:185], v[164:165] op_sel_hi:[0,1,1] neg_lo:[0,0,1] neg_hi:[0,0,1]
	v_pk_fma_f32 v[174:175], v[188:189], v[186:187], v[166:167] op_sel_hi:[0,1,1] neg_lo:[0,0,1] neg_hi:[0,0,1]
	v_cvt_pk_bf16_f32 v182, v172, v173
	v_cvt_pk_bf16_f32 v183, v174, v175
	global_store_dwordx2 v194, v[182:183], s[28:29] offset:2048
	s_waitcnt vmcnt(31)
; #define GAS __attribute__((address_space(1)))
; __device__ __forceinline__ unsigned pk2(float lo, float hi) { const f32x2 v = {lo, hi}; return __builtin_bit_cast(unsigned, __builtin_convertvector(v, b16x2)); }
; template <int W>
; __device__ __forceinline__ void pool_item(const bf16* U, bf16* Z, int b, int t0, int g, int lane) {
;     ...
;     for (int i = 0; i < 32; ++i) { const int t = t0 + i;
;         const u32x2 v = *(const GAS u32x2*)(U + base + (size_t)t * D);
;         const float c0 = bf2f(v.x & 0xffffu), c1 = bf2f(v.x >> 16), c2 = bf2f(v.y & 0xffffu), c3 = bf2f(v.y >> 16);
;         s[0] += c0; s[1] += c1; s[2] += c2; s[3] += c3;
;         if (t - W >= 0) { const u32x2 o = *(const GAS u32x2*)(U + base + (size_t)(t - W) * D);
;             s[0] -= bf2f(o.x & 0xffffu); s[1] -= bf2f(o.x >> 16); s[2] -= bf2f(o.y & 0xffffu); s[3] -= bf2f(o.y >> 16); }
;         const float inv = 1.0f / (float)((t + 1) < W ? (t + 1) : W);
;         u32x2 w; w.x = pk2(s[0] * inv - c0, s[1] * inv - c1); w.y = pk2(s[2] * inv - c2, s[3] * inv - c3);
;         *(GAS u32x2*)(Z + base + (size_t)t * D) = w; }
	v_lshlrev_b32_e32 v164, 16, v132
	v_and_b32_e32 v165, 0xffff0000, v132
	v_lshlrev_b32_e32 v166, 16, v133
	v_and_b32_e32 v167, 0xffff0000, v133
	v_pk_add_f32 v[184:185], v[184:185], v[164:165]
	v_pk_add_f32 v[186:187], v[186:187], v[166:167]
	v_lshlrev_b32_e32 v168, 16, v128
	v_and_b32_e32 v169, 0xffff0000, v128
	v_lshlrev_b32_e32 v170, 16, v129
	v_and_b32_e32 v171, 0xffff0000, v129
	v_pk_add_f32 v[184:185], v[184:185], v[168:169] neg_lo:[0,1] neg_hi:[0,1]
	v_pk_add_f32 v[186:187], v[186:187], v[170:171] neg_lo:[0,1] neg_hi:[0,1]
	v_pk_fma_f32 v[172:173], v[188:189], v[184:185], v[164:165] op_sel_hi:[0,1,1] neg_lo:[0,0,1] neg_hi:[0,0,1]
	v_pk_fma_f32 v[174:175], v[188:189], v[186:187], v[166:167] op_sel_hi:[0,1,1] neg_lo:[0,0,1] neg_hi:[0,0,1]
	v_cvt_pk_bf16_f32 v176, v172, v173
	v_cvt_pk_bf16_f32 v177, v174, v175
	v_add_u32_e32 v193, 0x8000, v190
	global_store_dwordx2 v193, v[176:177], s[28:29]
	s_waitcnt vmcnt(31)
	v_lshlrev_b32_e32 v164, 16, v134
	v_and_b32_e32 v165, 0xffff0000, v134
	v_lshlrev_b32_e32 v166, 16, v135
	v_and_b32_e32 v167, 0xffff0000, v135
	v_pk_add_f32 v[184:185], v[184:185], v[164:165]
	v_pk_add_f32 v[186:187], v[186:187], v[166:167]
	v_lshlrev_b32_e32 v168, 16, v130
	v_and_b32_e32 v169, 0xffff0000, v130
	v_lshlrev_b32_e32 v170, 16, v131
	v_and_b32_e32 v171, 0xffff0000, v131
	v_pk_add_f32 v[184:185], v[184:185], v[168:169] neg_lo:[0,1] neg_hi:[0,1]
	v_pk_add_f32 v[186:187], v[186:187], v[170:171] neg_lo:[0,1] neg_hi:[0,1]
	v_pk_fma_f32 v[172:173], v[188:189], v[184:185], v[164:165] op_sel_hi:[0,1,1] neg_lo:[0,0,1] neg_hi:[0,0,1]
	v_pk_fma_f32 v[174:175], v[188:189], v[186:187], v[166:167] op_sel_hi:[0,1,1] neg_lo:[0,0,1] neg_hi:[0,0,1]
	v_cvt_pk_bf16_f32 v178, v172, v173
	v_cvt_pk_bf16_f32 v179, v174, v175
	global_store_dwordx2 v193, v[178:179], s[28:29] offset:2048
	s_waitcnt vmcnt(31)
	v_lshlrev_b32_e32 v164, 16, v136
	v_and_b32_e32 v165, 0xffff0000, v136
	v_lshlrev_b32_e32 v166, 16, v137
	v_and_b32_e32 v167, 0xffff0000, v137
	v_pk_add_f32 v[184:185], v[184:185], v[164:165]
	v_pk_add_f32 v[186:187], v[186:187], v[166:167]
	v_lshlrev_b32_e32 v168, 16, v132
	v_and_b32_e32 v169, 0xffff0000, v132
	v_lshlrev_b32_e32 v170, 16, v133
	v_and_b32_e32 v171, 0xffff0000, v133
	v_pk_add_f32 v[184:185], v[184:185], v[168:169] neg_lo:[0,1] neg_hi:[0,1]
	v_pk_add_f32 v[186:187], v[186:187], v[170:171] neg_lo:[0,1] neg_hi:[0,1]
	v_pk_fma_f32 v[172:173], v[188:189], v[184:185], v[164:165] op_sel_hi:[0,1,1] neg_lo:[0,0,1] neg_hi:[0,0,1]
	v_pk_fma_f32 v[174:175], v[188:189], v[186:187], v[166:167] op_sel_hi:[0,1,1] neg_lo:[0,0,1] neg_hi:[0,0,1]
	v_cvt_pk_bf16_f32 v180, v172, v173
	v_cvt_pk_bf16_f32 v181, v174, v175
	v_add_u32_e32 v194, 0x9000, v190
	global_store_dwordx2 v194, v[180:181], s[28:29]
	s_waitcnt vmcnt(31)
	v_lshlrev_b32_e32 v164, 16, v138
	v_and_b32_e32 v165, 0xffff0000, v138
	v_lshlrev_b32_e32 v166, 16, v139
	v_and_b32_e32 v167, 0xffff0000, v139
	v_pk_add_f32 v[184:185], v[184:185], v[164:165]
	v_pk_add_f32 v[186:187], v[186:187], v[166:167]
	v_lshlrev_b32_e32 v168, 16, v134
	v_and_b32_e32 v169, 0xffff0000, v134
	v_lshlrev_b32_e32 v170, 16, v135
	v_and_b32_e32 v171, 0xffff0000, v135
	v_pk_add_f32 v[184:185], v[184:185], v[168:169] neg_lo:[0,1] neg_hi:[0,1]
	v_pk_add_f32 v[186:187], v[186:187], v[170:171] neg_lo:[0,1] neg_hi:[0,1]
	v_pk_fma_f32 v[172:173], v[188:189], v[184:185], v[164:165] op_sel_hi:[0,1,1] neg_lo:[0,0,1] neg_hi:[0,0,1]
	v_pk_fma_f32 v[174:175], v[188:189], v[186:187], v[166:167] op_sel_hi:[0,1,1] neg_lo:[0,0,1] neg_hi:[0,0,1]
	v_cvt_pk_bf16_f32 v182, v172, v173
	v_cvt_pk_bf16_f32 v183, v174, v175
	global_store_dwordx2 v194, v[182:183], s[28:29] offset:2048
	s_waitcnt vmcnt(31)
	v_lshlrev_b32_e32 v164, 16, v140
	v_and_b32_e32 v165, 0xffff0000, v140
	v_lshlrev_b32_e32 v166, 16, v141
	v_and_b32_e32 v167, 0xffff0000, v141
	v_pk_add_f32 v[184:185], v[184:185], v[164:165]
	v_pk_add_f32 v[186:187], v[186:187], v[166:167]
	v_lshlrev_b32_e32 v168, 16, v136
	v_and_b32_e32 v169, 0xffff0000, v136
	v_lshlrev_b32_e32 v170, 16, v137
	v_and_b32_e32 v171, 0xffff0000, v137
	v_pk_add_f32 v[184:185], v[184:185], v[168:169] neg_lo:[0,1] neg_hi:[0,1]
	v_pk_add_f32 v[186:187], v[186:187], v[170:171] neg_lo:[0,1] neg_hi:[0,1]
	v_pk_fma_f32 v[172:173], v[188:189], v[184:185], v[164:165] op_sel_hi:[0,1,1] neg_lo:[0,0,1] neg_hi:[0,0,1]
	v_pk_fma_f32 v[174:175], v[188:189], v[186:187], v[166:167] op_sel_hi:[0,1,1] neg_lo:[0,0,1] neg_hi:[0,0,1]
	v_cvt_pk_bf16_f32 v176, v172, v173
	v_cvt_pk_bf16_f32 v177, v174, v175
	v_add_u32_e32 v193, 0xa000, v190
	global_store_dwordx2 v193, v[176:177], s[28:29]
	s_waitcnt vmcnt(31)
	v_lshlrev_b32_e32 v164, 16, v142
	v_and_b32_e32 v165, 0xffff0000, v142
	v_lshlrev_b32_e32 v166, 16, v143
	v_and_b32_e32 v167, 0xffff0000, v143
	v_pk_add_f32 v[184:185], v[184:185], v[164:165]
	v_pk_add_f32 v[186:187], v[186:187], v[166:167]
	v_lshlrev_b32_e32 v168, 16, v138
	v_and_b32_e32 v169, 0xffff0000, v138
	v_lshlrev_b32_e32 v170, 16, v139
	v_and_b32_e32 v171, 0xffff0000, v139
	v_pk_add_f32 v[184:185], v[184:185], v[168:169] neg_lo:[0,1] neg_hi:[0,1]
	v_pk_add_f32 v[186:187], v[186:187], v[170:171] neg_lo:[0,1] neg_hi:[0,1]
	v_pk_fma_f32 v[172:173], v[188:189], v[184:185], v[164:165] op_sel_hi:[0,1,1] neg_lo:[0,0,1] neg_hi:[0,0,1]
	v_pk_fma_f32 v[174:175], v[188:189], v[186:187], v[166:167] op_sel_hi:[0,1,1] neg_lo:[0,0,1] neg_hi:[0,0,1]
	v_cvt_pk_bf16_f32 v178, v172, v173
	v_cvt_pk_bf16_f32 v179, v174, v175
	global_store_dwordx2 v193, v[178:179], s[28:29] offset:2048
	s_waitcnt vmcnt(31)
; #define GAS __attribute__((address_space(1)))
; __device__ __forceinline__ unsigned pk2(float lo, float hi) { const f32x2 v = {lo, hi}; return __builtin_bit_cast(unsigned, __builtin_convertvector(v, b16x2)); }
; template <int W>
; __device__ __forceinline__ void pool_item(const bf16* U, bf16* Z, int b, int t0, int g, int lane) {
;     ...
;     for (int i = 0; i < 32; ++i) { const int t = t0 + i;
;         const u32x2 v = *(const GAS u32x2*)(U + base + (size_t)t * D);
;         const float c0 = bf2f(v.x & 0xffffu), c1 = bf2f(v.x >> 16), c2 = bf2f(v.y & 0xffffu), c3 = bf2f(v.y >> 16);
;         s[0] += c0; s[1] += c1; s[2] += c2; s[3] += c3;
;         if (t - W >= 0) { const u32x2 o = *(const GAS u32x2*)(U + base + (size_t)(t - W) * D);
;             s[0] -= bf2f(o.x & 0xffffu); s[1] -= bf2f(o.x >> 16); s[2] -= bf2f(o.y & 0xffffu); s[3] -= bf2f(o.y >> 16); }
;         const float inv = 1.0f / (float)((t + 1) < W ? (t + 1) : W);
;         u32x2 w; w.x = pk2(s[0] * inv - c0, s[1] * inv - c1); w.y = pk2(s[2] * inv - c2, s[3] * inv - c3);
;         *(GAS u32x2*)(Z + base + (size_t)t * D) = w; }
	v_lshlrev_b32_e32 v164, 16, v144
	v_and_b32_e32 v165, 0xffff0000, v144
	v_lshlrev_b32_e32 v166, 16, v145
	v_and_b32_e32 v167, 0xffff0000, v145
	v_pk_add_f32 v[184:185], v[184:185], v[164:165]
	v_pk_add_f32 v[186:187], v[186:187], v[166:167]
	v_lshlrev_b32_e32 v168, 16, v140
	v_and_b32_e32 v169, 0xffff0000, v140
	v_lshlrev_b32_e32 v170, 16, v141
	v_and_b32_e32 v171, 0xffff0000, v141
	v_pk_add_f32 v[184:185], v[184:185], v[168:169] neg_lo:[0,1] neg_hi:[0,1]
	v_pk_add_f32 v[186:187], v[186:187], v[170:171] neg_lo:[0,1] neg_hi:[0,1]
	v_pk_fma_f32 v[172:173], v[188:189], v[184:185], v[164:165] op_sel_hi:[0,1,1] neg_lo:[0,0,1] neg_hi:[0,0,1]
	v_pk_fma_f32 v[174:175], v[188:189], v[186:187], v[166:167] op_sel_hi:[0,1,1] neg_lo:[0,0,1] neg_hi:[0,0,1]
	v_cvt_pk_bf16_f32 v180, v172, v173
	v_cvt_pk_bf16_f32 v181, v174, v175
	v_add_u32_e32 v194, 0xb000, v190
	global_store_dwordx2 v194, v[180:181], s[28:29]
	s_waitcnt vmcnt(31)
	v_lshlrev_b32_e32 v164, 16, v146
	v_and_b32_e32 v165, 0xffff0000, v146
	v_lshlrev_b32_e32 v166, 16, v147
	v_and_b32_e32 v167, 0xffff0000, v147
	v_pk_add_f32 v[184:185], v[184:185], v[164:165]
	v_pk_add_f32 v[186:187], v[186:187], v[166:167]
	v_lshlrev_b32_e32 v168, 16, v142
	v_and_b32_e32 v169, 0xffff0000, v142
	v_lshlrev_b32_e32 v170, 16, v143
	v_and_b32_e32 v171, 0xffff0000, v143
	v_pk_add_f32 v[184:185], v[184:185], v[168:169] neg_lo:[0,1] neg_hi:[0,1]
	v_pk_add_f32 v[186:187], v[186:187], v[170:171] neg_lo:[0,1] neg_hi:[0,1]
	v_pk_fma_f32 v[172:173], v[188:189], v[184:185], v[164:165] op_sel_hi:[0,1,1] neg_lo:[0,0,1] neg_hi:[0,0,1]
	v_pk_fma_f32 v[174:175], v[188:189], v[186:187], v[166:167] op_sel_hi:[0,1,1] neg_lo:[0,0,1] neg_hi:[0,0,1]
	v_cvt_pk_bf16_f32 v182, v172, v173
	v_cvt_pk_bf16_f32 v183, v174, v175
	global_store_dwordx2 v194, v[182:183], s[28:29] offset:2048
	s_waitcnt vmcnt(31)
	v_lshlrev_b32_e32 v164, 16, v148
	v_and_b32_e32 v165, 0xffff0000, v148
	v_lshlrev_b32_e32 v166, 16, v149
	v_and_b32_e32 v167, 0xffff0000, v149
	v_pk_add_f32 v[184:185], v[184:185], v[164:165]
	v_pk_add_f32 v[186:187], v[186:187], v[166:167]
	v_lshlrev_b32_e32 v168, 16, v144
	v_and_b32_e32 v169, 0xffff0000, v144
	v_lshlrev_b32_e32 v170, 16, v145
	v_and_b32_e32 v171, 0xffff0000, v145
	v_pk_add_f32 v[184:185], v[184:185], v[168:169] neg_lo:[0,1] neg_hi:[0,1]
	v_pk_add_f32 v[186:187], v[186:187], v[170:171] neg_lo:[0,1] neg_hi:[0,1]
	v_pk_fma_f32 v[172:173], v[188:189], v[184:185], v[164:165] op_sel_hi:[0,1,1] neg_lo:[0,0,1] neg_hi:[0,0,1]
	v_pk_fma_f32 v[174:175], v[188:189], v[186:187], v[166:167] op_sel_hi:[0,1,1] neg_lo:[0,0,1] neg_hi:[0,0,1]
	v_cvt_pk_bf16_f32 v176, v172, v173
	v_cvt_pk_bf16_f32 v177, v174, v175
	v_add_u32_e32 v193, 0xc000, v190
	global_store_dwordx2 v193, v[176:177], s[28:29]
	s_waitcnt vmcnt(31)
	v_lshlrev_b32_e32 v164, 16, v150
	v_and_b32_e32 v165, 0xffff0000, v150
	v_lshlrev_b32_e32 v166, 16, v151
	v_and_b32_e32 v167, 0xffff0000, v151
	v_pk_add_f32 v[184:185], v[184:185], v[164:165]
	v_pk_add_f32 v[186:187], v[186:187], v[166:167]
	v_lshlrev_b32_e32 v168, 16, v146
	v_and_b32_e32 v169, 0xffff0000, v146
	v_lshlrev_b32_e32 v170, 16, v147
	v_and_b32_e32 v171, 0xffff0000, v147
	v_pk_add_f32 v[184:185], v[184:185], v[168:169] neg_lo:[0,1] neg_hi:[0,1]
	v_pk_add_f32 v[186:187], v[186:187], v[170:171] neg_lo:[0,1] neg_hi:[0,1]
	v_pk_fma_f32 v[172:173], v[188:189], v[184:185], v[164:165] op_sel_hi:[0,1,1] neg_lo:[0,0,1] neg_hi:[0,0,1]
	v_pk_fma_f32 v[174:175], v[188:189], v[186:187], v[166:167] op_sel_hi:[0,1,1] neg_lo:[0,0,1] neg_hi:[0,0,1]
	v_cvt_pk_bf16_f32 v178, v172, v173
	v_cvt_pk_bf16_f32 v179, v174, v175
	global_store_dwordx2 v193, v[178:179], s[28:29] offset:2048
	s_waitcnt vmcnt(31)
	v_lshlrev_b32_e32 v164, 16, v152
	v_and_b32_e32 v165, 0xffff0000, v152
	v_lshlrev_b32_e32 v166, 16, v153
	v_and_b32_e32 v167, 0xffff0000, v153
	v_pk_add_f32 v[184:185], v[184:185], v[164:165]
	v_pk_add_f32 v[186:187], v[186:187], v[166:167]
	v_lshlrev_b32_e32 v168, 16, v148
	v_and_b32_e32 v169, 0xffff0000, v148
	v_lshlrev_b32_e32 v170, 16, v149
	v_and_b32_e32 v171, 0xffff0000, v149
	v_pk_add_f32 v[184:185], v[184:185], v[168:169] neg_lo:[0,1] neg_hi:[0,1]
	v_pk_add_f32 v[186:187], v[186:187], v[170:171] neg_lo:[0,1] neg_hi:[0,1]
	v_pk_fma_f32 v[172:173], v[188:189], v[184:185], v[164:165] op_sel_hi:[0,1,1] neg_lo:[0,0,1] neg_hi:[0,0,1]
	v_pk_fma_f32 v[174:175], v[188:189], v[186:187], v[166:167] op_sel_hi:[0,1,1] neg_lo:[0,0,1] neg_hi:[0,0,1]
	v_cvt_pk_bf16_f32 v180, v172, v173
	v_cvt_pk_bf16_f32 v181, v174, v175
	v_add_u32_e32 v194, 0xd000, v190
	global_store_dwordx2 v194, v[180:181], s[28:29]
	s_waitcnt vmcnt(31)
; #define GAS __attribute__((address_space(1)))
; __device__ __forceinline__ unsigned pk2(float lo, float hi) { const f32x2 v = {lo, hi}; return __builtin_bit_cast(unsigned, __builtin_convertvector(v, b16x2)); }
; template <int W>
; __device__ __forceinline__ void pool_item(const bf16* U, bf16* Z, int b, int t0, int g, int lane) {
;     ...
; #pragma unroll
;     for (int j = 1; j <= W; ++j) { const int t = t0 - j; if (t >= 0) { const u32x2 v = *(const GAS u32x2*)(U + base + (size_t)t * D);
;             s[0] += bf2f(v.x & 0xffffu); s[1] += bf2f(v.x >> 16); s[2] += bf2f(v.y & 0xffffu); s[3] += bf2f(v.y >> 16); } }
;     ...
;     for (int i = 0; i < 32; ++i) { const int t = t0 + i;
;         const u32x2 v = *(const GAS u32x2*)(U + base + (size_t)t * D);
;         const float c0 = bf2f(v.x & 0xffffu), c1 = bf2f(v.x >> 16), c2 = bf2f(v.y & 0xffffu), c3 = bf2f(v.y >> 16);
;         s[0] += c0; s[1] += c1; s[2] += c2; s[3] += c3;
;         if (t - W >= 0) { const u32x2 o = *(const GAS u32x2*)(U + base + (size_t)(t - W) * D);
;             s[0] -= bf2f(o.x & 0xffffu); s[1] -= bf2f(o.x >> 16); s[2] -= bf2f(o.y & 0xffffu); s[3] -= bf2f(o.y >> 16); }
;         const float inv = 1.0f / (float)((t + 1) < W ? (t + 1) : W);
;         u32x2 w; w.x = pk2(s[0] * inv - c0, s[1] * inv - c1); w.y = pk2(s[2] * inv - c2, s[3] * inv - c3);
;         *(GAS u32x2*)(Z + base + (size_t)t * D) = w; }
	v_lshlrev_b32_e32 v164, 16, v154
	v_and_b32_e32 v165, 0xffff0000, v154
	v_lshlrev_b32_e32 v166, 16, v155
	v_and_b32_e32 v167, 0xffff0000, v155
	v_pk_add_f32 v[184:185], v[184:185], v[164:165]
	v_pk_add_f32 v[186:187], v[186:187], v[166:167]
	v_lshlrev_b32_e32 v168, 16, v150
	v_and_b32_e32 v169, 0xffff0000, v150
	v_lshlrev_b32_e32 v170, 16, v151
	v_and_b32_e32 v171, 0xffff0000, v151
	v_pk_add_f32 v[184:185], v[184:185], v[168:169] neg_lo:[0,1] neg_hi:[0,1]
	v_pk_add_f32 v[186:187], v[186:187], v[170:171] neg_lo:[0,1] neg_hi:[0,1]
	v_pk_fma_f32 v[172:173], v[188:189], v[184:185], v[164:165] op_sel_hi:[0,1,1] neg_lo:[0,0,1] neg_hi:[0,0,1]
	v_pk_fma_f32 v[174:175], v[188:189], v[186:187], v[166:167] op_sel_hi:[0,1,1] neg_lo:[0,0,1] neg_hi:[0,0,1]
	v_cvt_pk_bf16_f32 v182, v172, v173
	v_cvt_pk_bf16_f32 v183, v174, v175
	global_store_dwordx2 v194, v[182:183], s[28:29] offset:2048
	s_waitcnt vmcnt(31)
	v_lshlrev_b32_e32 v164, 16, v156
	v_and_b32_e32 v165, 0xffff0000, v156
	v_lshlrev_b32_e32 v166, 16, v157
	v_and_b32_e32 v167, 0xffff0000, v157
	v_pk_add_f32 v[184:185], v[184:185], v[164:165]
	v_pk_add_f32 v[186:187], v[186:187], v[166:167]
	v_lshlrev_b32_e32 v168, 16, v152
	v_and_b32_e32 v169, 0xffff0000, v152
	v_lshlrev_b32_e32 v170, 16, v153
	v_and_b32_e32 v171, 0xffff0000, v153
	v_pk_add_f32 v[184:185], v[184:185], v[168:169] neg_lo:[0,1] neg_hi:[0,1]
	v_pk_add_f32 v[186:187], v[186:187], v[170:171] neg_lo:[0,1] neg_hi:[0,1]
	v_pk_fma_f32 v[172:173], v[188:189], v[184:185], v[164:165] op_sel_hi:[0,1,1] neg_lo:[0,0,1] neg_hi:[0,0,1]
	v_pk_fma_f32 v[174:175], v[188:189], v[186:187], v[166:167] op_sel_hi:[0,1,1] neg_lo:[0,0,1] neg_hi:[0,0,1]
	v_cvt_pk_bf16_f32 v176, v172, v173
	v_cvt_pk_bf16_f32 v177, v174, v175
	v_add_u32_e32 v193, 0xe000, v190
	global_store_dwordx2 v193, v[176:177], s[28:29]
	s_waitcnt vmcnt(31)
	v_lshlrev_b32_e32 v164, 16, v158
	v_and_b32_e32 v165, 0xffff0000, v158
	v_lshlrev_b32_e32 v166, 16, v159
	v_and_b32_e32 v167, 0xffff0000, v159
	v_pk_add_f32 v[184:185], v[184:185], v[164:165]
	v_pk_add_f32 v[186:187], v[186:187], v[166:167]
	v_lshlrev_b32_e32 v168, 16, v154
	v_and_b32_e32 v169, 0xffff0000, v154
	v_lshlrev_b32_e32 v170, 16, v155
	v_and_b32_e32 v171, 0xffff0000, v155
	v_pk_add_f32 v[184:185], v[184:185], v[168:169] neg_lo:[0,1] neg_hi:[0,1]
	v_pk_add_f32 v[186:187], v[186:187], v[170:171] neg_lo:[0,1] neg_hi:[0,1]
	v_pk_fma_f32 v[172:173], v[188:189], v[184:185], v[164:165] op_sel_hi:[0,1,1] neg_lo:[0,0,1] neg_hi:[0,0,1]
	v_pk_fma_f32 v[174:175], v[188:189], v[186:187], v[166:167] op_sel_hi:[0,1,1] neg_lo:[0,0,1] neg_hi:[0,0,1]
	v_cvt_pk_bf16_f32 v178, v172, v173
	v_cvt_pk_bf16_f32 v179, v174, v175
	global_store_dwordx2 v193, v[178:179], s[28:29] offset:2048
	s_waitcnt vmcnt(31)
	v_lshlrev_b32_e32 v164, 16, v160
	v_and_b32_e32 v165, 0xffff0000, v160
	v_lshlrev_b32_e32 v166, 16, v161
	v_and_b32_e32 v167, 0xffff0000, v161
	v_pk_add_f32 v[184:185], v[184:185], v[164:165]
	v_pk_add_f32 v[186:187], v[186:187], v[166:167]
	v_lshlrev_b32_e32 v168, 16, v156
	v_and_b32_e32 v169, 0xffff0000, v156
	v_lshlrev_b32_e32 v170, 16, v157
	v_and_b32_e32 v171, 0xffff0000, v157
	v_pk_add_f32 v[184:185], v[184:185], v[168:169] neg_lo:[0,1] neg_hi:[0,1]
	v_pk_add_f32 v[186:187], v[186:187], v[170:171] neg_lo:[0,1] neg_hi:[0,1]
	v_pk_fma_f32 v[172:173], v[188:189], v[184:185], v[164:165] op_sel_hi:[0,1,1] neg_lo:[0,0,1] neg_hi:[0,0,1]
	v_pk_fma_f32 v[174:175], v[188:189], v[186:187], v[166:167] op_sel_hi:[0,1,1] neg_lo:[0,0,1] neg_hi:[0,0,1]
	v_cvt_pk_bf16_f32 v180, v172, v173
	v_cvt_pk_bf16_f32 v181, v174, v175
	v_add_u32_e32 v194, 0xf000, v190
	global_store_dwordx2 v194, v[180:181], s[28:29]
	s_waitcnt vmcnt(31)
	v_lshlrev_b32_e32 v164, 16, v162
	v_and_b32_e32 v165, 0xffff0000, v162
	v_lshlrev_b32_e32 v166, 16, v163
	v_and_b32_e32 v167, 0xffff0000, v163
	v_pk_add_f32 v[184:185], v[184:185], v[164:165]
	v_pk_add_f32 v[186:187], v[186:187], v[166:167]
	v_lshlrev_b32_e32 v168, 16, v158
	v_and_b32_e32 v169, 0xffff0000, v158
	v_lshlrev_b32_e32 v170, 16, v159
	v_and_b32_e32 v171, 0xffff0000, v159
	v_pk_add_f32 v[184:185], v[184:185], v[168:169] neg_lo:[0,1] neg_hi:[0,1]
	v_pk_add_f32 v[186:187], v[186:187], v[170:171] neg_lo:[0,1] neg_hi:[0,1]
	v_pk_fma_f32 v[172:173], v[188:189], v[184:185], v[164:165] op_sel_hi:[0,1,1] neg_lo:[0,0,1] neg_hi:[0,0,1]
	v_pk_fma_f32 v[174:175], v[188:189], v[186:187], v[166:167] op_sel_hi:[0,1,1] neg_lo:[0,0,1] neg_hi:[0,0,1]
	v_cvt_pk_bf16_f32 v182, v172, v173
	v_cvt_pk_bf16_f32 v183, v174, v175
	global_store_dwordx2 v194, v[182:183], s[28:29] offset:2048
	s_branch .LBB0_861
	s_cmp_lt_i32 s9, 1
	s_mov_b64 s[54:55], 0
	s_cbranch_scc1 .LBB0_882
	v_readlane_b32 s9, v255, 3
	s_cmp_gt_i32 s9, 1
	s_cbranch_scc0 .LBB0_911
	s_cmp_eq_u32 s9, 2
	s_mov_b64 s[54:55], -1
	s_cbranch_scc0 .LBB0_910
	v_mov_b32_e32 v19, s51
	v_or_b32_e32 v18, s50, v6
	s_andn2_b64 vcc, exec, s[40:41]
	s_cbranch_vccnz .LBB0_1013
	s_add_i32 s22, s46, -1
	s_lshl_b64 s[10:11], s[22:23], 11
	s_add_u32 s10, s44, s10
	s_addc_u32 s11, s45, s11
	v_lshl_add_u64 v[20:21], v[18:19], 1, s[10:11]
	global_load_dwordx2 v[20:21], v[20:21], off
	s_waitcnt vmcnt(0)
	v_and_b32_e32 v22, 0xffff0000, v20
	v_lshlrev_b32_e32 v23, 16, v20
	v_and_b32_e32 v20, 0xffff0000, v21
	v_lshlrev_b32_e32 v21, 16, v21
	v_pk_add_f32 v[22:23], v[22:23], 0 op_sel_hi:[1,0]
	v_pk_add_f32 v[24:25], v[20:21], 0 op_sel_hi:[1,0]
	s_cmp_lt_i32 s46, 2
	s_cbranch_scc1 .LBB0_876
